# accumulator clearing with 64-bit moves (half the instructions per unit); MFMA-to-VALU pads after fp8 K-loops trimmed to the required 12 states
# speedup vs baseline: 1.0231x; 1.0000x over previous
.LBB0_163:
	s_ashr_i32 s31, s30, 31
	s_lshl_b64 s[36:37], s[30:31], 19
	s_add_u32 s36, s44, s36
	s_addc_u32 s37, s45, s37
	s_and_b64 s[38:39], s[4:5], exec
	s_cselect_b32 s11, s37, s13
	s_cselect_b32 s31, s36, s12
	s_ashr_i32 s35, s34, 31
	s_lshl_b64 s[38:39], s[34:35], 19
	s_add_u32 s38, s46, s38
	s_addc_u32 s39, s47, s39
	s_and_b64 s[40:41], s[4:5], exec
	s_cselect_b32 s35, s39, s15
	s_cselect_b32 s64, s38, s14
	s_add_u32 s65, s14, 0x100
	v_mov_b32_e32 v6, 0
	s_addc_u32 s66, s15, 0
	s_mov_b32 s67, -2
	v_mov_b64_e32 v[2:3], 0
	v_mov_b64_e32 v[4:5], 0
	v_mov_b32_e32 v7, v6
	v_mov_b64_e32 v[8:9], 0
	v_mov_b64_e32 v[10:11], 0
	v_mov_b64_e32 v[12:13], 0
	v_mov_b64_e32 v[14:15], 0
	v_mov_b64_e32 v[16:17], 0
	v_mov_b64_e32 v[18:19], 0
	v_mov_b64_e32 v[20:21], 0
	v_mov_b64_e32 v[22:23], 0
	v_mov_b64_e32 v[24:25], 0
	v_mov_b64_e32 v[26:27], 0
	v_mov_b64_e32 v[28:29], 0
	v_mov_b64_e32 v[30:31], 0
	v_mov_b64_e32 v[32:33], 0
	v_mov_b64_e32 v[34:35], 0
	v_mov_b64_e32 v[36:37], 0
	v_mov_b64_e32 v[38:39], 0
	v_mov_b64_e32 v[40:41], 0
	v_mov_b64_e32 v[42:43], 0
	v_mov_b64_e32 v[44:45], 0
	v_mov_b64_e32 v[46:47], 0
	v_mov_b64_e32 v[48:49], 0
	v_mov_b64_e32 v[50:51], 0
	v_mov_b64_e32 v[52:53], 0
	v_mov_b64_e32 v[54:55], 0
	v_mov_b64_e32 v[56:57], 0
	v_mov_b64_e32 v[58:59], 0
	v_mov_b64_e32 v[60:61], 0
	v_mov_b64_e32 v[62:63], 0
	v_mov_b64_e32 v[64:65], 0
	v_mov_b64_e32 v[66:67], 0
	v_mov_b64_e32 v[68:69], 0
	v_mov_b64_e32 v[70:71], 0
	v_mov_b64_e32 v[72:73], 0
	v_mov_b64_e32 v[74:75], 0
	v_mov_b64_e32 v[76:77], 0
	v_mov_b64_e32 v[78:79], 0
	v_mov_b64_e32 v[80:81], 0
	v_mov_b64_e32 v[82:83], 0
	v_mov_b64_e32 v[84:85], 0
	v_mov_b64_e32 v[86:87], 0
	v_mov_b64_e32 v[88:89], 0
	v_mov_b64_e32 v[90:91], 0
	v_mov_b64_e32 v[92:93], 0
	v_mov_b64_e32 v[94:95], 0
	v_mov_b64_e32 v[96:97], 0
	v_mov_b64_e32 v[98:99], 0
	v_mov_b64_e32 v[100:101], 0
	v_mov_b64_e32 v[102:103], 0
	v_mov_b64_e32 v[104:105], 0
	v_mov_b64_e32 v[122:123], 0
	v_mov_b64_e32 v[124:125], 0
	v_mov_b64_e32 v[126:127], 0
	v_mov_b64_e32 v[128:129], 0
	v_mov_b64_e32 v[130:131], 0
	v_mov_b64_e32 v[132:133], 0
	v_mov_b64_e32 v[134:135], 0
	v_mov_b64_e32 v[136:137], 0
	v_mov_b64_e32 v[138:139], 0
	v_mov_b64_e32 v[140:141], 0
	v_mov_b64_e32 v[142:143], 0
	v_mov_b64_e32 v[144:145], 0

.LBB0_245:
	s_ashr_i32 s19, s18, 31
	s_lshl_b64 s[30:31], s[18:19], 19
	s_add_u32 s30, s44, s30
	s_addc_u32 s31, s45, s31
	s_and_b64 s[34:35], s[4:5], exec
	s_cselect_b32 s11, s31, s13
	s_cselect_b32 s19, s30, s12
	s_ashr_i32 s29, s28, 31
	s_lshl_b64 s[34:35], s[28:29], 19
	s_add_u32 s34, s46, s34
	s_addc_u32 s35, s47, s35
	s_and_b64 s[36:37], s[4:5], exec
	s_cselect_b32 s29, s35, s15
	s_cselect_b32 s60, s34, s14
	s_add_u32 s61, s14, 0x100
	v_mov_b32_e32 v6, 0
	s_addc_u32 s62, s15, 0
	s_mov_b32 s63, -2
	v_mov_b64_e32 v[2:3], 0
	v_mov_b64_e32 v[4:5], 0
	v_mov_b32_e32 v7, v6
	v_mov_b64_e32 v[8:9], 0
	v_mov_b64_e32 v[10:11], 0
	v_mov_b64_e32 v[12:13], 0
	v_mov_b64_e32 v[14:15], 0
	v_mov_b64_e32 v[16:17], 0
	v_mov_b64_e32 v[18:19], 0
	v_mov_b64_e32 v[20:21], 0
	v_mov_b64_e32 v[22:23], 0
	v_mov_b64_e32 v[24:25], 0
	v_mov_b64_e32 v[26:27], 0
	v_mov_b64_e32 v[28:29], 0
	v_mov_b64_e32 v[30:31], 0
	v_mov_b64_e32 v[32:33], 0
	v_mov_b64_e32 v[34:35], 0
	v_mov_b64_e32 v[36:37], 0
	v_mov_b64_e32 v[38:39], 0
	v_mov_b64_e32 v[40:41], 0
	v_mov_b64_e32 v[42:43], 0
	v_mov_b64_e32 v[44:45], 0
	v_mov_b64_e32 v[46:47], 0
	v_mov_b64_e32 v[48:49], 0
	v_mov_b64_e32 v[50:51], 0
	v_mov_b64_e32 v[52:53], 0
	v_mov_b64_e32 v[54:55], 0
	v_mov_b64_e32 v[56:57], 0
	v_mov_b64_e32 v[58:59], 0
	v_mov_b64_e32 v[60:61], 0
	v_mov_b64_e32 v[62:63], 0
	v_mov_b64_e32 v[64:65], 0
	v_mov_b64_e32 v[66:67], 0
	v_mov_b64_e32 v[68:69], 0
	v_mov_b64_e32 v[70:71], 0
	v_mov_b64_e32 v[72:73], 0
	v_mov_b64_e32 v[74:75], 0
	v_mov_b64_e32 v[76:77], 0
	v_mov_b64_e32 v[78:79], 0
	v_mov_b64_e32 v[80:81], 0
	v_mov_b64_e32 v[82:83], 0
	v_mov_b64_e32 v[84:85], 0
	v_mov_b64_e32 v[86:87], 0
	v_mov_b64_e32 v[88:89], 0
	v_mov_b64_e32 v[90:91], 0
	v_mov_b64_e32 v[92:93], 0
	v_mov_b64_e32 v[94:95], 0
	v_mov_b64_e32 v[96:97], 0
	v_mov_b64_e32 v[98:99], 0
	v_mov_b64_e32 v[100:101], 0
	v_mov_b64_e32 v[102:103], 0
	v_mov_b64_e32 v[104:105], 0
	v_mov_b64_e32 v[122:123], 0
	v_mov_b64_e32 v[124:125], 0
	v_mov_b64_e32 v[126:127], 0
	v_mov_b64_e32 v[128:129], 0
	v_mov_b64_e32 v[130:131], 0
	v_mov_b64_e32 v[132:133], 0
	v_mov_b64_e32 v[134:135], 0
	v_mov_b64_e32 v[136:137], 0
	v_mov_b64_e32 v[138:139], 0
	v_mov_b64_e32 v[140:141], 0
	v_mov_b64_e32 v[142:143], 0
	v_mov_b64_e32 v[144:145], 0

.LBB0_389:
	s_add_i32 s87, s88, 0
	v_add3_u32 v13, s87, v129, v140
	v_add3_u32 v12, s87, v130, v140
	ds_read_b128 v[162:165], v13
	ds_read_b128 v[166:169], v12
	v_mov_b64_e32 v[92:93], s[38:39]
	v_mov_b64_e32 v[90:91], s[36:37]
	v_add3_u32 v13, s87, v129, v141
	s_waitcnt vmcnt(8) lgkmcnt(0)
	s_nop 1
	v_mfma_f32_16x16x128_f8f6f4 v[90:93], v[162:169], v[2:9], v[90:93]
	v_add3_u32 v12, s87, v130, v141
	ds_read_b128 v[162:165], v13
	ds_read_b128 v[166:169], v12
	v_mov_b64_e32 v[72:73], s[38:39]
	v_mov_b64_e32 v[70:71], s[36:37]
	s_waitcnt lgkmcnt(0)
	s_nop 1
	v_mfma_f32_16x16x128_f8f6f4 v[70:73], v[162:169], v[2:9], v[70:73]
	s_nop 11
	v_cndmask_b32_e64 v2, v112, v113, s[16:17]
	ds_read_b128 v[2:5], v2
	s_mov_b32 s16, 0xff800000
	v_cndmask_b32_e64 v13, v143, v113, s[20:21]
	s_waitcnt lgkmcnt(0)
	v_fmamk_f32 v2, v66, 0x3a0293ee, v2
	v_fmamk_f32 v3, v67, 0x3a0293ee, v3
	v_max3_f32 v6, v2, s16, v3
	v_fmamk_f32 v4, v68, 0x3a0293ee, v4
	v_fmac_f32_e32 v5, 0x3a0293ee, v69
	v_max3_f32 v12, v6, v4, v5
	v_cndmask_b32_e64 v6, v142, v113, s[18:19]
	ds_read_b128 v[6:9], v6
	s_waitcnt lgkmcnt(0)
	v_fmamk_f32 v6, v54, 0x3a0293ee, v6
	v_fmamk_f32 v7, v55, 0x3a0293ee, v7
	v_fmamk_f32 v8, v56, 0x3a0293ee, v8
	v_fmac_f32_e32 v9, 0x3a0293ee, v57
	ds_read_b128 v[54:57], v13
	v_max3_f32 v12, v12, v6, v7
	v_max3_f32 v12, v12, v8, v9
	s_waitcnt lgkmcnt(0)
	v_fmamk_f32 v13, v78, 0x3a0293ee, v54
	v_fmamk_f32 v54, v79, 0x3a0293ee, v55
	v_fmamk_f32 v55, v80, 0x3a0293ee, v56
	v_cndmask_b32_e64 v56, v144, v113, s[22:23]
	ds_read_b128 v[66:69], v56
	v_fmac_f32_e32 v57, 0x3a0293ee, v81
	v_max3_f32 v12, v12, v13, v54
	v_max3_f32 v12, v12, v55, v57
	s_waitcnt lgkmcnt(0)
	v_fmamk_f32 v56, v58, 0x3a0293ee, v66
	v_fmamk_f32 v66, v59, 0x3a0293ee, v67
	v_fmamk_f32 v67, v60, 0x3a0293ee, v68
	v_cndmask_b32_e64 v58, v145, v113, s[24:25]
	v_cndmask_b32_e64 v68, v146, v113, s[26:27]
	v_fmac_f32_e32 v69, 0x3a0293ee, v61
	ds_read_b128 v[58:61], v58
	ds_read_b128 v[78:81], v68
	v_max3_f32 v12, v12, v56, v66
	v_max3_f32 v12, v12, v67, v69
	s_waitcnt lgkmcnt(1)
	v_fmamk_f32 v58, v82, 0x3a0293ee, v58
	v_fmamk_f32 v59, v83, 0x3a0293ee, v59
	v_fmamk_f32 v60, v84, 0x3a0293ee, v60
	v_fmac_f32_e32 v61, 0x3a0293ee, v85
	s_waitcnt lgkmcnt(0)
	v_fmamk_f32 v68, v62, 0x3a0293ee, v78
	v_cndmask_b32_e64 v62, v147, v113, s[28:29]
	ds_read_b128 v[82:85], v10
	v_fmamk_f32 v79, v63, 0x3a0293ee, v79
	v_fmamk_f32 v80, v64, 0x3a0293ee, v80
	v_fmac_f32_e32 v81, 0x3a0293ee, v65
	ds_read_b128 v[62:65], v62
	v_max3_f32 v12, v12, v58, v59
	v_max3_f32 v12, v12, v60, v61
	v_max3_f32 v12, v12, v68, v79
	s_waitcnt lgkmcnt(1)
	v_fmamk_f32 v10, v74, 0x3a0293ee, v82
	v_fmamk_f32 v82, v75, 0x3a0293ee, v83
	v_fmamk_f32 v83, v76, 0x3a0293ee, v84
	v_fmac_f32_e32 v85, 0x3a0293ee, v77
	ds_read_b128 v[74:77], v111 offset:640
	v_max3_f32 v12, v12, v80, v81
	s_waitcnt lgkmcnt(1)
	v_fmamk_f32 v62, v86, 0x3a0293ee, v62
	v_fmamk_f32 v63, v87, 0x3a0293ee, v63
	v_fmamk_f32 v64, v88, 0x3a0293ee, v64
	v_fmac_f32_e32 v65, 0x3a0293ee, v89
	ds_read_b128 v[86:89], v111 offset:704
	v_max3_f32 v12, v12, v62, v63
	v_max3_f32 v12, v12, v64, v65
	v_max3_f32 v12, v12, v10, v82
	v_max3_f32 v12, v12, v83, v85
	s_waitcnt lgkmcnt(1)
	v_fmamk_f32 v74, v90, 0x3a0293ee, v74
	v_fmamk_f32 v75, v91, 0x3a0293ee, v75
	v_and_b32_e32 v78, 64, v158
	v_max3_f32 v12, v12, v74, v75
	v_fmamk_f32 v76, v92, 0x3a0293ee, v76
	v_fmac_f32_e32 v77, 0x3a0293ee, v93
	s_waitcnt lgkmcnt(0)
	v_fmac_f32_e32 v89, 0x3a0293ee, v73
	v_xor_b32_e32 v73, 16, v158
	v_add_u32_e32 v78, 64, v78
	v_max3_f32 v12, v12, v76, v77
	v_fmamk_f32 v70, v70, 0x3a0293ee, v86
	v_fmamk_f32 v71, v71, 0x3a0293ee, v87
	v_cmp_lt_i32_e32 vcc, v73, v78
	v_max3_f32 v12, v12, v70, v71
	v_fmamk_f32 v72, v72, 0x3a0293ee, v88
	v_cndmask_b32_e32 v73, v158, v73, vcc
	v_max3_f32 v12, v12, v72, v89
	v_lshlrev_b32_e32 v73, 2, v73
	ds_bpermute_b32 v84, v73, v12
	s_waitcnt lgkmcnt(0)
	v_max_f32_e32 v84, v84, v84
	v_max_f32_e32 v12, v12, v84
	v_xor_b32_e32 v84, 32, v158
	v_cmp_lt_i32_e32 vcc, v84, v78
	s_nop 1
	v_cndmask_b32_e32 v78, v158, v84, vcc
	v_lshlrev_b32_e32 v180, 2, v78
	ds_bpermute_b32 v78, v180, v12
	s_andn2_b64 vcc, exec, s[68:69]
	s_waitcnt lgkmcnt(0)
	v_max_f32_e32 v78, v78, v78
	v_max_f32_e32 v78, v12, v78
	v_sub_f32_e32 v2, v2, v78
	v_exp_f32_e32 v2, v2
	v_sub_f32_e32 v3, v3, v78
	v_exp_f32_e32 v3, v3
	v_sub_f32_e32 v4, v4, v78
	v_exp_f32_e32 v4, v4
	v_sub_f32_e32 v5, v5, v78
	v_exp_f32_e32 v5, v5
	v_sub_f32_e32 v6, v6, v78
	v_add_f32_e32 v12, 0, v2
	v_exp_f32_e32 v6, v6
	v_sub_f32_e32 v7, v7, v78
	v_add_f32_e32 v12, v3, v12
	v_exp_f32_e32 v7, v7
	v_sub_f32_e32 v8, v8, v78
	v_add_f32_e32 v12, v4, v12
	v_exp_f32_e32 v8, v8
	v_sub_f32_e32 v9, v9, v78
	v_add_f32_e32 v12, v5, v12
	v_exp_f32_e32 v9, v9
	v_sub_f32_e32 v13, v13, v78
	v_add_f32_e32 v12, v6, v12
	v_exp_f32_e32 v172, v13
	v_sub_f32_e32 v13, v54, v78
	v_add_f32_e32 v12, v7, v12
	v_exp_f32_e32 v173, v13
	v_sub_f32_e32 v13, v55, v78
	v_add_f32_e32 v12, v8, v12
	v_exp_f32_e32 v174, v13
	v_sub_f32_e32 v13, v57, v78
	v_add_f32_e32 v12, v9, v12
	v_exp_f32_e32 v175, v13
	v_sub_f32_e32 v13, v56, v78
	v_add_f32_e32 v12, v172, v12
	v_exp_f32_e32 v176, v13
	v_sub_f32_e32 v13, v66, v78
	v_add_f32_e32 v12, v173, v12
	v_exp_f32_e32 v177, v13
	v_sub_f32_e32 v13, v67, v78
	v_add_f32_e32 v12, v174, v12
	v_exp_f32_e32 v178, v13
	v_sub_f32_e32 v13, v69, v78
	v_add_f32_e32 v12, v175, v12
	v_exp_f32_e32 v179, v13
	v_sub_f32_e32 v13, v58, v78
	v_add_f32_e32 v12, v176, v12
	v_exp_f32_e32 v164, v13
	v_sub_f32_e32 v13, v59, v78
	v_add_f32_e32 v12, v177, v12
	v_exp_f32_e32 v165, v13
	v_sub_f32_e32 v13, v60, v78
	v_add_f32_e32 v12, v178, v12
	v_exp_f32_e32 v166, v13
	v_sub_f32_e32 v13, v61, v78
	v_add_f32_e32 v12, v179, v12
	v_exp_f32_e32 v167, v13
	v_sub_f32_e32 v13, v68, v78
	v_add_f32_e32 v12, v164, v12
	v_exp_f32_e32 v168, v13
	v_sub_f32_e32 v13, v79, v78
	v_add_f32_e32 v12, v165, v12
	v_exp_f32_e32 v169, v13
	v_sub_f32_e32 v13, v80, v78
	v_add_f32_e32 v12, v166, v12
	v_exp_f32_e32 v170, v13
	v_sub_f32_e32 v13, v81, v78
	v_add_f32_e32 v12, v167, v12
	v_exp_f32_e32 v171, v13
	v_sub_f32_e32 v13, v62, v78
	v_add_f32_e32 v12, v168, v12
	v_exp_f32_e32 v88, v13
	v_sub_f32_e32 v13, v63, v78
	v_add_f32_e32 v12, v169, v12
	v_exp_f32_e32 v90, v13
	v_sub_f32_e32 v13, v64, v78
	v_add_f32_e32 v12, v170, v12
	v_exp_f32_e32 v91, v13
	v_sub_f32_e32 v13, v65, v78
	v_add_f32_e32 v12, v171, v12
	v_exp_f32_e32 v92, v13
	v_sub_f32_e32 v10, v10, v78
	v_add_f32_e32 v12, v88, v12
	v_exp_f32_e32 v93, v10
	v_add_f32_e32 v12, v90, v12
	v_add_f32_e32 v12, v91, v12
	v_add_f32_e32 v12, v92, v12
	v_add_f32_e32 v10, v93, v12
	v_sub_f32_e32 v12, v82, v78
	v_exp_f32_e32 v161, v12
	v_sub_f32_e32 v12, v83, v78
	v_exp_f32_e32 v162, v12
	v_sub_f32_e32 v12, v85, v78
	v_exp_f32_e32 v163, v12
	v_sub_f32_e32 v12, v74, v78
	v_exp_f32_e32 v81, v12
	v_sub_f32_e32 v12, v75, v78
	v_add_f32_e32 v10, v161, v10
	v_exp_f32_e32 v82, v12
	v_sub_f32_e32 v12, v76, v78
	v_add_f32_e32 v10, v162, v10
	v_exp_f32_e32 v83, v12
	v_sub_f32_e32 v12, v77, v78
	v_add_f32_e32 v10, v163, v10
	v_exp_f32_e32 v84, v12
	v_sub_f32_e32 v12, v70, v78
	v_add_f32_e32 v10, v81, v10
	v_exp_f32_e32 v85, v12
	v_sub_f32_e32 v12, v71, v78
	v_add_f32_e32 v10, v82, v10
	v_exp_f32_e32 v86, v12
	v_sub_f32_e32 v12, v72, v78
	v_add_f32_e32 v10, v83, v10
	v_exp_f32_e32 v87, v12
	v_sub_f32_e32 v12, v89, v78
	v_add_f32_e32 v10, v84, v10
	v_exp_f32_e32 v89, v12
	v_add_f32_e32 v10, v85, v10
	v_add_f32_e32 v10, v86, v10
	v_add_f32_e32 v10, v87, v10
	v_add_f32_e32 v10, v89, v10
	ds_bpermute_b32 v12, v73, v10
	s_waitcnt lgkmcnt(0)
	v_add_f32_e32 v79, v10, v12
	ds_bpermute_b32 v80, v180, v79
	s_cbranch_vccnz .LBB0_391
	s_and_b64 s[16:17], s[46:47], exec
	s_cselect_b32 s16, s43, s86
	v_add_u32_e32 v10, s16, v157
	v_cvt_pk_bf16_f32 v54, v2, v3
	v_cvt_pk_bf16_f32 v55, v4, v5
	v_cvt_pk_bf16_f32 v56, v6, v7
	v_cvt_pk_bf16_f32 v57, v8, v9
	v_add_u32_e32 v4, v10, v149
	v_add_u32_e32 v8, v10, v150
	v_add_u32_e32 v12, v10, v151
	ds_read_b64_tr_b16 v[2:3], v4
	ds_read_b64_tr_b16 v[4:5], v4 offset:4096
	ds_read_b64_tr_b16 v[6:7], v8
	ds_read_b64_tr_b16 v[8:9], v8 offset:4096
	ds_read_b64_tr_b16 v[58:59], v12
	ds_read_b64_tr_b16 v[60:61], v12 offset:4096
	v_add_u32_e32 v12, v10, v152
	ds_read_b64_tr_b16 v[62:63], v12
	ds_read_b64_tr_b16 v[64:65], v12 offset:4096
	v_add_u32_e32 v12, v10, v153
	ds_read_b64_tr_b16 v[66:67], v12
	ds_read_b64_tr_b16 v[68:69], v12 offset:4096
	v_add_u32_e32 v12, v10, v154
	ds_read_b64_tr_b16 v[70:71], v12
	ds_read_b64_tr_b16 v[72:73], v12 offset:4096
	v_add_u32_e32 v12, v10, v155
	v_add_u32_e32 v10, v10, v156
	ds_read_b64_tr_b16 v[180:181], v12
	ds_read_b64_tr_b16 v[182:183], v12 offset:4096
	ds_read_b64_tr_b16 v[184:185], v10
	ds_read_b64_tr_b16 v[186:187], v10 offset:4096
	s_waitcnt lgkmcnt(14)
	v_mfma_f32_16x16x32_bf16 v[2:5], v[2:5], v[54:57], 0
	s_waitcnt lgkmcnt(12)
	v_mfma_f32_16x16x32_bf16 v[6:9], v[6:9], v[54:57], 0
	s_waitcnt lgkmcnt(10)
	v_mfma_f32_16x16x32_bf16 v[58:61], v[58:61], v[54:57], 0
	s_waitcnt lgkmcnt(8)
	v_mfma_f32_16x16x32_bf16 v[62:65], v[62:65], v[54:57], 0
	s_waitcnt lgkmcnt(6)
	v_mfma_f32_16x16x32_bf16 v[66:69], v[66:69], v[54:57], 0
	s_waitcnt lgkmcnt(4)
	v_mfma_f32_16x16x32_bf16 v[74:77], v[70:73], v[54:57], 0
	s_waitcnt lgkmcnt(2)
	v_mfma_f32_16x16x32_bf16 v[70:73], v[180:183], v[54:57], 0
	s_waitcnt lgkmcnt(0)
	v_mfma_f32_16x16x32_bf16 v[54:57], v[184:187], v[54:57], 0
	s_branch .LBB0_392

.LBB0_529:
	s_ashr_i32 s19, s18, 31
	s_lshl_b64 s[22:23], s[18:19], 18
	s_add_u32 s22, s38, s22
	s_addc_u32 s23, s39, s23
	s_and_b64 s[24:25], s[34:35], exec
	s_cselect_b32 s19, s23, s31
	s_cselect_b32 s53, s22, s30
	s_ashr_i32 s21, s20, 31
	s_lshl_b64 s[24:25], s[20:21], 18
	s_add_u32 s24, s40, s24
	s_addc_u32 s25, s41, s25
	s_and_b64 s[34:35], s[34:35], exec
	s_cselect_b32 s21, s25, s29
	s_cselect_b32 s54, s24, s28
	s_add_u32 s55, s28, 0x100
	v_mov_b32_e32 v38, 0
	s_addc_u32 s56, s29, 0
	s_mov_b32 s57, -2
	v_mov_b64_e32 v[34:35], 0
	v_mov_b64_e32 v[36:37], 0
	v_mov_b32_e32 v39, v38
	v_mov_b64_e32 v[40:41], 0
	v_mov_b64_e32 v[50:51], 0
	v_mov_b64_e32 v[52:53], 0
	v_mov_b64_e32 v[54:55], 0
	v_mov_b64_e32 v[56:57], 0
	v_mov_b64_e32 v[66:67], 0
	v_mov_b64_e32 v[68:69], 0
	v_mov_b64_e32 v[70:71], 0
	v_mov_b64_e32 v[72:73], 0
	v_mov_b64_e32 v[82:83], 0
	v_mov_b64_e32 v[84:85], 0
	v_mov_b64_e32 v[86:87], 0
	v_mov_b64_e32 v[88:89], 0
	v_mov_b64_e32 v[98:99], 0
	v_mov_b64_e32 v[100:101], 0
	v_mov_b64_e32 v[102:103], 0
	v_mov_b64_e32 v[104:105], 0
	s_waitcnt lgkmcnt(0)
	v_mov_b64_e32 v[42:43], 0
	v_mov_b64_e32 v[44:45], 0
	v_mov_b64_e32 v[46:47], 0
	v_mov_b64_e32 v[48:49], 0
	v_mov_b64_e32 v[58:59], 0
	v_mov_b64_e32 v[60:61], 0
	v_mov_b64_e32 v[62:63], 0
	v_mov_b64_e32 v[64:65], 0
	v_mov_b64_e32 v[74:75], 0
	v_mov_b64_e32 v[76:77], 0
	v_mov_b64_e32 v[78:79], 0
	v_mov_b64_e32 v[80:81], 0
	v_mov_b64_e32 v[90:91], 0
	v_mov_b64_e32 v[92:93], 0
	v_mov_b64_e32 v[94:95], 0
	v_mov_b64_e32 v[96:97], 0
	v_mov_b64_e32 v[106:107], 0
	v_mov_b64_e32 v[108:109], 0
	v_mov_b64_e32 v[110:111], 0
	v_mov_b64_e32 v[112:113], 0
	v_mov_b64_e32 v[114:115], 0
	v_mov_b64_e32 v[116:117], 0
	v_mov_b64_e32 v[118:119], 0
	v_mov_b64_e32 v[120:121], 0
	v_mov_b64_e32 v[122:123], 0
	v_mov_b64_e32 v[124:125], 0
	v_mov_b64_e32 v[126:127], 0
	v_mov_b64_e32 v[128:129], 0
	v_mov_b64_e32 v[130:131], 0
	v_mov_b64_e32 v[132:133], 0
	v_mov_b64_e32 v[134:135], 0
	v_mov_b64_e32 v[136:137], 0
	v_mov_b64_e32 v[138:139], 0
	v_mov_b64_e32 v[140:141], 0
	v_mov_b64_e32 v[142:143], 0
	v_mov_b64_e32 v[144:145], 0
	v_mov_b64_e32 v[146:147], 0
	v_mov_b64_e32 v[148:149], 0
	v_mov_b64_e32 v[150:151], 0
	v_mov_b64_e32 v[152:153], 0
	v_mov_b64_e32 v[154:155], 0
	v_mov_b64_e32 v[156:157], 0
	v_mov_b64_e32 v[158:159], 0
	v_mov_b64_e32 v[160:161], 0

.LBB0_533:
	v_lshl_add_u32 v22, s26, 8, v190
	v_lshl_or_b32 v14, s52, 8, v194
	v_mov_b64_e32 v[16:17], s[88:89]
	v_ashrrev_i32_e32 v15, 31, v14
	v_mad_i64_i32 v[2:3], s[28:29], v22, s51, v[16:17]
	v_lshl_add_u64 v[2:3], v[2:3], 0, s[14:15]
	v_lshlrev_b64 v[18:19], 1, v[14:15]
	s_nop 11
	v_lshl_add_u64 v[4:5], v[2:3], 0, v[18:19]
	global_load_dwordx4 v[24:27], v[4:5], off
	v_or_b32_e32 v4, 0x80, v14
	v_ashrrev_i32_e32 v5, 31, v4
	v_lshlrev_b64 v[20:21], 1, v[4:5]
	v_lshl_add_u64 v[2:3], v[2:3], 0, v[20:21]
	global_load_dwordx4 v[28:31], v[2:3], off
	v_or_b32_e32 v2, 16, v22
	v_mad_i64_i32 v[2:3], s[28:29], v2, s51, v[16:17]
	v_lshl_add_u64 v[2:3], v[2:3], 0, s[14:15]
	v_lshl_add_u64 v[4:5], v[2:3], 0, v[18:19]
	v_pk_mul_f32 v[198:199], v[148:149], s[16:17] op_sel_hi:[1,0]
	v_pk_mul_f32 v[200:201], v[146:147], s[16:17] op_sel_hi:[1,0]
	global_load_dwordx4 v[146:149], v[4:5], off
	v_or_b32_e32 v6, 32, v22
	v_or_b32_e32 v7, 48, v22
	v_mad_i64_i32 v[4:5], s[28:29], v6, s51, v[16:17]
	v_mad_i64_i32 v[6:7], s[28:29], v7, s51, v[16:17]
	v_lshl_add_u64 v[4:5], v[4:5], 0, s[14:15]
	v_lshl_add_u64 v[6:7], v[6:7], 0, s[14:15]
	v_lshl_add_u64 v[2:3], v[2:3], 0, v[20:21]
	v_lshl_add_u64 v[8:9], v[4:5], 0, v[18:19]
	v_lshl_add_u64 v[4:5], v[4:5], 0, v[20:21]
	v_pk_mul_f32 v[32:33], v[160:161], s[16:17] op_sel_hi:[1,0]
	v_pk_mul_f32 v[182:183], v[158:159], s[16:17] op_sel_hi:[1,0]
	v_pk_mul_f32 v[186:187], v[152:153], s[16:17] op_sel_hi:[1,0]
	v_pk_mul_f32 v[188:189], v[150:151], s[16:17] op_sel_hi:[1,0]
	v_lshl_add_u64 v[202:203], v[6:7], 0, v[18:19]
	v_lshl_add_u64 v[204:205], v[6:7], 0, v[20:21]
	global_load_dwordx4 v[150:153], v[2:3], off
	global_load_dwordx4 v[158:161], v[8:9], off
	global_load_dwordx4 v[10:13], v[4:5], off
	s_nop 0
	global_load_dwordx4 v[6:9], v[202:203], off
	global_load_dwordx4 v[2:5], v[204:205], off
	v_pk_mul_f32 v[184:185], v[154:155], s[16:17] op_sel_hi:[1,0]
	v_mov_b32_e32 v154, 0
	v_mov_b32_e32 v155, 0
	v_pk_mul_f32 v[156:157], v[156:157], s[16:17] op_sel_hi:[1,0]
	s_and_b64 vcc, exec, s[6:7]
	s_mov_b64 s[6:7], -1
	s_waitcnt vmcnt(0)
	v_lshlrev_b32_e32 v23, 16, v24
	v_and_b32_e32 v24, 0xffff0000, v24
	v_lshlrev_b32_e32 v202, 16, v25
	v_and_b32_e32 v25, 0xffff0000, v25
	v_lshlrev_b32_e32 v203, 16, v26
	v_and_b32_e32 v26, 0xffff0000, v26
	v_mul_f32_e32 v23, v182, v23
	v_mul_f32_e32 v24, v183, v24
	v_mul_f32_e32 v25, v33, v25
	v_mul_f32_e32 v33, v184, v203
	v_mul_f32_e32 v26, v185, v26
	v_mul_f32_e32 v23, 0x41800000, v23
	v_mul_f32_e32 v24, 0x41800000, v24
	v_mul_f32_e32 v33, 0x41800000, v33
	v_mul_f32_e32 v26, 0x41800000, v26
	v_cvt_pk_fp8_f32 v154, v23, v24
	v_cvt_pk_fp8_f32 v155, v33, v26
	v_lshlrev_b32_e32 v204, 16, v27
	v_and_b32_e32 v27, 0xffff0000, v27
	v_mul_f32_e32 v32, v32, v202
	v_mul_f32_e32 v156, v156, v204
	v_mul_f32_e32 v27, v157, v27
	v_lshlrev_b32_e32 v157, 16, v28
	v_and_b32_e32 v28, 0xffff0000, v28
	v_lshlrev_b32_e32 v183, 16, v30
	v_and_b32_e32 v30, 0xffff0000, v30
	v_mul_f32_e32 v32, 0x41800000, v32
	v_mul_f32_e32 v25, 0x41800000, v25
	v_mul_f32_e32 v156, 0x41800000, v156
	v_mul_f32_e32 v27, 0x41800000, v27
	v_mul_f32_e32 v157, v188, v157
	v_mul_f32_e32 v28, v189, v28
	v_and_b32_e32 v24, 0xffff0000, v31
	v_mul_f32_e32 v183, v200, v183
	v_mul_f32_e32 v23, v201, v30
	v_cvt_pk_fp8_f32 v154, v32, v25 op_sel:[0,0,1]
	v_cvt_pk_fp8_f32 v155, v156, v27 op_sel:[0,0,1]
	v_mul_f32_e32 v27, v199, v24
	v_mul_f32_e32 v25, 0x41800000, v157
	v_mul_f32_e32 v28, 0x41800000, v28
	v_mov_b32_e32 v24, 0
	v_cvt_pk_fp8_f32 v24, v25, v28
	v_mul_f32_e32 v28, 0x41800000, v183
	v_mul_f32_e32 v23, 0x41800000, v23
	v_mov_b32_e32 v25, 0
	v_cvt_pk_fp8_f32 v25, v28, v23
	v_lshlrev_b32_e32 v182, 16, v29
	v_and_b32_e32 v29, 0xffff0000, v29
	v_lshlrev_b32_e32 v184, 16, v31
	v_mul_f32_e32 v182, v186, v182
	v_mul_f32_e32 v29, v187, v29
	v_mul_f32_e32 v26, v198, v184
	v_mul_f32_e32 v30, 0x41800000, v182
	v_mul_f32_e32 v29, 0x41800000, v29
	v_mul_f32_e32 v23, 0x41800000, v26
	v_mul_f32_e32 v26, 0x41800000, v27
	v_cvt_pk_fp8_f32 v24, v30, v29 op_sel:[0,0,1]
	v_cvt_pk_fp8_f32 v25, v23, v26 op_sel:[0,0,1]
	v_pk_mul_f32 v[28:29], v[144:145], s[16:17] op_sel_hi:[1,0]
	v_lshlrev_b32_e32 v23, 16, v149
	v_mul_f32_e32 v23, v28, v23
	v_and_b32_e32 v28, 0xffff0000, v149
	v_pk_mul_f32 v[30:31], v[142:143], s[16:17] op_sel_hi:[1,0]
	v_mul_f32_e32 v32, v29, v28
	v_lshlrev_b32_e32 v28, 16, v148
	v_and_b32_e32 v29, 0xffff0000, v148
	v_mul_f32_e32 v28, v30, v28
	v_mul_f32_e32 v29, v31, v29
	v_mul_f32_e32 v28, 0x41800000, v28
	v_mul_f32_e32 v29, 0x41800000, v29
	v_mov_b32_e32 v157, 0
	v_cvt_pk_fp8_f32 v157, v28, v29
	v_pk_mul_f32 v[28:29], v[140:141], s[16:17] op_sel_hi:[1,0]
	v_lshlrev_b32_e32 v33, 16, v147
	v_pk_mul_f32 v[30:31], v[138:139], s[16:17] op_sel_hi:[1,0]
	v_mul_f32_e32 v28, v28, v33
	v_lshlrev_b32_e32 v33, 16, v146
	v_mul_f32_e32 v30, v30, v33
	v_and_b32_e32 v33, 0xffff0000, v146
	v_mul_f32_e32 v31, v31, v33
	v_mul_f32_e32 v30, 0x41800000, v30
	v_mul_f32_e32 v31, 0x41800000, v31
	v_mov_b32_e32 v156, 0
	v_or_b32_e32 v26, v22, v192
	v_cvt_pk_fp8_f32 v156, v30, v31
	v_ashrrev_i32_e32 v27, 31, v26
	v_and_b32_e32 v30, 0xffff0000, v147
	v_lshlrev_b64 v[26:27], 11, v[26:27]
	v_mul_f32_e32 v29, v29, v30
	v_mul_f32_e32 v28, 0x41800000, v28
	v_mul_f32_e32 v29, 0x41800000, v29
	v_lshl_add_u64 v[26:27], s[8:9], 0, v[26:27]
	v_mul_f32_e32 v23, 0x41800000, v23
	v_cvt_pk_fp8_f32 v156, v28, v29 op_sel:[0,0,1]
	v_mul_f32_e32 v28, 0x41800000, v32
	v_lshl_add_u64 v[26:27], v[26:27], 0, v[14:15]
	v_cvt_pk_fp8_f32 v157, v23, v28 op_sel:[0,0,1]
	v_lshl_add_u64 v[28:29], v[26:27], 0, v[174:175]
	v_pk_mul_f32 v[26:27], v[136:137], s[16:17] op_sel_hi:[1,0]
	v_lshlrev_b32_e32 v23, 16, v153
	v_mul_f32_e32 v23, v26, v23
	v_and_b32_e32 v26, 0xffff0000, v153
	v_pk_mul_f32 v[30:31], v[134:135], s[16:17] op_sel_hi:[1,0]
	v_mul_f32_e32 v134, v27, v26
	v_lshlrev_b32_e32 v26, 16, v152
	v_and_b32_e32 v27, 0xffff0000, v152
	v_mul_f32_e32 v26, v30, v26
	v_mul_f32_e32 v27, v31, v27
	v_mul_f32_e32 v26, 0x41800000, v26
	v_mul_f32_e32 v30, 0x41800000, v27
	v_mov_b32_e32 v27, 0
	v_cvt_pk_fp8_f32 v27, v26, v30
	v_pk_mul_f32 v[30:31], v[132:133], s[16:17] op_sel_hi:[1,0]
	v_lshlrev_b32_e32 v26, 16, v151
	v_mul_f32_e32 v26, v30, v26
	v_pk_mul_f32 v[32:33], v[130:131], s[16:17] op_sel_hi:[1,0]
	v_mul_f32_e32 v30, 0x41800000, v26
	v_lshlrev_b32_e32 v26, 16, v150
	v_mul_f32_e32 v26, v32, v26
	v_mul_f32_e32 v32, 0x41800000, v26
	v_and_b32_e32 v26, 0xffff0000, v150
	v_mul_f32_e32 v26, v33, v26
	v_mul_f32_e32 v33, 0x41800000, v26
	v_mov_b32_e32 v26, 0
	v_cvt_pk_fp8_f32 v26, v32, v33
	v_and_b32_e32 v32, 0xffff0000, v151
	v_mul_f32_e32 v31, v31, v32
	v_mul_f32_e32 v31, 0x41800000, v31
	v_mul_f32_e32 v23, 0x41800000, v23
	v_cvt_pk_fp8_f32 v26, v30, v31 op_sel:[0,0,1]
	v_mul_f32_e32 v30, 0x41800000, v134
	v_cvt_pk_fp8_f32 v27, v23, v30 op_sel:[0,0,1]
	v_lshlrev_b32_e32 v23, 16, v158
	v_permlane16_swap_b32_e32 v24, v26
	v_permlane16_swap_b32_e32 v25, v27
	global_store_dwordx4 v[28:29], v[24:27], off offset:128
	v_pk_mul_f32 v[30:31], v[122:123], s[16:17] op_sel_hi:[1,0]
	v_permlane16_swap_b32_e32 v154, v156
	v_pk_mul_f32 v[26:27], v[126:127], s[16:17] op_sel_hi:[1,0]
	v_pk_mul_f32 v[24:25], v[128:129], s[16:17] op_sel_hi:[1,0]
	v_mul_f32_e32 v23, v26, v23
	v_and_b32_e32 v26, 0xffff0000, v158
	v_mul_f32_e32 v26, v27, v26
	v_lshlrev_b32_e32 v27, 16, v159
	v_mul_f32_e32 v24, v24, v27
	v_and_b32_e32 v27, 0xffff0000, v159
	v_mul_f32_e32 v25, v25, v27
	v_lshlrev_b32_e32 v27, 16, v160
	v_permlane16_swap_b32_e32 v155, v157
	v_mul_f32_e32 v27, v30, v27
	v_and_b32_e32 v30, 0xffff0000, v160
	global_store_dwordx4 v[28:29], v[154:157], off
	v_pk_mul_f32 v[28:29], v[124:125], s[16:17] op_sel_hi:[1,0]
	v_mul_f32_e32 v30, v31, v30
	v_lshlrev_b32_e32 v31, 16, v161
	v_mul_f32_e32 v28, v28, v31
	v_and_b32_e32 v31, 0xffff0000, v161
	v_mul_f32_e32 v29, v29, v31
	v_mul_f32_e32 v23, 0x41800000, v23
	v_mul_f32_e32 v26, 0x41800000, v26
	v_mul_f32_e32 v31, 0x41800000, v24
	v_mov_b32_e32 v24, 0
	v_mul_f32_e32 v32, 0x41800000, v25
	v_cvt_pk_fp8_f32 v24, v23, v26
	v_mul_f32_e32 v23, 0x41800000, v27
	v_mul_f32_e32 v26, 0x41800000, v30
	v_mov_b32_e32 v25, 0
	v_cvt_pk_fp8_f32 v25, v23, v26
	v_mul_f32_e32 v23, 0x41800000, v28
	v_mul_f32_e32 v26, 0x41800000, v29
	v_pk_mul_f32 v[28:29], v[118:119], s[16:17] op_sel_hi:[1,0]
	v_cvt_pk_fp8_f32 v25, v23, v26 op_sel:[0,0,1]
	v_lshlrev_b32_e32 v23, 16, v10
	v_and_b32_e32 v10, 0xffff0000, v10
	v_mul_f32_e32 v23, v28, v23
	v_mul_f32_e32 v10, v29, v10
	v_mul_f32_e32 v23, 0x41800000, v23
	v_mul_f32_e32 v29, 0x41800000, v10
	v_mov_b32_e32 v10, 0
	v_pk_mul_f32 v[26:27], v[120:121], s[16:17] op_sel_hi:[1,0]
	v_lshlrev_b32_e32 v28, 16, v11
	v_and_b32_e32 v11, 0xffff0000, v11
	v_cvt_pk_fp8_f32 v10, v23, v29
	v_cvt_pk_fp8_f32 v24, v31, v32 op_sel:[0,0,1]
	v_pk_mul_f32 v[32:33], v[114:115], s[16:17] op_sel_hi:[1,0]
	v_mul_f32_e32 v11, v27, v11
	v_lshlrev_b32_e32 v27, 16, v12
	v_and_b32_e32 v12, 0xffff0000, v12
	v_pk_mul_f32 v[30:31], v[116:117], s[16:17] op_sel_hi:[1,0]
	v_mul_f32_e32 v26, v26, v28
	v_mul_f32_e32 v27, v32, v27
	v_mul_f32_e32 v12, v33, v12
	v_lshlrev_b32_e32 v28, 16, v13
	v_mul_f32_e32 v28, v30, v28
	v_mul_f32_e32 v26, 0x41800000, v26
	v_mul_f32_e32 v30, 0x41800000, v11
	v_mul_f32_e32 v23, 0x41800000, v27
	v_mul_f32_e32 v12, 0x41800000, v12
	v_mov_b32_e32 v11, 0
	v_cvt_pk_fp8_f32 v11, v23, v12
	v_cvt_pk_fp8_f32 v10, v26, v30 op_sel:[0,0,1]
	v_pk_mul_f32 v[26:27], v[112:113], s[16:17] op_sel_hi:[1,0]
	v_lshlrev_b32_e32 v23, 16, v9
	v_and_b32_e32 v9, 0xffff0000, v9
	v_mul_f32_e32 v12, 0x41800000, v28
	v_pk_mul_f32 v[28:29], v[110:111], s[16:17] op_sel_hi:[1,0]
	v_mul_f32_e32 v30, v27, v9
	v_lshlrev_b32_e32 v9, 16, v8
	v_and_b32_e32 v8, 0xffff0000, v8
	v_mul_f32_e32 v9, v28, v9
	v_mul_f32_e32 v8, v29, v8
	v_mul_f32_e32 v9, 0x41800000, v9
	v_mul_f32_e32 v8, 0x41800000, v8
	v_mov_b32_e32 v27, 0
	v_mul_f32_e32 v23, v26, v23
	v_cvt_pk_fp8_f32 v27, v9, v8
	v_pk_mul_f32 v[8:9], v[108:109], s[16:17] op_sel_hi:[1,0]
	v_lshlrev_b32_e32 v26, 16, v7
	v_pk_mul_f32 v[28:29], v[106:107], s[16:17] op_sel_hi:[1,0]
	v_mul_f32_e32 v8, v8, v26
	v_lshlrev_b32_e32 v26, 16, v6
	v_and_b32_e32 v6, 0xffff0000, v6
	v_mul_f32_e32 v26, v28, v26
	v_mul_f32_e32 v6, v29, v6
	v_mul_f32_e32 v28, 0x41800000, v26
	v_mul_f32_e32 v6, 0x41800000, v6
	v_mov_b32_e32 v26, 0
	v_cvt_pk_fp8_f32 v26, v28, v6
	v_and_b32_e32 v13, 0xffff0000, v13
	v_and_b32_e32 v6, 0xffff0000, v7
	v_mul_f32_e32 v13, v31, v13
	v_mul_f32_e32 v6, v9, v6
	v_mul_f32_e32 v13, 0x41800000, v13
	v_mul_f32_e32 v8, 0x41800000, v8
	v_mul_f32_e32 v6, 0x41800000, v6
	v_cvt_pk_fp8_f32 v11, v12, v13 op_sel:[0,0,1]
	v_or_b32_e32 v12, v22, v193
	v_mul_f32_e32 v23, 0x41800000, v23
	v_cvt_pk_fp8_f32 v26, v8, v6 op_sel:[0,0,1]
	v_mul_f32_e32 v6, 0x41800000, v30
	v_ashrrev_i32_e32 v13, 31, v12
	v_cvt_pk_fp8_f32 v27, v23, v6 op_sel:[0,0,1]
	v_lshlrev_b64 v[12:13], 11, v[12:13]
	v_lshl_add_u64 v[6:7], s[8:9], 0, v[12:13]
	v_lshl_add_u64 v[6:7], v[6:7], 0, v[14:15]
	v_permlane16_swap_b32_e32 v24, v26
	v_permlane16_swap_b32_e32 v25, v27
	v_lshl_add_u64 v[6:7], v[6:7], 0, v[174:175]
	v_pk_mul_f32 v[8:9], v[104:105], s[16:17] op_sel_hi:[1,0]
	v_lshlrev_b32_e32 v23, 16, v5
	v_and_b32_e32 v5, 0xffff0000, v5
	global_store_dwordx4 v[6:7], v[24:27], off
	v_pk_mul_f32 v[12:13], v[102:103], s[16:17] op_sel_hi:[1,0]
	v_mul_f32_e32 v8, v8, v23
	v_mul_f32_e32 v24, v9, v5
	v_lshlrev_b32_e32 v5, 16, v4
	v_and_b32_e32 v4, 0xffff0000, v4
	v_mul_f32_e32 v5, v12, v5
	v_mul_f32_e32 v4, v13, v4
	v_mul_f32_e32 v5, 0x41800000, v5
	v_mul_f32_e32 v4, 0x41800000, v4
	v_mov_b32_e32 v13, 0
	v_cvt_pk_fp8_f32 v13, v5, v4
	v_pk_mul_f32 v[4:5], v[100:101], s[16:17] op_sel_hi:[1,0]
	v_lshlrev_b32_e32 v12, 16, v3
	v_mul_f32_e32 v23, 0x41800000, v8
	v_pk_mul_f32 v[8:9], v[98:99], s[16:17] op_sel_hi:[1,0]
	v_mul_f32_e32 v4, v4, v12
	v_lshlrev_b32_e32 v12, 16, v2
	v_and_b32_e32 v2, 0xffff0000, v2
	v_mul_f32_e32 v8, v8, v12
	v_mul_f32_e32 v2, v9, v2
	v_mul_f32_e32 v8, 0x41800000, v8
	v_mul_f32_e32 v2, 0x41800000, v2
	v_mov_b32_e32 v12, 0
	v_cvt_pk_fp8_f32 v12, v8, v2
	v_and_b32_e32 v2, 0xffff0000, v3
	v_mul_f32_e32 v2, v5, v2
	v_mul_f32_e32 v4, 0x41800000, v4
	v_mul_f32_e32 v2, 0x41800000, v2
	v_cvt_pk_fp8_f32 v12, v4, v2 op_sel:[0,0,1]
	v_mul_f32_e32 v2, 0x41800000, v24
	v_cvt_pk_fp8_f32 v13, v23, v2 op_sel:[0,0,1]
	v_add_u32_e32 v32, 0x80, v22
	v_mad_i64_i32 v[2:3], s[28:29], v32, s51, v[16:17]
	v_permlane16_swap_b32_e32 v10, v12
	v_permlane16_swap_b32_e32 v11, v13
	v_lshl_add_u64 v[2:3], v[2:3], 0, s[14:15]
	global_store_dwordx4 v[6:7], v[10:13], off offset:128
	v_lshl_add_u64 v[4:5], v[2:3], 0, v[18:19]
	global_load_dwordx4 v[24:27], v[4:5], off
	v_lshl_add_u64 v[2:3], v[2:3], 0, v[20:21]
	global_load_dwordx4 v[28:31], v[2:3], off
	v_add_u32_e32 v2, 0x90, v22
	v_mad_i64_i32 v[2:3], s[28:29], v2, s51, v[16:17]
	v_lshl_add_u64 v[2:3], v[2:3], 0, s[14:15]
	v_lshl_add_u64 v[4:5], v[2:3], 0, v[18:19]
	v_lshl_add_u64 v[2:3], v[2:3], 0, v[20:21]
	global_load_dwordx4 v[98:101], v[4:5], off
	global_load_dwordx4 v[102:105], v[2:3], off
	v_add_u32_e32 v2, 0xa0, v22
	v_mad_i64_i32 v[2:3], s[28:29], v2, s51, v[16:17]
	v_lshl_add_u64 v[2:3], v[2:3], 0, s[14:15]
	v_lshl_add_u64 v[4:5], v[2:3], 0, v[18:19]
	v_lshl_add_u64 v[2:3], v[2:3], 0, v[20:21]
	global_load_dwordx4 v[106:109], v[4:5], off
	global_load_dwordx4 v[10:13], v[2:3], off
	v_add_u32_e32 v2, 0xb0, v22
	v_mad_i64_i32 v[2:3], s[28:29], v2, s51, v[16:17]
	v_lshl_add_u64 v[2:3], v[2:3], 0, s[14:15]
	v_lshl_add_u64 v[4:5], v[2:3], 0, v[18:19]
	v_pk_mul_f32 v[18:19], v[86:87], s[16:17] op_sel_hi:[1,0]
	v_pk_mul_f32 v[16:17], v[88:89], s[16:17] op_sel_hi:[1,0]
	v_pk_mul_f32 v[22:23], v[82:83], s[16:17] op_sel_hi:[1,0]
	v_lshl_add_u64 v[2:3], v[2:3], 0, v[20:21]
	v_pk_mul_f32 v[20:21], v[84:85], s[16:17] op_sel_hi:[1,0]
	global_load_dwordx4 v[6:9], v[4:5], off
	s_nop 0
	global_load_dwordx4 v[2:5], v[2:3], off
	s_waitcnt vmcnt(7)
	v_lshlrev_b32_e32 v33, 16, v24
	v_and_b32_e32 v24, 0xffff0000, v24
	v_mul_f32_e32 v19, v19, v24
	v_lshlrev_b32_e32 v24, 16, v25
	v_mul_f32_e32 v16, v16, v24
	v_and_b32_e32 v24, 0xffff0000, v25
	v_mul_f32_e32 v17, v17, v24
	v_lshlrev_b32_e32 v24, 16, v26
	v_mul_f32_e32 v22, v22, v24
	v_and_b32_e32 v24, 0xffff0000, v26
	v_mul_f32_e32 v23, v23, v24
	v_lshlrev_b32_e32 v24, 16, v27
	v_mul_f32_e32 v18, v18, v33
	v_mul_f32_e32 v20, v20, v24
	v_and_b32_e32 v24, 0xffff0000, v27
	v_mul_f32_e32 v21, v21, v24
	v_mul_f32_e32 v18, 0x41800000, v18
	v_mul_f32_e32 v19, 0x41800000, v19
	v_mul_f32_e32 v24, 0x41800000, v16
	v_mov_b32_e32 v16, 0
	v_mul_f32_e32 v25, 0x41800000, v17
	v_cvt_pk_fp8_f32 v16, v18, v19
	v_mul_f32_e32 v18, 0x41800000, v22
	v_mul_f32_e32 v19, 0x41800000, v23
	v_mov_b32_e32 v17, 0
	v_cvt_pk_fp8_f32 v17, v18, v19
	v_mul_f32_e32 v18, 0x41800000, v20
	v_mul_f32_e32 v19, 0x41800000, v21
	v_pk_mul_f32 v[20:21], v[94:95], s[16:17] op_sel_hi:[1,0]
	s_waitcnt vmcnt(6)
	v_lshlrev_b32_e32 v26, 16, v28
	v_mul_f32_e32 v20, v20, v26
	v_and_b32_e32 v26, 0xffff0000, v28
	v_cvt_pk_fp8_f32 v17, v18, v19 op_sel:[0,0,1]
	v_pk_mul_f32 v[18:19], v[96:97], s[16:17] op_sel_hi:[1,0]
	v_mul_f32_e32 v21, v21, v26
	v_lshlrev_b32_e32 v26, 16, v29
	v_mul_f32_e32 v18, v18, v26
	v_and_b32_e32 v26, 0xffff0000, v29
	v_cvt_pk_fp8_f32 v16, v24, v25 op_sel:[0,0,1]
	v_pk_mul_f32 v[24:25], v[90:91], s[16:17] op_sel_hi:[1,0]
	v_mul_f32_e32 v19, v19, v26
	v_lshlrev_b32_e32 v26, 16, v30
	v_mul_f32_e32 v24, v24, v26
	v_and_b32_e32 v26, 0xffff0000, v30
	v_pk_mul_f32 v[22:23], v[92:93], s[16:17] op_sel_hi:[1,0]
	v_mul_f32_e32 v25, v25, v26
	v_lshlrev_b32_e32 v26, 16, v31
	v_mul_f32_e32 v22, v22, v26
	v_and_b32_e32 v26, 0xffff0000, v31
	v_mul_f32_e32 v23, v23, v26
	v_mul_f32_e32 v26, 0x41800000, v20
	v_mul_f32_e32 v21, 0x41800000, v21
	v_mov_b32_e32 v20, 0
	v_cvt_pk_fp8_f32 v20, v26, v21
	v_mul_f32_e32 v24, 0x41800000, v24
	v_mul_f32_e32 v25, 0x41800000, v25
	v_mov_b32_e32 v21, 0
	v_cvt_pk_fp8_f32 v21, v24, v25
	v_mul_f32_e32 v18, 0x41800000, v18
	v_mul_f32_e32 v19, 0x41800000, v19
	v_cvt_pk_fp8_f32 v20, v18, v19 op_sel:[0,0,1]
	v_mul_f32_e32 v18, 0x41800000, v22
	v_mul_f32_e32 v19, 0x41800000, v23
	v_cvt_pk_fp8_f32 v21, v18, v19 op_sel:[0,0,1]
	v_or_b32_e32 v18, v32, v192
	v_ashrrev_i32_e32 v19, 31, v18
	v_lshlrev_b64 v[22:23], 11, v[18:19]
	v_pk_mul_f32 v[18:19], v[72:73], s[16:17] op_sel_hi:[1,0]
	s_waitcnt vmcnt(5)
	v_lshlrev_b32_e32 v26, 16, v101
	v_mul_f32_e32 v18, v18, v26
	v_mul_f32_e32 v28, 0x41800000, v18
	v_and_b32_e32 v18, 0xffff0000, v101
	v_pk_mul_f32 v[24:25], v[70:71], s[16:17] op_sel_hi:[1,0]
	v_mul_f32_e32 v29, v19, v18
	v_lshlrev_b32_e32 v18, 16, v100
	v_and_b32_e32 v19, 0xffff0000, v100
	v_mul_f32_e32 v18, v24, v18
	v_mul_f32_e32 v19, v25, v19
	v_mul_f32_e32 v18, 0x41800000, v18
	v_mul_f32_e32 v24, 0x41800000, v19
	v_mov_b32_e32 v19, 0
	v_cvt_pk_fp8_f32 v19, v18, v24
	v_pk_mul_f32 v[24:25], v[68:69], s[16:17] op_sel_hi:[1,0]
	v_lshlrev_b32_e32 v18, 16, v99
	v_mul_f32_e32 v18, v24, v18
	v_pk_mul_f32 v[26:27], v[66:67], s[16:17] op_sel_hi:[1,0]
	v_mul_f32_e32 v24, 0x41800000, v18
	v_lshlrev_b32_e32 v18, 16, v98
	v_mul_f32_e32 v18, v26, v18
	v_mul_f32_e32 v26, 0x41800000, v18
	v_and_b32_e32 v18, 0xffff0000, v98
	v_mul_f32_e32 v18, v27, v18
	v_mul_f32_e32 v27, 0x41800000, v18
	v_mov_b32_e32 v18, 0
	v_cvt_pk_fp8_f32 v18, v26, v27
	v_and_b32_e32 v26, 0xffff0000, v99
	v_mul_f32_e32 v25, v25, v26
	v_mul_f32_e32 v25, 0x41800000, v25
	v_cvt_pk_fp8_f32 v18, v24, v25 op_sel:[0,0,1]
	v_mul_f32_e32 v24, 0x41800000, v29
	v_cvt_pk_fp8_f32 v19, v28, v24 op_sel:[0,0,1]
	v_lshl_add_u64 v[22:23], s[8:9], 0, v[22:23]
	v_lshl_add_u64 v[22:23], v[22:23], 0, v[14:15]
	v_permlane16_swap_b32_e32 v16, v18
	v_permlane16_swap_b32_e32 v17, v19
	v_lshl_add_u64 v[24:25], v[22:23], 0, v[174:175]
	global_store_dwordx4 v[24:25], v[16:19], off
	s_waitcnt vmcnt(5)
	v_lshlrev_b32_e32 v22, 16, v105
	v_mov_b32_e32 v23, 0
	v_pk_mul_f32 v[16:17], v[80:81], s[16:17] op_sel_hi:[1,0]
	v_pk_mul_f32 v[18:19], v[78:79], s[16:17] op_sel_hi:[1,0]
	v_mul_f32_e32 v16, v16, v22
	v_mul_f32_e32 v26, 0x41800000, v16
	v_and_b32_e32 v16, 0xffff0000, v105
	v_mul_f32_e32 v27, v17, v16
	v_lshlrev_b32_e32 v16, 16, v104
	v_and_b32_e32 v17, 0xffff0000, v104
	v_mul_f32_e32 v16, v18, v16
	v_mul_f32_e32 v17, v19, v17
	v_mul_f32_e32 v16, 0x41800000, v16
	v_mul_f32_e32 v17, 0x41800000, v17
	v_cvt_pk_fp8_f32 v23, v16, v17
	v_pk_mul_f32 v[16:17], v[76:77], s[16:17] op_sel_hi:[1,0]
	v_lshlrev_b32_e32 v22, 16, v103
	v_pk_mul_f32 v[18:19], v[74:75], s[16:17] op_sel_hi:[1,0]
	v_mul_f32_e32 v16, v16, v22
	v_lshlrev_b32_e32 v22, 16, v102
	v_mul_f32_e32 v18, v18, v22
	v_and_b32_e32 v22, 0xffff0000, v102
	v_mul_f32_e32 v19, v19, v22
	v_mul_f32_e32 v18, 0x41800000, v18
	v_mul_f32_e32 v19, 0x41800000, v19
	v_mov_b32_e32 v22, 0
	v_cvt_pk_fp8_f32 v22, v18, v19
	v_and_b32_e32 v18, 0xffff0000, v103
	v_mul_f32_e32 v17, v17, v18
	v_mul_f32_e32 v16, 0x41800000, v16
	v_mul_f32_e32 v17, 0x41800000, v17
	v_cvt_pk_fp8_f32 v22, v16, v17 op_sel:[0,0,1]
	v_mul_f32_e32 v16, 0x41800000, v27
	v_cvt_pk_fp8_f32 v23, v26, v16 op_sel:[0,0,1]
	v_pk_mul_f32 v[18:19], v[54:55], s[16:17] op_sel_hi:[1,0]
	v_permlane16_swap_b32_e32 v20, v22
	v_permlane16_swap_b32_e32 v21, v23
	global_store_dwordx4 v[24:25], v[20:23], off offset:128
	s_waitcnt vmcnt(5)
	v_lshlrev_b32_e32 v24, 16, v106
	v_mul_f32_e32 v18, v18, v24
	v_and_b32_e32 v24, 0xffff0000, v106
	v_pk_mul_f32 v[16:17], v[56:57], s[16:17] op_sel_hi:[1,0]
	v_mul_f32_e32 v19, v19, v24
	v_lshlrev_b32_e32 v24, 16, v107
	v_mul_f32_e32 v16, v16, v24
	v_and_b32_e32 v24, 0xffff0000, v107
	v_pk_mul_f32 v[22:23], v[50:51], s[16:17] op_sel_hi:[1,0]
	v_mul_f32_e32 v17, v17, v24
	v_lshlrev_b32_e32 v24, 16, v108
	v_mul_f32_e32 v22, v22, v24
	v_and_b32_e32 v24, 0xffff0000, v108
	v_pk_mul_f32 v[20:21], v[52:53], s[16:17] op_sel_hi:[1,0]
	v_mul_f32_e32 v23, v23, v24
	v_lshlrev_b32_e32 v24, 16, v109
	v_mul_f32_e32 v20, v20, v24
	v_and_b32_e32 v24, 0xffff0000, v109
	v_mul_f32_e32 v21, v21, v24
	v_mul_f32_e32 v18, 0x41800000, v18
	v_mul_f32_e32 v19, 0x41800000, v19
	v_mul_f32_e32 v24, 0x41800000, v16
	v_mov_b32_e32 v16, 0
	v_mul_f32_e32 v25, 0x41800000, v17
	v_cvt_pk_fp8_f32 v16, v18, v19
	v_mul_f32_e32 v18, 0x41800000, v22
	v_mul_f32_e32 v19, 0x41800000, v23
	v_mov_b32_e32 v17, 0
	v_cvt_pk_fp8_f32 v17, v18, v19
	v_mul_f32_e32 v18, 0x41800000, v20
	v_mul_f32_e32 v19, 0x41800000, v21
	v_pk_mul_f32 v[20:21], v[62:63], s[16:17] op_sel_hi:[1,0]
	s_waitcnt vmcnt(4)
	v_lshlrev_b32_e32 v26, 16, v10
	v_and_b32_e32 v10, 0xffff0000, v10
	v_cvt_pk_fp8_f32 v17, v18, v19 op_sel:[0,0,1]
	v_pk_mul_f32 v[18:19], v[64:65], s[16:17] op_sel_hi:[1,0]
	v_mul_f32_e32 v10, v21, v10
	v_lshlrev_b32_e32 v21, 16, v11
	v_pk_mul_f32 v[22:23], v[60:61], s[16:17] op_sel_hi:[1,0]
	v_mul_f32_e32 v20, v20, v26
	v_mul_f32_e32 v18, v18, v21
	v_lshlrev_b32_e32 v21, 16, v13
	v_mul_f32_e32 v21, v22, v21
	v_mul_f32_e32 v20, 0x41800000, v20
	v_mul_f32_e32 v22, 0x41800000, v10
	v_mov_b32_e32 v10, 0
	v_and_b32_e32 v11, 0xffff0000, v11
	v_cvt_pk_fp8_f32 v10, v20, v22
	v_cvt_pk_fp8_f32 v16, v24, v25 op_sel:[0,0,1]
	v_pk_mul_f32 v[24:25], v[58:59], s[16:17] op_sel_hi:[1,0]
	v_mul_f32_e32 v11, v19, v11
	v_lshlrev_b32_e32 v19, 16, v12
	v_and_b32_e32 v12, 0xffff0000, v12
	v_mul_f32_e32 v19, v24, v19
	v_mul_f32_e32 v12, v25, v12
	v_and_b32_e32 v13, 0xffff0000, v13
	v_mul_f32_e32 v13, v23, v13
	v_mul_f32_e32 v18, 0x41800000, v18
	v_mul_f32_e32 v23, 0x41800000, v11
	v_mul_f32_e32 v19, 0x41800000, v19
	v_mul_f32_e32 v12, 0x41800000, v12
	v_mov_b32_e32 v11, 0
	v_cvt_pk_fp8_f32 v11, v19, v12
	v_cvt_pk_fp8_f32 v10, v18, v23 op_sel:[0,0,1]
	v_pk_mul_f32 v[18:19], v[40:41], s[16:17] op_sel_hi:[1,0]
	s_waitcnt vmcnt(3)
	v_lshlrev_b32_e32 v22, 16, v9
	v_and_b32_e32 v9, 0xffff0000, v9
	v_mul_f32_e32 v12, 0x41800000, v21
	v_pk_mul_f32 v[20:21], v[38:39], s[16:17] op_sel_hi:[1,0]
	v_mul_f32_e32 v23, v19, v9
	v_lshlrev_b32_e32 v9, 16, v8
	v_and_b32_e32 v8, 0xffff0000, v8
	v_mul_f32_e32 v9, v20, v9
	v_mul_f32_e32 v8, v21, v8
	v_mul_f32_e32 v18, v18, v22
	v_mul_f32_e32 v9, 0x41800000, v9
	v_mul_f32_e32 v8, 0x41800000, v8
	v_mov_b32_e32 v19, 0
	v_mul_f32_e32 v22, 0x41800000, v18
	v_cvt_pk_fp8_f32 v19, v9, v8
	v_pk_mul_f32 v[8:9], v[36:37], s[16:17] op_sel_hi:[1,0]
	v_lshlrev_b32_e32 v18, 16, v7
	v_pk_mul_f32 v[20:21], v[34:35], s[16:17] op_sel_hi:[1,0]
	v_mul_f32_e32 v8, v8, v18
	v_lshlrev_b32_e32 v18, 16, v6
	v_and_b32_e32 v6, 0xffff0000, v6
	v_mul_f32_e32 v18, v20, v18
	v_mul_f32_e32 v6, v21, v6
	v_mul_f32_e32 v20, 0x41800000, v18
	v_mul_f32_e32 v6, 0x41800000, v6
	v_mov_b32_e32 v18, 0
	v_cvt_pk_fp8_f32 v18, v20, v6
	v_mul_f32_e32 v13, 0x41800000, v13
	v_and_b32_e32 v6, 0xffff0000, v7
	v_cvt_pk_fp8_f32 v11, v12, v13 op_sel:[0,0,1]
	v_or_b32_e32 v12, v32, v193
	v_mul_f32_e32 v6, v9, v6
	v_ashrrev_i32_e32 v13, 31, v12
	v_mul_f32_e32 v8, 0x41800000, v8
	v_mul_f32_e32 v6, 0x41800000, v6
	v_lshlrev_b64 v[12:13], 11, v[12:13]
	v_cvt_pk_fp8_f32 v18, v8, v6 op_sel:[0,0,1]
	v_mul_f32_e32 v6, 0x41800000, v23
	v_cvt_pk_fp8_f32 v19, v22, v6 op_sel:[0,0,1]
	v_lshl_add_u64 v[6:7], s[8:9], 0, v[12:13]
	v_lshl_add_u64 v[6:7], v[6:7], 0, v[14:15]
	v_pk_mul_f32 v[8:9], v[48:49], s[16:17] op_sel_hi:[1,0]
	s_waitcnt vmcnt(2)
	v_lshlrev_b32_e32 v14, 16, v5
	v_and_b32_e32 v5, 0xffff0000, v5
	v_pk_mul_f32 v[12:13], v[46:47], s[16:17] op_sel_hi:[1,0]
	v_mul_f32_e32 v15, v9, v5
	v_lshlrev_b32_e32 v5, 16, v4
	v_and_b32_e32 v4, 0xffff0000, v4
	v_mul_f32_e32 v5, v12, v5
	v_mul_f32_e32 v4, v13, v4
	v_mul_f32_e32 v5, 0x41800000, v5
	v_mul_f32_e32 v4, 0x41800000, v4
	v_mov_b32_e32 v13, 0
	v_mul_f32_e32 v8, v8, v14
	v_cvt_pk_fp8_f32 v13, v5, v4
	v_pk_mul_f32 v[4:5], v[44:45], s[16:17] op_sel_hi:[1,0]
	v_lshlrev_b32_e32 v12, 16, v3
	v_mul_f32_e32 v14, 0x41800000, v8
	v_pk_mul_f32 v[8:9], v[42:43], s[16:17] op_sel_hi:[1,0]
	v_mul_f32_e32 v4, v4, v12
	v_lshlrev_b32_e32 v12, 16, v2
	v_and_b32_e32 v2, 0xffff0000, v2
	v_mul_f32_e32 v8, v8, v12
	v_mul_f32_e32 v2, v9, v2
	v_mul_f32_e32 v8, 0x41800000, v8
	v_mul_f32_e32 v2, 0x41800000, v2
	v_mov_b32_e32 v12, 0
	v_cvt_pk_fp8_f32 v12, v8, v2
	v_and_b32_e32 v2, 0xffff0000, v3
	v_mul_f32_e32 v2, v5, v2
	v_mul_f32_e32 v4, 0x41800000, v4
	v_mul_f32_e32 v2, 0x41800000, v2
	v_cvt_pk_fp8_f32 v12, v4, v2 op_sel:[0,0,1]
	v_mul_f32_e32 v2, 0x41800000, v15
	v_cvt_pk_fp8_f32 v13, v14, v2 op_sel:[0,0,1]
	v_permlane16_swap_b32_e32 v16, v18
	v_permlane16_swap_b32_e32 v17, v19
	v_lshl_add_u64 v[6:7], v[6:7], 0, v[174:175]
	v_permlane16_swap_b32_e32 v10, v12
	v_permlane16_swap_b32_e32 v11, v13
	global_store_dwordx4 v[6:7], v[16:19], off
	global_store_dwordx4 v[6:7], v[10:13], off offset:128
	s_cbranch_vccnz .LBB0_522
	s_andn2_b64 vcc, exec, s[4:5]
	s_cbranch_vccnz .LBB0_521
	s_barrier
	s_branch .LBB0_521

.LBB0_553:
	s_ashr_i32 s19, s18, 31
	s_lshl_b64 s[22:23], s[18:19], 18
	s_add_u32 s22, s38, s22
	s_addc_u32 s23, s39, s23
	s_and_b64 s[24:25], s[34:35], exec
	s_cselect_b32 s19, s23, s29
	s_cselect_b32 s53, s22, s28
	s_ashr_i32 s21, s20, 31
	s_lshl_b64 s[24:25], s[20:21], 18
	s_add_u32 s24, s40, s24
	s_addc_u32 s25, s41, s25
	s_and_b64 s[34:35], s[34:35], exec
	s_cselect_b32 s21, s25, s31
	s_cselect_b32 s54, s24, s30
	s_add_u32 s55, s30, 0x100
	v_mov_b32_e32 v42, 0
	s_addc_u32 s56, s31, 0
	s_mov_b32 s57, -2
	v_mov_b64_e32 v[34:35], 0
	v_mov_b64_e32 v[36:37], 0
	v_mov_b64_e32 v[38:39], 0
	v_mov_b64_e32 v[40:41], 0
	v_mov_b32_e32 v43, v42
	v_mov_b64_e32 v[44:45], 0
	v_mov_b64_e32 v[46:47], 0
	v_mov_b64_e32 v[48:49], 0
	v_mov_b64_e32 v[50:51], 0
	v_mov_b64_e32 v[52:53], 0
	v_mov_b64_e32 v[54:55], 0
	v_mov_b64_e32 v[56:57], 0
	v_mov_b64_e32 v[58:59], 0
	v_mov_b64_e32 v[60:61], 0
	v_mov_b64_e32 v[62:63], 0
	v_mov_b64_e32 v[64:65], 0
	v_mov_b64_e32 v[66:67], 0
	v_mov_b64_e32 v[68:69], 0
	v_mov_b64_e32 v[70:71], 0
	v_mov_b64_e32 v[72:73], 0
	v_mov_b64_e32 v[74:75], 0
	v_mov_b64_e32 v[76:77], 0
	v_mov_b64_e32 v[78:79], 0
	v_mov_b64_e32 v[80:81], 0
	v_mov_b64_e32 v[82:83], 0
	v_mov_b64_e32 v[84:85], 0
	v_mov_b64_e32 v[86:87], 0
	v_mov_b64_e32 v[88:89], 0
	v_mov_b64_e32 v[90:91], 0
	v_mov_b64_e32 v[92:93], 0
	v_mov_b64_e32 v[94:95], 0
	v_mov_b64_e32 v[96:97], 0
	v_mov_b64_e32 v[98:99], 0
	v_mov_b64_e32 v[100:101], 0
	v_mov_b64_e32 v[102:103], 0
	v_mov_b64_e32 v[104:105], 0
	v_mov_b64_e32 v[106:107], 0
	v_mov_b64_e32 v[108:109], 0
	v_mov_b64_e32 v[110:111], 0
	v_mov_b64_e32 v[112:113], 0
	v_mov_b64_e32 v[114:115], 0
	v_mov_b64_e32 v[116:117], 0
	v_mov_b64_e32 v[118:119], 0
	v_mov_b64_e32 v[120:121], 0
	v_mov_b64_e32 v[122:123], 0
	v_mov_b64_e32 v[124:125], 0
	v_mov_b64_e32 v[126:127], 0
	v_mov_b64_e32 v[128:129], 0
	v_mov_b64_e32 v[130:131], 0
	v_mov_b64_e32 v[132:133], 0
	v_mov_b64_e32 v[134:135], 0
	v_mov_b64_e32 v[136:137], 0
	v_mov_b64_e32 v[138:139], 0
	v_mov_b64_e32 v[140:141], 0
	v_mov_b64_e32 v[142:143], 0
	v_mov_b64_e32 v[144:145], 0
	v_mov_b64_e32 v[146:147], 0
	v_mov_b64_e32 v[148:149], 0
	v_mov_b64_e32 v[150:151], 0
	v_mov_b64_e32 v[152:153], 0
	v_mov_b64_e32 v[154:155], 0
	v_mov_b64_e32 v[156:157], 0
	v_mov_b64_e32 v[158:159], 0
	v_mov_b64_e32 v[160:161], 0

.LBB0_557:
	v_lshl_or_b32 v30, s52, 8, v196
	v_lshl_add_u32 v32, s26, 8, v192
	v_mov_b64_e32 v[184:185], s[88:89]
	v_or_b32_e32 v6, 0x80, v30
	v_ashrrev_i32_e32 v31, 31, v30
	v_mad_i64_i32 v[2:3], s[28:29], v32, s51, v[184:185]
	v_ashrrev_i32_e32 v7, 31, v6
	v_lshl_add_u64 v[2:3], v[2:3], 0, s[14:15]
	v_lshlrev_b64 v[186:187], 1, v[30:31]
	v_pk_mul_f32 v[214:215], v[154:155], s[16:17] op_sel_hi:[1,0]
	v_lshlrev_b64 v[154:155], 1, v[6:7]
	s_nop 11
	v_lshl_add_u64 v[4:5], v[2:3], 0, v[186:187]
	v_ashrrev_i32_e32 v33, 31, v32
	v_lshl_add_u64 v[2:3], v[2:3], 0, v[154:155]
	global_load_dwordx4 v[200:203], v[4:5], off
	global_load_dwordx4 v[204:207], v[2:3], off
	v_lshlrev_b64 v[4:5], 11, v[32:33]
	v_lshl_add_u64 v[4:5], s[8:9], 0, v[4:5]
	v_lshl_add_u64 v[4:5], v[4:5], 0, v[30:31]
	global_load_dwordx2 v[26:27], v[4:5], off
	global_load_dwordx2 v[224:225], v[4:5], off offset:128
	v_or_b32_e32 v8, 16, v32
	v_or_b32_e32 v10, 32, v32
	v_or_b32_e32 v12, 48, v32
	v_ashrrev_i32_e32 v9, 31, v8
	v_ashrrev_i32_e32 v11, 31, v10
	v_mad_i64_i32 v[14:15], s[28:29], v8, s51, v[184:185]
	v_mad_i64_i32 v[16:17], s[28:29], v10, s51, v[184:185]
	v_ashrrev_i32_e32 v13, 31, v12
	v_mad_i64_i32 v[18:19], s[28:29], v12, s51, v[184:185]
	v_lshlrev_b64 v[8:9], 11, v[8:9]
	v_lshlrev_b64 v[10:11], 11, v[10:11]
	v_lshl_add_u64 v[6:7], v[14:15], 0, s[14:15]
	v_lshl_add_u64 v[14:15], v[16:17], 0, s[14:15]
	v_lshl_add_u64 v[16:17], v[18:19], 0, s[14:15]
	v_lshlrev_b64 v[12:13], 11, v[12:13]
	v_lshl_add_u64 v[8:9], s[8:9], 0, v[8:9]
	v_lshl_add_u64 v[10:11], s[8:9], 0, v[10:11]
	v_pk_mul_f32 v[210:211], v[158:159], s[16:17] op_sel_hi:[1,0]
	v_pk_mul_f32 v[212:213], v[156:157], s[16:17] op_sel_hi:[1,0]
	v_lshl_add_u64 v[18:19], v[6:7], 0, v[186:187]
	v_lshl_add_u64 v[6:7], v[6:7], 0, v[154:155]
	v_lshl_add_u64 v[156:157], v[14:15], 0, v[186:187]
	v_lshl_add_u64 v[158:159], v[14:15], 0, v[154:155]
	v_lshl_add_u64 v[12:13], s[8:9], 0, v[12:13]
	v_lshl_add_u64 v[2:3], v[16:17], 0, v[186:187]
	v_lshl_add_u64 v[4:5], v[8:9], 0, v[30:31]
	v_lshl_add_u64 v[8:9], v[10:11], 0, v[30:31]
	v_pk_mul_f32 v[208:209], v[160:161], s[16:17] op_sel_hi:[1,0]
	v_lshl_add_u64 v[222:223], v[16:17], 0, v[154:155]
	v_lshl_add_u64 v[226:227], v[12:13], 0, v[30:31]
	global_load_dwordx4 v[22:25], v[18:19], off
	global_load_dwordx2 v[190:191], v[4:5], off
	s_nop 0
	global_load_dwordx4 v[18:21], v[6:7], off
	global_load_dwordx2 v[28:29], v[4:5], off offset:128
	global_load_dwordx4 v[14:17], v[156:157], off
	global_load_dwordx2 v[188:189], v[8:9], off
	global_load_dwordx4 v[10:13], v[158:159], off
	global_load_dwordx2 v[160:161], v[8:9], off offset:128
	s_nop 0
	global_load_dwordx4 v[6:9], v[2:3], off
	global_load_dwordx2 v[158:159], v[226:227], off
	s_nop 0
	global_load_dwordx4 v[2:5], v[222:223], off
	global_load_dwordx2 v[156:157], v[226:227], off offset:128
	v_mov_b32_e32 v219, v183
	v_mov_b32_e32 v220, v210
	v_mov_b32_e32 v210, v208
	v_mov_b32_e32 v217, v183
	v_mov_b32_e32 v223, v183
	v_mov_b32_e32 v227, v183
	v_pk_mul_f32 v[150:151], v[150:151], s[16:17] op_sel_hi:[1,0]
	v_pk_mul_f32 v[146:147], v[146:147], s[16:17] op_sel_hi:[1,0]
	v_pk_mul_f32 v[148:149], v[148:149], s[16:17] op_sel_hi:[1,0]
	v_pk_mul_f32 v[144:145], v[144:145], s[16:17] op_sel_hi:[1,0]
	v_pk_mul_f32 v[142:143], v[142:143], s[16:17] op_sel_hi:[1,0]
	v_pk_mul_f32 v[138:139], v[138:139], s[16:17] op_sel_hi:[1,0]
	v_pk_mul_f32 v[134:135], v[134:135], s[16:17] op_sel_hi:[1,0]
	v_pk_mul_f32 v[130:131], v[130:131], s[16:17] op_sel_hi:[1,0]
	v_pk_mul_f32 v[94:95], v[94:95], s[16:17] op_sel_hi:[1,0]
	v_pk_mul_f32 v[96:97], v[96:97], s[16:17] op_sel_hi:[1,0]
	v_pk_mul_f32 v[90:91], v[90:91], s[16:17] op_sel_hi:[1,0]
	v_pk_mul_f32 v[92:93], v[92:93], s[16:17] op_sel_hi:[1,0]
	v_pk_mul_f32 v[86:87], v[86:87], s[16:17] op_sel_hi:[1,0]
	v_pk_mul_f32 v[82:83], v[82:83], s[16:17] op_sel_hi:[1,0]
	v_pk_mul_f32 v[84:85], v[84:85], s[16:17] op_sel_hi:[1,0]
	v_pk_mul_f32 v[80:81], v[80:81], s[16:17] op_sel_hi:[1,0]
	v_pk_mul_f32 v[78:79], v[78:79], s[16:17] op_sel_hi:[1,0]
	v_pk_mul_f32 v[70:71], v[70:71], s[16:17] op_sel_hi:[1,0]
	v_pk_mul_f32 v[66:67], v[66:67], s[16:17] op_sel_hi:[1,0]
	s_and_b64 vcc, exec, s[6:7]
	s_mov_b64 s[6:7], -1
	s_waitcnt vmcnt(0)
	v_lshlrev_b32_e32 v182, 16, v200
	v_and_b32_e32 v216, 0xffff0000, v200
	v_lshlrev_b32_e32 v218, 16, v201
	v_and_b32_e32 v200, 0xffff0000, v201
	v_mov_b32_e32 v201, v183
	v_cvt_pk_f32_fp8_e32 v[228:229], v26
	v_cvt_pk_f32_fp8_sdwa v[230:231], v26 src0_sel:WORD_1
	v_cvt_pk_f32_fp8_e32 v[232:233], v27
	v_cvt_pk_f32_fp8_sdwa v[26:27], v27 src0_sel:WORD_1
	v_mov_b32_e32 v221, v228
	v_mov_b32_e32 v228, v211
	v_mov_b32_e32 v211, v230
	v_mov_b32_e32 v230, v209
	v_pk_mul_f32 v[210:211], v[210:211], v[218:219]
	v_pk_mul_f32 v[200:201], v[230:231], v[200:201]
	v_lshlrev_b32_e32 v208, 16, v202
	v_add_f32_e32 v210, v210, v211
	v_add_f32_e32 v211, v200, v201
	v_mov_b32_e32 v200, v214
	v_mov_b32_e32 v201, v232
	v_mov_b32_e32 v209, v183
	v_and_b32_e32 v202, 0xffff0000, v202
	v_lshlrev_b32_e32 v222, 16, v203
	v_and_b32_e32 v226, 0xffff0000, v203
	v_pk_mul_f32 v[200:201], v[200:201], v[208:209]
	v_mov_b32_e32 v232, v215
	v_mov_b32_e32 v203, v183
	v_add_f32_e32 v208, v200, v201
	v_pk_mul_f32 v[200:201], v[232:233], v[202:203]
	v_pk_mul_f32 v[220:221], v[220:221], v[182:183]
	v_pk_mul_f32 v[216:217], v[228:229], v[216:217]
	v_add_f32_e32 v202, v200, v201
	v_mov_b32_e32 v200, v212
	v_mov_b32_e32 v201, v26
	v_mov_b32_e32 v26, v213
	v_add_f32_e32 v33, v220, v221
	v_add_f32_e32 v182, v216, v217
	v_pk_mul_f32 v[200:201], v[200:201], v[222:223]
	v_pk_mul_f32 v[26:27], v[26:27], v[226:227]
	v_add_f32_e32 v203, v200, v201
	v_add_f32_e32 v26, v26, v27
	v_mul_f32_e32 v27, 0x41800000, v33
	v_mul_f32_e32 v33, 0x41800000, v182
	v_mov_b32_e32 v200, 0
	v_cvt_pk_fp8_f32 v200, v27, v33
	v_mul_f32_e32 v27, 0x41800000, v208
	v_mul_f32_e32 v33, 0x41800000, v202
	v_mov_b32_e32 v201, 0
	v_cvt_pk_fp8_f32 v201, v27, v33
	v_cvt_pk_f32_fp8_e32 v[214:215], v224
	v_cvt_pk_f32_fp8_sdwa v[216:217], v224 src0_sel:WORD_1
	v_mul_f32_e32 v27, 0x41800000, v203
	v_mul_f32_e32 v26, 0x41800000, v26
	v_cvt_pk_fp8_f32 v201, v27, v26 op_sel:[0,0,1]
	v_pk_mul_f32 v[26:27], v[152:153], s[16:17] op_sel_hi:[1,0]
	v_and_b32_e32 v152, 0xffff0000, v204
	v_cvt_pk_f32_fp8_e32 v[218:219], v225
	v_mov_b32_e32 v223, v214
	v_mov_b32_e32 v214, v151
	v_mov_b32_e32 v153, v183
	v_mul_f32_e32 v182, 0x41800000, v210
	v_mul_f32_e32 v209, 0x41800000, v211
	v_mov_b32_e32 v222, v150
	v_pk_mul_f32 v[150:151], v[214:215], v[152:153]
	v_cvt_pk_fp8_f32 v200, v182, v209 op_sel:[0,0,1]
	v_lshlrev_b32_e32 v182, 16, v204
	v_lshlrev_b32_e32 v202, 16, v205
	v_and_b32_e32 v204, 0xffff0000, v205
	v_add_f32_e32 v152, v150, v151
	v_mov_b32_e32 v150, v26
	v_mov_b32_e32 v151, v216
	v_mov_b32_e32 v203, v183
	v_mov_b32_e32 v216, v27
	v_mov_b32_e32 v205, v183
	v_cvt_pk_f32_fp8_sdwa v[220:221], v225 src0_sel:WORD_1
	v_pk_mul_f32 v[150:151], v[150:151], v[202:203]
	v_pk_mul_f32 v[26:27], v[216:217], v[204:205]
	v_lshlrev_b32_e32 v208, 16, v206
	v_add_f32_e32 v150, v150, v151
	v_add_f32_e32 v151, v26, v27
	v_mov_b32_e32 v26, v146
	v_mov_b32_e32 v27, v218
	v_mov_b32_e32 v209, v183
	v_and_b32_e32 v206, 0xffff0000, v206
	v_lshlrev_b32_e32 v210, 16, v207
	v_and_b32_e32 v212, 0xffff0000, v207
	v_pk_mul_f32 v[26:27], v[26:27], v[208:209]
	v_mov_b32_e32 v218, v147
	v_mov_b32_e32 v207, v183
	v_add_f32_e32 v146, v26, v27
	v_pk_mul_f32 v[26:27], v[218:219], v[206:207]
	v_mov_b32_e32 v211, v183
	v_add_f32_e32 v147, v26, v27
	v_mov_b32_e32 v26, v148
	v_mov_b32_e32 v27, v220
	v_pk_mul_f32 v[222:223], v[222:223], v[182:183]
	v_pk_mul_f32 v[26:27], v[26:27], v[210:211]
	v_mov_b32_e32 v220, v149
	v_mov_b32_e32 v213, v183
	v_add_f32_e32 v33, v222, v223
	v_add_f32_e32 v148, v26, v27
	v_pk_mul_f32 v[26:27], v[220:221], v[212:213]
	v_mul_f32_e32 v150, 0x41800000, v150
	v_add_f32_e32 v149, v26, v27
	v_mul_f32_e32 v27, 0x41800000, v33
	v_mul_f32_e32 v33, 0x41800000, v152
	v_mov_b32_e32 v26, 0
	v_cvt_pk_fp8_f32 v26, v27, v33
	v_mul_f32_e32 v33, 0x41800000, v146
	v_mul_f32_e32 v146, 0x41800000, v147
	v_mov_b32_e32 v27, 0
	v_cvt_pk_fp8_f32 v27, v33, v146
	v_mul_f32_e32 v33, 0x41800000, v148
	v_mul_f32_e32 v146, 0x41800000, v149
	v_cvt_pk_f32_fp8_sdwa v[148:149], v191 src0_sel:WORD_1
	v_mul_f32_e32 v151, 0x41800000, v151
	v_cvt_pk_fp8_f32 v26, v150, v151 op_sel:[0,0,1]
	v_lshlrev_b32_e32 v182, 16, v25
	v_mov_b32_e32 v150, v144
	v_mov_b32_e32 v151, v148
	v_pk_mul_f32 v[150:151], v[150:151], v[182:183]
	v_and_b32_e32 v182, 0xffff0000, v25
	v_mov_b32_e32 v148, v145
	v_pk_mul_f32 v[144:145], v[148:149], v[182:183]
	v_cvt_pk_f32_fp8_e32 v[148:149], v191
	v_cvt_pk_fp8_f32 v27, v33, v146 op_sel:[0,0,1]
	v_add_f32_e32 v33, v150, v151
	v_add_f32_e32 v150, v144, v145
	v_lshlrev_b32_e32 v182, 16, v24
	v_mov_b32_e32 v144, v142
	v_mov_b32_e32 v145, v148
	v_pk_mul_f32 v[144:145], v[144:145], v[182:183]
	v_and_b32_e32 v182, 0xffff0000, v24
	v_add_f32_e32 v25, v144, v145
	v_mov_b32_e32 v148, v143
	v_mul_f32_e32 v142, 0x41800000, v25
	v_pk_mul_f32 v[24:25], v[148:149], v[182:183]
	v_mov_b32_e32 v203, 0
	v_add_f32_e32 v24, v24, v25
	v_mul_f32_e32 v24, 0x41800000, v24
	v_cvt_pk_fp8_f32 v203, v142, v24
	v_pk_mul_f32 v[24:25], v[140:141], s[16:17] op_sel_hi:[1,0]
	v_cvt_pk_f32_fp8_sdwa v[140:141], v190 src0_sel:WORD_1
	v_mov_b32_e32 v142, v24
	v_lshlrev_b32_e32 v182, 16, v23
	v_mov_b32_e32 v202, 0
	v_mov_b32_e32 v143, v140
	v_mov_b32_e32 v140, v25
	v_cvt_pk_f32_fp8_e32 v[24:25], v190
	v_pk_mul_f32 v[142:143], v[142:143], v[182:183]
	v_and_b32_e32 v182, 0xffff0000, v23
	v_add_f32_e32 v144, v142, v143
	v_pk_mul_f32 v[140:141], v[140:141], v[182:183]
	v_lshlrev_b32_e32 v182, 16, v22
	v_mov_b32_e32 v142, v138
	v_mov_b32_e32 v143, v24
	v_pk_mul_f32 v[142:143], v[142:143], v[182:183]
	v_and_b32_e32 v182, 0xffff0000, v22
	v_add_f32_e32 v23, v142, v143
	v_mov_b32_e32 v24, v139
	v_mul_f32_e32 v138, 0x41800000, v23
	v_pk_mul_f32 v[22:23], v[24:25], v[182:183]
	v_pk_mul_f32 v[24:25], v[136:137], s[16:17] op_sel_hi:[1,0]
	v_add_f32_e32 v22, v22, v23
	v_cvt_pk_f32_fp8_sdwa v[136:137], v29 src0_sel:WORD_1
	v_mul_f32_e32 v22, 0x41800000, v22
	v_cvt_pk_fp8_f32 v202, v138, v22
	v_add_f32_e32 v23, v140, v141
	v_lshlrev_b32_e32 v182, 16, v21
	v_mov_b32_e32 v138, v24
	v_mov_b32_e32 v139, v136
	v_mul_f32_e32 v22, 0x41800000, v144
	v_mul_f32_e32 v23, 0x41800000, v23
	v_pk_mul_f32 v[138:139], v[138:139], v[182:183]
	v_mul_f32_e32 v33, 0x41800000, v33
	v_cvt_pk_fp8_f32 v202, v22, v23 op_sel:[0,0,1]
	v_mul_f32_e32 v22, 0x41800000, v150
	v_add_f32_e32 v24, v138, v139
	v_and_b32_e32 v182, 0xffff0000, v21
	v_mov_b32_e32 v136, v25
	v_cvt_pk_fp8_f32 v203, v33, v22 op_sel:[0,0,1]
	v_mul_f32_e32 v33, 0x41800000, v24
	v_pk_mul_f32 v[24:25], v[136:137], v[182:183]
	v_cvt_pk_f32_fp8_e32 v[136:137], v29
	v_add_f32_e32 v138, v24, v25
	v_lshlrev_b32_e32 v182, 16, v20
	v_mov_b32_e32 v24, v134
	v_mov_b32_e32 v25, v136
	v_pk_mul_f32 v[24:25], v[24:25], v[182:183]
	v_and_b32_e32 v182, 0xffff0000, v20
	v_add_f32_e32 v21, v24, v25
	v_mov_b32_e32 v136, v135
	v_mul_f32_e32 v24, 0x41800000, v21
	v_pk_mul_f32 v[20:21], v[136:137], v[182:183]
	v_mov_b32_e32 v29, 0
	v_add_f32_e32 v20, v20, v21
	v_mul_f32_e32 v20, 0x41800000, v20
	v_cvt_pk_fp8_f32 v29, v24, v20
	v_cvt_pk_f32_fp8_sdwa v[24:25], v28 src0_sel:WORD_1
	v_pk_mul_f32 v[20:21], v[132:133], s[16:17] op_sel_hi:[1,0]
	v_lshlrev_b32_e32 v182, 16, v19
	v_mov_b32_e32 v132, v20
	v_mov_b32_e32 v133, v24
	v_mov_b32_e32 v24, v21
	v_cvt_pk_f32_fp8_e32 v[20:21], v28
	v_pk_mul_f32 v[132:133], v[132:133], v[182:183]
	v_and_b32_e32 v182, 0xffff0000, v19
	v_add_f32_e32 v134, v132, v133
	v_pk_mul_f32 v[24:25], v[24:25], v[182:183]
	v_lshlrev_b32_e32 v182, 16, v18
	v_mov_b32_e32 v132, v130
	v_mov_b32_e32 v133, v20
	v_pk_mul_f32 v[132:133], v[132:133], v[182:183]
	v_and_b32_e32 v182, 0xffff0000, v18
	v_add_f32_e32 v19, v132, v133
	v_mov_b32_e32 v20, v131
	v_mul_f32_e32 v130, 0x41800000, v19
	v_pk_mul_f32 v[18:19], v[20:21], v[182:183]
	v_mov_b32_e32 v28, 0
	v_add_f32_e32 v18, v18, v19
	v_mul_f32_e32 v18, 0x41800000, v18
	v_cvt_pk_fp8_f32 v28, v130, v18
	v_add_f32_e32 v19, v24, v25
	v_mul_f32_e32 v18, 0x41800000, v134
	v_mul_f32_e32 v19, 0x41800000, v19
	v_or_b32_e32 v146, v32, v194
	v_cvt_pk_fp8_f32 v28, v18, v19 op_sel:[0,0,1]
	v_mul_f32_e32 v18, 0x41800000, v138
	v_ashrrev_i32_e32 v147, 31, v146
	v_cvt_pk_fp8_f32 v29, v33, v18 op_sel:[0,0,1]
	v_lshlrev_b64 v[146:147], 11, v[146:147]
	v_pk_mul_f32 v[18:19], v[128:129], s[16:17] op_sel_hi:[1,0]
	v_cvt_pk_f32_fp8_e32 v[128:129], v188
	v_lshl_add_u64 v[22:23], s[4:5], 0, v[146:147]
	v_lshl_add_u64 v[22:23], v[22:23], 0, v[30:31]
	v_cvt_pk_f32_fp8_sdwa v[130:131], v188 src0_sel:WORD_1
	v_lshl_add_u64 v[22:23], v[22:23], 0, v[174:175]
	v_permlane16_swap_b32_e32 v26, v28
	v_permlane16_swap_b32_e32 v27, v29
	v_pk_mul_f32 v[20:21], v[126:127], s[16:17] op_sel_hi:[1,0]
	global_store_dwordx4 v[22:23], v[26:29], off offset:128
	v_lshlrev_b32_e32 v182, 16, v14
	v_and_b32_e32 v14, 0xffff0000, v14
	v_lshlrev_b32_e32 v26, 16, v15
	v_and_b32_e32 v28, 0xffff0000, v15
	v_mov_b32_e32 v137, v128
	v_mov_b32_e32 v128, v21
	v_mov_b32_e32 v15, v183
	v_cvt_pk_f32_fp8_e32 v[132:133], v189
	v_pk_mul_f32 v[14:15], v[128:129], v[14:15]
	v_mov_b32_e32 v27, v183
	v_add_f32_e32 v21, v14, v15
	v_mov_b32_e32 v14, v18
	v_mov_b32_e32 v15, v130
	v_pk_mul_f32 v[14:15], v[14:15], v[26:27]
	v_mov_b32_e32 v130, v19
	v_mov_b32_e32 v29, v183
	v_pk_mul_f32 v[24:25], v[122:123], s[16:17] op_sel_hi:[1,0]
	v_cvt_pk_f32_fp8_sdwa v[134:135], v189 src0_sel:WORD_1
	v_add_f32_e32 v18, v14, v15
	v_pk_mul_f32 v[14:15], v[130:131], v[28:29]
	v_permlane16_swap_b32_e32 v200, v202
	v_permlane16_swap_b32_e32 v201, v203
	v_lshlrev_b32_e32 v122, 16, v16
	v_add_f32_e32 v19, v14, v15
	v_mov_b32_e32 v14, v24
	v_mov_b32_e32 v15, v132
	v_mov_b32_e32 v123, v183
	global_store_dwordx4 v[22:23], v[200:203], off
	v_pk_mul_f32 v[22:23], v[124:125], s[16:17] op_sel_hi:[1,0]
	v_and_b32_e32 v16, 0xffff0000, v16
	v_lshlrev_b32_e32 v124, 16, v17
	v_and_b32_e32 v126, 0xffff0000, v17
	v_pk_mul_f32 v[14:15], v[14:15], v[122:123]
	v_mov_b32_e32 v132, v25
	v_mov_b32_e32 v17, v183
	v_add_f32_e32 v24, v14, v15
	v_pk_mul_f32 v[14:15], v[132:133], v[16:17]
	v_mov_b32_e32 v136, v20
	v_add_f32_e32 v16, v14, v15
	v_mov_b32_e32 v14, v22
	v_mov_b32_e32 v15, v134
	v_mov_b32_e32 v125, v183
	v_pk_mul_f32 v[136:137], v[136:137], v[182:183]
	v_pk_mul_f32 v[14:15], v[14:15], v[124:125]
	v_mov_b32_e32 v134, v23
	v_mov_b32_e32 v127, v183
	v_add_f32_e32 v20, v136, v137
	v_add_f32_e32 v17, v14, v15
	v_pk_mul_f32 v[14:15], v[134:135], v[126:127]
	v_mul_f32_e32 v16, 0x41800000, v16
	v_add_f32_e32 v22, v14, v15
	v_mul_f32_e32 v15, 0x41800000, v20
	v_mul_f32_e32 v20, 0x41800000, v21
	v_mov_b32_e32 v14, 0
	v_cvt_pk_fp8_f32 v14, v15, v20
	v_mul_f32_e32 v20, 0x41800000, v24
	v_mov_b32_e32 v15, 0
	v_cvt_pk_fp8_f32 v15, v20, v16
	v_mul_f32_e32 v18, 0x41800000, v18
	v_mul_f32_e32 v19, 0x41800000, v19
	v_cvt_pk_fp8_f32 v14, v18, v19 op_sel:[0,0,1]
	v_pk_mul_f32 v[18:19], v[118:119], s[16:17] op_sel_hi:[1,0]
	v_cvt_pk_f32_fp8_e32 v[118:119], v160
	v_mul_f32_e32 v16, 0x41800000, v17
	v_mul_f32_e32 v17, 0x41800000, v22
	v_cvt_pk_fp8_f32 v15, v16, v17 op_sel:[0,0,1]
	v_pk_mul_f32 v[16:17], v[120:121], s[16:17] op_sel_hi:[1,0]
	v_cvt_pk_f32_fp8_sdwa v[120:121], v160 src0_sel:WORD_1
	v_lshlrev_b32_e32 v182, 16, v10
	v_and_b32_e32 v10, 0xffff0000, v10
	v_lshlrev_b32_e32 v24, 16, v11
	v_and_b32_e32 v26, 0xffff0000, v11
	v_mov_b32_e32 v127, v118
	v_mov_b32_e32 v118, v19
	v_mov_b32_e32 v11, v183
	v_cvt_pk_f32_fp8_e32 v[122:123], v161
	v_pk_mul_f32 v[10:11], v[118:119], v[10:11]
	v_mov_b32_e32 v25, v183
	v_add_f32_e32 v19, v10, v11
	v_mov_b32_e32 v10, v16
	v_mov_b32_e32 v11, v120
	v_pk_mul_f32 v[10:11], v[10:11], v[24:25]
	v_mov_b32_e32 v120, v17
	v_pk_mul_f32 v[22:23], v[114:115], s[16:17] op_sel_hi:[1,0]
	v_cvt_pk_f32_fp8_sdwa v[124:125], v161 src0_sel:WORD_1
	v_add_f32_e32 v16, v10, v11
	v_pk_mul_f32 v[10:11], v[120:121], v[26:27]
	v_lshlrev_b32_e32 v28, 16, v12
	v_add_f32_e32 v17, v10, v11
	v_mov_b32_e32 v10, v22
	v_mov_b32_e32 v11, v122
	v_pk_mul_f32 v[20:21], v[116:117], s[16:17] op_sel_hi:[1,0]
	v_and_b32_e32 v12, 0xffff0000, v12
	v_lshlrev_b32_e32 v114, 16, v13
	v_and_b32_e32 v116, 0xffff0000, v13
	v_pk_mul_f32 v[10:11], v[10:11], v[28:29]
	v_mov_b32_e32 v122, v23
	v_mov_b32_e32 v13, v183
	v_add_f32_e32 v22, v10, v11
	v_pk_mul_f32 v[10:11], v[122:123], v[12:13]
	v_mov_b32_e32 v126, v18
	v_add_f32_e32 v12, v10, v11
	v_mov_b32_e32 v10, v20
	v_mov_b32_e32 v11, v124
	v_mov_b32_e32 v115, v183
	v_pk_mul_f32 v[126:127], v[126:127], v[182:183]
	v_pk_mul_f32 v[10:11], v[10:11], v[114:115]
	v_mov_b32_e32 v124, v21
	v_mov_b32_e32 v117, v183
	v_add_f32_e32 v18, v126, v127
	v_add_f32_e32 v13, v10, v11
	v_pk_mul_f32 v[10:11], v[124:125], v[116:117]
	v_mul_f32_e32 v12, 0x41800000, v12
	v_add_f32_e32 v20, v10, v11
	v_mul_f32_e32 v11, 0x41800000, v18
	v_mul_f32_e32 v18, 0x41800000, v19
	v_mov_b32_e32 v10, 0
	v_cvt_pk_fp8_f32 v10, v11, v18
	v_mul_f32_e32 v18, 0x41800000, v22
	v_mov_b32_e32 v11, 0
	v_cvt_pk_fp8_f32 v11, v18, v12
	v_cvt_pk_f32_fp8_sdwa v[18:19], v159 src0_sel:WORD_1
	v_mul_f32_e32 v16, 0x41800000, v16
	v_mul_f32_e32 v17, 0x41800000, v17
	v_cvt_pk_fp8_f32 v10, v16, v17 op_sel:[0,0,1]
	v_pk_mul_f32 v[16:17], v[112:113], s[16:17] op_sel_hi:[1,0]
	v_lshlrev_b32_e32 v182, 16, v9
	v_mov_b32_e32 v22, v16
	v_mov_b32_e32 v23, v18
	v_pk_mul_f32 v[22:23], v[22:23], v[182:183]
	v_and_b32_e32 v182, 0xffff0000, v9
	v_add_f32_e32 v16, v22, v23
	v_mov_b32_e32 v18, v17
	v_mul_f32_e32 v24, 0x41800000, v16
	v_pk_mul_f32 v[16:17], v[18:19], v[182:183]
	v_cvt_pk_f32_fp8_e32 v[18:19], v159
	v_mul_f32_e32 v12, 0x41800000, v13
	v_mul_f32_e32 v13, 0x41800000, v20
	v_pk_mul_f32 v[20:21], v[110:111], s[16:17] op_sel_hi:[1,0]
	v_add_f32_e32 v25, v16, v17
	v_lshlrev_b32_e32 v182, 16, v8
	v_mov_b32_e32 v16, v20
	v_mov_b32_e32 v17, v18
	v_pk_mul_f32 v[16:17], v[16:17], v[182:183]
	v_and_b32_e32 v182, 0xffff0000, v8
	v_add_f32_e32 v9, v16, v17
	v_mov_b32_e32 v18, v21
	v_mul_f32_e32 v16, 0x41800000, v9
	v_pk_mul_f32 v[8:9], v[18:19], v[182:183]
	v_cvt_pk_f32_fp8_sdwa v[18:19], v158 src0_sel:WORD_1
	v_add_f32_e32 v8, v8, v9
	v_mul_f32_e32 v8, 0x41800000, v8
	v_mov_b32_e32 v17, 0
	v_cvt_pk_fp8_f32 v17, v16, v8
	v_pk_mul_f32 v[8:9], v[108:109], s[16:17] op_sel_hi:[1,0]
	v_mov_b32_e32 v23, v18
	v_mov_b32_e32 v22, v8
	v_mov_b32_e32 v18, v9
	v_cvt_pk_f32_fp8_e32 v[8:9], v158
	v_lshlrev_b32_e32 v182, 16, v7
	v_pk_mul_f32 v[20:21], v[106:107], s[16:17] op_sel_hi:[1,0]
	v_pk_mul_f32 v[22:23], v[22:23], v[182:183]
	v_and_b32_e32 v182, 0xffff0000, v7
	v_add_f32_e32 v26, v22, v23
	v_pk_mul_f32 v[18:19], v[18:19], v[182:183]
	v_lshlrev_b32_e32 v182, 16, v6
	v_mov_b32_e32 v22, v20
	v_mov_b32_e32 v23, v8
	v_pk_mul_f32 v[22:23], v[22:23], v[182:183]
	v_and_b32_e32 v182, 0xffff0000, v6
	v_add_f32_e32 v7, v22, v23
	v_mov_b32_e32 v8, v21
	v_mul_f32_e32 v20, 0x41800000, v7
	v_pk_mul_f32 v[6:7], v[8:9], v[182:183]
	v_mov_b32_e32 v16, 0
	v_add_f32_e32 v6, v6, v7
	v_mul_f32_e32 v6, 0x41800000, v6
	v_cvt_pk_fp8_f32 v16, v20, v6
	v_add_f32_e32 v7, v18, v19
	v_cvt_pk_fp8_f32 v11, v12, v13 op_sel:[0,0,1]
	v_or_b32_e32 v12, v32, v195
	v_mul_f32_e32 v6, 0x41800000, v26
	v_mul_f32_e32 v7, 0x41800000, v7
	v_ashrrev_i32_e32 v13, 31, v12
	v_cvt_pk_fp8_f32 v16, v6, v7 op_sel:[0,0,1]
	v_mul_f32_e32 v6, 0x41800000, v25
	v_lshlrev_b64 v[12:13], 11, v[12:13]
	v_cvt_pk_fp8_f32 v17, v24, v6 op_sel:[0,0,1]
	v_lshl_add_u64 v[6:7], s[4:5], 0, v[12:13]
	v_cvt_pk_f32_fp8_sdwa v[12:13], v157 src0_sel:WORD_1
	v_lshl_add_u64 v[6:7], v[6:7], 0, v[30:31]
	v_permlane16_swap_b32_e32 v14, v16
	v_permlane16_swap_b32_e32 v15, v17
	v_lshl_add_u64 v[6:7], v[6:7], 0, v[174:175]
	v_pk_mul_f32 v[8:9], v[104:105], s[16:17] op_sel_hi:[1,0]
	global_store_dwordx4 v[6:7], v[14:17], off
	v_lshlrev_b32_e32 v182, 16, v5
	v_mov_b32_e32 v134, v94
	v_mov_b32_e32 v16, v8
	v_mov_b32_e32 v17, v12
	v_pk_mul_f32 v[16:17], v[16:17], v[182:183]
	v_and_b32_e32 v182, 0xffff0000, v5
	v_add_f32_e32 v8, v16, v17
	v_mov_b32_e32 v12, v9
	v_mul_f32_e32 v18, 0x41800000, v8
	v_pk_mul_f32 v[8:9], v[12:13], v[182:183]
	v_cvt_pk_f32_fp8_e32 v[12:13], v157
	v_pk_mul_f32 v[14:15], v[102:103], s[16:17] op_sel_hi:[1,0]
	v_add_f32_e32 v19, v8, v9
	v_lshlrev_b32_e32 v182, 16, v4
	v_mov_b32_e32 v8, v14
	v_mov_b32_e32 v9, v12
	v_pk_mul_f32 v[8:9], v[8:9], v[182:183]
	v_and_b32_e32 v182, 0xffff0000, v4
	v_add_f32_e32 v5, v8, v9
	v_mov_b32_e32 v12, v15
	v_mul_f32_e32 v8, 0x41800000, v5
	v_pk_mul_f32 v[4:5], v[12:13], v[182:183]
	v_mov_b32_e32 v13, 0
	v_add_f32_e32 v4, v4, v5
	v_mul_f32_e32 v4, 0x41800000, v4
	v_cvt_pk_fp8_f32 v13, v8, v4
	v_cvt_pk_f32_fp8_sdwa v[8:9], v156 src0_sel:WORD_1
	v_pk_mul_f32 v[4:5], v[100:101], s[16:17] op_sel_hi:[1,0]
	v_lshlrev_b32_e32 v182, 16, v3
	v_mov_b32_e32 v16, v4
	v_mov_b32_e32 v17, v8
	v_mov_b32_e32 v8, v5
	v_cvt_pk_f32_fp8_e32 v[4:5], v156
	v_pk_mul_f32 v[14:15], v[98:99], s[16:17] op_sel_hi:[1,0]
	v_pk_mul_f32 v[16:17], v[16:17], v[182:183]
	v_and_b32_e32 v182, 0xffff0000, v3
	v_add_f32_e32 v20, v16, v17
	v_pk_mul_f32 v[8:9], v[8:9], v[182:183]
	v_lshlrev_b32_e32 v182, 16, v2
	v_mov_b32_e32 v16, v14
	v_mov_b32_e32 v17, v4
	v_pk_mul_f32 v[16:17], v[16:17], v[182:183]
	v_and_b32_e32 v182, 0xffff0000, v2
	v_add_f32_e32 v3, v16, v17
	v_mov_b32_e32 v4, v15
	v_mul_f32_e32 v14, 0x41800000, v3
	v_pk_mul_f32 v[2:3], v[4:5], v[182:183]
	v_mov_b32_e32 v12, 0
	v_add_f32_e32 v2, v2, v3
	v_mul_f32_e32 v2, 0x41800000, v2
	v_cvt_pk_fp8_f32 v12, v14, v2
	v_add_f32_e32 v3, v8, v9
	v_mul_f32_e32 v2, 0x41800000, v20
	v_mul_f32_e32 v3, 0x41800000, v3
	v_cvt_pk_fp8_f32 v12, v2, v3 op_sel:[0,0,1]
	v_mul_f32_e32 v2, 0x41800000, v19
	v_cvt_pk_fp8_f32 v13, v18, v2 op_sel:[0,0,1]
	v_add_u32_e32 v100, 0x80, v32
	v_mad_i64_i32 v[2:3], s[28:29], v100, s51, v[184:185]
	v_permlane16_swap_b32_e32 v10, v12
	v_permlane16_swap_b32_e32 v11, v13
	v_lshl_add_u64 v[2:3], v[2:3], 0, s[14:15]
	global_store_dwordx4 v[6:7], v[10:13], off offset:128
	v_lshl_add_u64 v[4:5], v[2:3], 0, v[186:187]
	v_ashrrev_i32_e32 v101, 31, v100
	global_load_dwordx4 v[108:111], v[4:5], off
	v_lshlrev_b64 v[4:5], 11, v[100:101]
	v_lshl_add_u64 v[4:5], s[8:9], 0, v[4:5]
	v_lshl_add_u64 v[4:5], v[4:5], 0, v[30:31]
	global_load_dwordx2 v[26:27], v[4:5], off
	v_lshl_add_u64 v[2:3], v[2:3], 0, v[154:155]
	global_load_dwordx4 v[112:115], v[2:3], off
	global_load_dwordx2 v[116:117], v[4:5], off offset:128
	v_add_u32_e32 v2, 0x90, v32
	v_ashrrev_i32_e32 v3, 31, v2
	v_mad_i64_i32 v[4:5], s[28:29], v2, s51, v[184:185]
	v_lshl_add_u64 v[4:5], v[4:5], 0, s[14:15]
	v_lshlrev_b64 v[2:3], 11, v[2:3]
	v_lshl_add_u64 v[2:3], s[8:9], 0, v[2:3]
	v_lshl_add_u64 v[6:7], v[4:5], 0, v[186:187]
	v_lshl_add_u64 v[2:3], v[2:3], 0, v[30:31]
	global_load_dwordx4 v[22:25], v[6:7], off
	global_load_dwordx2 v[106:107], v[2:3], off
	v_lshl_add_u64 v[4:5], v[4:5], 0, v[154:155]
	global_load_dwordx4 v[18:21], v[4:5], off
	global_load_dwordx2 v[28:29], v[2:3], off offset:128
	v_mov_b32_e32 v119, v183
	v_mov_b32_e32 v121, v183
	v_mov_b32_e32 v123, v183
	v_mov_b32_e32 v125, v183
	v_mov_b32_e32 v127, v183
	v_add_u32_e32 v2, 0xa0, v32
	v_ashrrev_i32_e32 v3, 31, v2
	v_mad_i64_i32 v[4:5], s[28:29], v2, s51, v[184:185]
	v_lshl_add_u64 v[4:5], v[4:5], 0, s[14:15]
	v_lshlrev_b64 v[2:3], 11, v[2:3]
	v_lshl_add_u64 v[2:3], s[8:9], 0, v[2:3]
	v_lshl_add_u64 v[6:7], v[4:5], 0, v[186:187]
	v_lshl_add_u64 v[2:3], v[2:3], 0, v[30:31]
	global_load_dwordx4 v[14:17], v[6:7], off
	global_load_dwordx2 v[104:105], v[2:3], off
	v_lshl_add_u64 v[4:5], v[4:5], 0, v[154:155]
	global_load_dwordx4 v[10:13], v[4:5], off
	global_load_dwordx2 v[102:103], v[2:3], off offset:128
	v_add_u32_e32 v2, 0xb0, v32
	v_ashrrev_i32_e32 v3, 31, v2
	v_mad_i64_i32 v[4:5], s[28:29], v2, s51, v[184:185]
	v_lshl_add_u64 v[4:5], v[4:5], 0, s[14:15]
	v_lshlrev_b64 v[2:3], 11, v[2:3]
	v_lshl_add_u64 v[2:3], s[8:9], 0, v[2:3]
	v_lshl_add_u64 v[6:7], v[4:5], 0, v[186:187]
	v_lshl_add_u64 v[32:33], v[2:3], 0, v[30:31]
	global_load_dwordx4 v[6:9], v[6:7], off
	s_nop 0
	global_load_dwordx2 v[98:99], v[32:33], off
	v_lshl_add_u64 v[2:3], v[4:5], 0, v[154:155]
	global_load_dwordx4 v[2:5], v[2:3], off
	s_nop 0
	global_load_dwordx2 v[32:33], v[32:33], off offset:128
	s_waitcnt vmcnt(15)
	v_lshlrev_b32_e32 v182, 16, v108
	v_and_b32_e32 v108, 0xffff0000, v108
	v_lshlrev_b32_e32 v118, 16, v109
	v_and_b32_e32 v120, 0xffff0000, v109
	s_waitcnt vmcnt(14)
	v_cvt_pk_f32_fp8_e32 v[128:129], v26
	v_cvt_pk_f32_fp8_sdwa v[130:131], v26 src0_sel:WORD_1
	v_mov_b32_e32 v109, v183
	v_cvt_pk_f32_fp8_e32 v[132:133], v27
	v_mov_b32_e32 v135, v128
	v_mov_b32_e32 v128, v95
	v_pk_mul_f32 v[94:95], v[128:129], v[108:109]
	v_cvt_pk_f32_fp8_sdwa v[26:27], v27 src0_sel:WORD_1
	v_add_f32_e32 v108, v94, v95
	v_mov_b32_e32 v94, v96
	v_mov_b32_e32 v95, v130
	v_pk_mul_f32 v[94:95], v[94:95], v[118:119]
	v_mov_b32_e32 v130, v97
	v_add_f32_e32 v96, v94, v95
	v_pk_mul_f32 v[94:95], v[130:131], v[120:121]
	v_lshlrev_b32_e32 v122, 16, v110
	v_and_b32_e32 v110, 0xffff0000, v110
	v_lshlrev_b32_e32 v124, 16, v111
	v_and_b32_e32 v126, 0xffff0000, v111
	v_add_f32_e32 v97, v94, v95
	v_mov_b32_e32 v94, v90
	v_mov_b32_e32 v95, v132
	v_mov_b32_e32 v132, v91
	v_mov_b32_e32 v111, v183
	v_pk_mul_f32 v[94:95], v[94:95], v[122:123]
	v_pk_mul_f32 v[90:91], v[132:133], v[110:111]
	v_pk_mul_f32 v[134:135], v[134:135], v[182:183]
	v_add_f32_e32 v94, v94, v95
	v_add_f32_e32 v95, v90, v91
	v_mov_b32_e32 v90, v92
	v_mov_b32_e32 v91, v26
	v_mov_b32_e32 v26, v93
	v_add_f32_e32 v101, v134, v135
	v_pk_mul_f32 v[90:91], v[90:91], v[124:125]
	v_pk_mul_f32 v[26:27], v[26:27], v[126:127]
	v_add_f32_e32 v92, v90, v91
	v_add_f32_e32 v26, v26, v27
	v_mul_f32_e32 v27, 0x41800000, v101
	v_mul_f32_e32 v91, 0x41800000, v108
	v_mov_b32_e32 v90, 0
	v_cvt_pk_fp8_f32 v90, v27, v91
	v_mul_f32_e32 v27, 0x41800000, v94
	v_mul_f32_e32 v94, 0x41800000, v95
	v_mov_b32_e32 v91, 0
	v_cvt_pk_fp8_f32 v91, v27, v94
	v_mul_f32_e32 v93, 0x41800000, v96
	v_mul_f32_e32 v96, 0x41800000, v97
	v_mul_f32_e32 v27, 0x41800000, v92
	v_mul_f32_e32 v26, 0x41800000, v26
	v_cvt_pk_fp8_f32 v90, v93, v96 op_sel:[0,0,1]
	v_cvt_pk_fp8_f32 v91, v27, v26 op_sel:[0,0,1]
	v_pk_mul_f32 v[26:27], v[88:89], s[16:17] op_sel_hi:[1,0]
	s_waitcnt vmcnt(13)
	v_lshlrev_b32_e32 v182, 16, v112
	v_and_b32_e32 v88, 0xffff0000, v112
	v_lshlrev_b32_e32 v96, 16, v114
	v_and_b32_e32 v108, 0xffff0000, v114
	v_lshlrev_b32_e32 v110, 16, v115
	v_and_b32_e32 v112, 0xffff0000, v115
	s_waitcnt vmcnt(12)
	v_cvt_pk_f32_fp8_e32 v[114:115], v116
	v_cvt_pk_f32_fp8_sdwa v[118:119], v116 src0_sel:WORD_1
	v_cvt_pk_f32_fp8_e32 v[120:121], v117
	v_mov_b32_e32 v89, v183
	v_mov_b32_e32 v123, v114
	v_mov_b32_e32 v114, v87
	v_mov_b32_e32 v122, v86
	v_pk_mul_f32 v[86:87], v[114:115], v[88:89]
	v_lshlrev_b32_e32 v92, 16, v113
	v_and_b32_e32 v94, 0xffff0000, v113
	v_add_f32_e32 v88, v86, v87
	v_mov_b32_e32 v86, v26
	v_mov_b32_e32 v87, v118
	v_mov_b32_e32 v93, v183
	v_mov_b32_e32 v118, v27
	v_mov_b32_e32 v95, v183
	v_cvt_pk_f32_fp8_sdwa v[116:117], v117 src0_sel:WORD_1
	v_pk_mul_f32 v[86:87], v[86:87], v[92:93]
	v_pk_mul_f32 v[26:27], v[118:119], v[94:95]
	v_add_f32_e32 v86, v86, v87
	v_add_f32_e32 v87, v26, v27
	v_mov_b32_e32 v26, v82
	v_mov_b32_e32 v27, v120
	v_mov_b32_e32 v97, v183
	v_pk_mul_f32 v[26:27], v[26:27], v[96:97]
	v_mov_b32_e32 v120, v83
	v_add_f32_e32 v82, v26, v27
	v_pk_mul_f32 v[26:27], v[120:121], v[108:109]
	v_pk_mul_f32 v[122:123], v[122:123], v[182:183]
	v_add_f32_e32 v83, v26, v27
	v_mov_b32_e32 v26, v84
	v_mov_b32_e32 v27, v116
	v_pk_mul_f32 v[26:27], v[26:27], v[110:111]
	v_mov_b32_e32 v116, v85
	v_mov_b32_e32 v113, v183
	v_add_f32_e32 v101, v122, v123
	v_add_f32_e32 v84, v26, v27
	v_pk_mul_f32 v[26:27], v[116:117], v[112:113]
	v_mul_f32_e32 v88, 0x41800000, v88
	v_add_f32_e32 v85, v26, v27
	v_mul_f32_e32 v27, 0x41800000, v101
	v_mov_b32_e32 v26, 0
	v_cvt_pk_fp8_f32 v26, v27, v88
	v_mul_f32_e32 v82, 0x41800000, v82
	v_mul_f32_e32 v83, 0x41800000, v83
	v_mov_b32_e32 v27, 0
	v_cvt_pk_fp8_f32 v27, v82, v83
	v_mul_f32_e32 v82, 0x41800000, v84
	v_mul_f32_e32 v83, 0x41800000, v85
	s_waitcnt vmcnt(10)
	v_cvt_pk_f32_fp8_sdwa v[84:85], v107 src0_sel:WORD_1
	v_mul_f32_e32 v86, 0x41800000, v86
	v_mul_f32_e32 v87, 0x41800000, v87
	v_cvt_pk_fp8_f32 v26, v86, v87 op_sel:[0,0,1]
	v_lshlrev_b32_e32 v182, 16, v25
	v_mov_b32_e32 v86, v80
	v_mov_b32_e32 v87, v84
	v_pk_mul_f32 v[86:87], v[86:87], v[182:183]
	v_and_b32_e32 v182, 0xffff0000, v25
	v_add_f32_e32 v80, v86, v87
	v_mov_b32_e32 v84, v81
	v_mul_f32_e32 v86, 0x41800000, v80
	v_pk_mul_f32 v[80:81], v[84:85], v[182:183]
	v_cvt_pk_f32_fp8_e32 v[84:85], v107
	v_add_f32_e32 v87, v80, v81
	v_lshlrev_b32_e32 v182, 16, v24
	v_mov_b32_e32 v80, v78
	v_mov_b32_e32 v81, v84
	v_pk_mul_f32 v[80:81], v[80:81], v[182:183]
	v_and_b32_e32 v182, 0xffff0000, v24
	v_add_f32_e32 v25, v80, v81
	v_mov_b32_e32 v84, v79
	v_mul_f32_e32 v78, 0x41800000, v25
	v_pk_mul_f32 v[24:25], v[84:85], v[182:183]
	v_mov_b32_e32 v93, 0
	v_add_f32_e32 v24, v24, v25
	v_mul_f32_e32 v24, 0x41800000, v24
	v_cvt_pk_fp8_f32 v93, v78, v24
	v_pk_mul_f32 v[24:25], v[72:73], s[16:17] op_sel_hi:[1,0]
	v_cvt_pk_f32_fp8_sdwa v[72:73], v106 src0_sel:WORD_1
	v_mov_b32_e32 v78, v24
	v_lshlrev_b32_e32 v182, 16, v23
	v_mov_b32_e32 v92, 0
	v_mov_b32_e32 v79, v72
	v_mov_b32_e32 v72, v25
	v_cvt_pk_f32_fp8_e32 v[24:25], v106
	v_pk_mul_f32 v[78:79], v[78:79], v[182:183]
	v_and_b32_e32 v182, 0xffff0000, v23
	v_add_f32_e32 v80, v78, v79
	v_pk_mul_f32 v[72:73], v[72:73], v[182:183]
	v_lshlrev_b32_e32 v182, 16, v22
	v_mov_b32_e32 v78, v70
	v_mov_b32_e32 v79, v24
	v_pk_mul_f32 v[78:79], v[78:79], v[182:183]
	v_and_b32_e32 v182, 0xffff0000, v22
	v_add_f32_e32 v23, v78, v79
	v_mov_b32_e32 v24, v71
	v_mul_f32_e32 v70, 0x41800000, v23
	v_pk_mul_f32 v[22:23], v[24:25], v[182:183]
	v_pk_mul_f32 v[24:25], v[76:77], s[16:17] op_sel_hi:[1,0]
	v_add_f32_e32 v22, v22, v23
	v_mul_f32_e32 v22, 0x41800000, v22
	v_cvt_pk_fp8_f32 v92, v70, v22
	s_waitcnt vmcnt(8)
	v_cvt_pk_f32_fp8_sdwa v[70:71], v29 src0_sel:WORD_1
	v_add_f32_e32 v23, v72, v73
	v_pk_mul_f32 v[72:73], v[74:75], s[16:17] op_sel_hi:[1,0]
	v_lshlrev_b32_e32 v182, 16, v21
	v_mov_b32_e32 v74, v24
	v_mov_b32_e32 v75, v70
	v_pk_mul_f32 v[74:75], v[74:75], v[182:183]
	v_and_b32_e32 v182, 0xffff0000, v21
	v_add_f32_e32 v24, v74, v75
	v_mov_b32_e32 v70, v25
	v_mul_f32_e32 v74, 0x41800000, v24
	v_pk_mul_f32 v[24:25], v[70:71], v[182:183]
	v_cvt_pk_f32_fp8_e32 v[70:71], v29
	v_add_f32_e32 v75, v24, v25
	v_lshlrev_b32_e32 v182, 16, v20
	v_mov_b32_e32 v24, v72
	v_mov_b32_e32 v25, v70
	v_pk_mul_f32 v[24:25], v[24:25], v[182:183]
	v_and_b32_e32 v182, 0xffff0000, v20
	v_add_f32_e32 v21, v24, v25
	v_mov_b32_e32 v70, v73
	v_mul_f32_e32 v24, 0x41800000, v21
	v_pk_mul_f32 v[20:21], v[70:71], v[182:183]
	v_mov_b32_e32 v29, 0
	v_add_f32_e32 v20, v20, v21
	v_mul_f32_e32 v20, 0x41800000, v20
	v_cvt_pk_fp8_f32 v29, v24, v20
	v_cvt_pk_f32_fp8_sdwa v[24:25], v28 src0_sel:WORD_1
	v_pk_mul_f32 v[20:21], v[68:69], s[16:17] op_sel_hi:[1,0]
	v_lshlrev_b32_e32 v182, 16, v19
	v_mov_b32_e32 v68, v20
	v_mov_b32_e32 v69, v24
	v_mov_b32_e32 v24, v21
	v_cvt_pk_f32_fp8_e32 v[20:21], v28
	v_pk_mul_f32 v[68:69], v[68:69], v[182:183]
	v_and_b32_e32 v182, 0xffff0000, v19
	v_add_f32_e32 v70, v68, v69
	v_pk_mul_f32 v[24:25], v[24:25], v[182:183]
	v_lshlrev_b32_e32 v182, 16, v18
	v_mov_b32_e32 v68, v66
	v_mov_b32_e32 v69, v20
	v_pk_mul_f32 v[68:69], v[68:69], v[182:183]
	v_and_b32_e32 v182, 0xffff0000, v18
	v_add_f32_e32 v19, v68, v69
	v_mov_b32_e32 v20, v67
	v_mul_f32_e32 v66, 0x41800000, v19
	v_pk_mul_f32 v[18:19], v[20:21], v[182:183]
	v_mov_b32_e32 v28, 0
	v_add_f32_e32 v18, v18, v19
	v_mul_f32_e32 v18, 0x41800000, v18
	v_cvt_pk_fp8_f32 v28, v66, v18
	v_add_f32_e32 v19, v24, v25
	v_mul_f32_e32 v18, 0x41800000, v70
	v_mul_f32_e32 v19, 0x41800000, v19
	v_cvt_pk_fp8_f32 v27, v82, v83 op_sel:[0,0,1]
	v_or_b32_e32 v82, v100, v194
	v_cvt_pk_fp8_f32 v28, v18, v19 op_sel:[0,0,1]
	v_mul_f32_e32 v18, 0x41800000, v75
	v_ashrrev_i32_e32 v83, 31, v82
	v_mul_f32_e32 v22, 0x41800000, v80
	v_mul_f32_e32 v23, 0x41800000, v23
	v_cvt_pk_fp8_f32 v29, v74, v18 op_sel:[0,0,1]
	v_lshlrev_b64 v[82:83], 11, v[82:83]
	v_cvt_pk_fp8_f32 v92, v22, v23 op_sel:[0,0,1]
	v_mul_f32_e32 v22, 0x41800000, v87
	v_pk_mul_f32 v[18:19], v[56:57], s[16:17] op_sel_hi:[1,0]
	s_waitcnt vmcnt(6)
	v_cvt_pk_f32_fp8_e32 v[56:57], v104
	v_cvt_pk_fp8_f32 v93, v86, v22 op_sel:[0,0,1]
	v_lshl_add_u64 v[22:23], s[4:5], 0, v[82:83]
	v_lshl_add_u64 v[22:23], v[22:23], 0, v[30:31]
	v_cvt_pk_f32_fp8_sdwa v[66:67], v104 src0_sel:WORD_1
	v_lshl_add_u64 v[22:23], v[22:23], 0, v[174:175]
	v_permlane16_swap_b32_e32 v26, v28
	v_permlane16_swap_b32_e32 v27, v29
	v_pk_mul_f32 v[20:21], v[54:55], s[16:17] op_sel_hi:[1,0]
	global_store_dwordx4 v[22:23], v[26:29], off offset:128
	v_lshlrev_b32_e32 v182, 16, v14
	v_and_b32_e32 v14, 0xffff0000, v14
	v_lshlrev_b32_e32 v26, 16, v15
	v_and_b32_e32 v28, 0xffff0000, v15
	v_mov_b32_e32 v73, v56
	v_mov_b32_e32 v56, v21
	v_mov_b32_e32 v15, v183
	v_cvt_pk_f32_fp8_e32 v[68:69], v105
	v_pk_mul_f32 v[14:15], v[56:57], v[14:15]
	v_mov_b32_e32 v27, v183
	v_add_f32_e32 v21, v14, v15
	v_mov_b32_e32 v14, v18
	v_mov_b32_e32 v15, v66
	v_pk_mul_f32 v[14:15], v[14:15], v[26:27]
	v_mov_b32_e32 v66, v19
	v_mov_b32_e32 v29, v183
	v_pk_mul_f32 v[24:25], v[50:51], s[16:17] op_sel_hi:[1,0]
	v_cvt_pk_f32_fp8_sdwa v[70:71], v105 src0_sel:WORD_1
	v_add_f32_e32 v18, v14, v15
	v_pk_mul_f32 v[14:15], v[66:67], v[28:29]
	v_permlane16_swap_b32_e32 v90, v92
	v_permlane16_swap_b32_e32 v91, v93
	v_lshlrev_b32_e32 v50, 16, v16
	v_add_f32_e32 v19, v14, v15
	v_mov_b32_e32 v14, v24
	v_mov_b32_e32 v15, v68
	v_mov_b32_e32 v51, v183
	global_store_dwordx4 v[22:23], v[90:93], off
	v_pk_mul_f32 v[22:23], v[52:53], s[16:17] op_sel_hi:[1,0]
	v_and_b32_e32 v16, 0xffff0000, v16
	v_lshlrev_b32_e32 v52, 16, v17
	v_and_b32_e32 v54, 0xffff0000, v17
	v_pk_mul_f32 v[14:15], v[14:15], v[50:51]
	v_mov_b32_e32 v68, v25
	v_mov_b32_e32 v17, v183
	v_add_f32_e32 v24, v14, v15
	v_pk_mul_f32 v[14:15], v[68:69], v[16:17]
	v_mov_b32_e32 v72, v20
	v_add_f32_e32 v16, v14, v15
	v_mov_b32_e32 v14, v22
	v_mov_b32_e32 v15, v70
	v_mov_b32_e32 v53, v183
	v_pk_mul_f32 v[72:73], v[72:73], v[182:183]
	v_pk_mul_f32 v[14:15], v[14:15], v[52:53]
	v_mov_b32_e32 v70, v23
	v_mov_b32_e32 v55, v183
	v_add_f32_e32 v20, v72, v73
	v_add_f32_e32 v17, v14, v15
	v_pk_mul_f32 v[14:15], v[70:71], v[54:55]
	v_mul_f32_e32 v16, 0x41800000, v16
	v_add_f32_e32 v22, v14, v15
	v_mul_f32_e32 v15, 0x41800000, v20
	v_mul_f32_e32 v20, 0x41800000, v21
	v_mov_b32_e32 v14, 0
	v_cvt_pk_fp8_f32 v14, v15, v20
	v_mul_f32_e32 v20, 0x41800000, v24
	v_mov_b32_e32 v15, 0
	s_waitcnt vmcnt(6)
	v_cvt_pk_f32_fp8_e32 v[54:55], v102
	v_cvt_pk_fp8_f32 v15, v20, v16
	v_mul_f32_e32 v18, 0x41800000, v18
	v_mul_f32_e32 v19, 0x41800000, v19
	v_cvt_pk_f32_fp8_sdwa v[56:57], v102 src0_sel:WORD_1
	v_cvt_pk_fp8_f32 v14, v18, v19 op_sel:[0,0,1]
	v_pk_mul_f32 v[18:19], v[62:63], s[16:17] op_sel_hi:[1,0]
	v_mul_f32_e32 v16, 0x41800000, v17
	v_mul_f32_e32 v17, 0x41800000, v22
	v_lshlrev_b32_e32 v182, 16, v10
	v_and_b32_e32 v10, 0xffff0000, v10
	v_lshlrev_b32_e32 v24, 16, v11
	v_and_b32_e32 v26, 0xffff0000, v11
	v_mov_b32_e32 v63, v54
	v_mov_b32_e32 v54, v19
	v_mov_b32_e32 v11, v183
	v_cvt_pk_fp8_f32 v15, v16, v17 op_sel:[0,0,1]
	v_pk_mul_f32 v[16:17], v[64:65], s[16:17] op_sel_hi:[1,0]
	v_pk_mul_f32 v[22:23], v[58:59], s[16:17] op_sel_hi:[1,0]
	v_cvt_pk_f32_fp8_e32 v[58:59], v103
	v_pk_mul_f32 v[10:11], v[54:55], v[10:11]
	v_mov_b32_e32 v25, v183
	v_add_f32_e32 v19, v10, v11
	v_mov_b32_e32 v10, v16
	v_mov_b32_e32 v11, v56
	v_pk_mul_f32 v[10:11], v[10:11], v[24:25]
	v_mov_b32_e32 v56, v17
	v_pk_mul_f32 v[20:21], v[60:61], s[16:17] op_sel_hi:[1,0]
	v_cvt_pk_f32_fp8_sdwa v[60:61], v103 src0_sel:WORD_1
	v_add_f32_e32 v16, v10, v11
	v_pk_mul_f32 v[10:11], v[56:57], v[26:27]
	v_lshlrev_b32_e32 v28, 16, v12
	v_add_f32_e32 v17, v10, v11
	v_mov_b32_e32 v10, v22
	v_mov_b32_e32 v11, v58
	v_and_b32_e32 v12, 0xffff0000, v12
	v_lshlrev_b32_e32 v50, 16, v13
	v_and_b32_e32 v52, 0xffff0000, v13
	v_pk_mul_f32 v[10:11], v[10:11], v[28:29]
	v_mov_b32_e32 v58, v23
	v_mov_b32_e32 v13, v183
	v_add_f32_e32 v22, v10, v11
	v_pk_mul_f32 v[10:11], v[58:59], v[12:13]
	v_mov_b32_e32 v62, v18
	v_add_f32_e32 v12, v10, v11
	v_mov_b32_e32 v10, v20
	v_mov_b32_e32 v11, v60
	v_pk_mul_f32 v[62:63], v[62:63], v[182:183]
	v_pk_mul_f32 v[10:11], v[10:11], v[50:51]
	v_mov_b32_e32 v60, v21
	v_add_f32_e32 v18, v62, v63
	v_add_f32_e32 v13, v10, v11
	v_pk_mul_f32 v[10:11], v[60:61], v[52:53]
	v_mul_f32_e32 v12, 0x41800000, v12
	v_add_f32_e32 v20, v10, v11
	v_mul_f32_e32 v11, 0x41800000, v18
	v_mul_f32_e32 v18, 0x41800000, v19
	v_mov_b32_e32 v10, 0
	v_cvt_pk_fp8_f32 v10, v11, v18
	v_mul_f32_e32 v18, 0x41800000, v22
	v_mov_b32_e32 v11, 0
	v_cvt_pk_fp8_f32 v11, v18, v12
	s_waitcnt vmcnt(4)
	v_cvt_pk_f32_fp8_sdwa v[18:19], v99 src0_sel:WORD_1
	v_mul_f32_e32 v16, 0x41800000, v16
	v_mul_f32_e32 v17, 0x41800000, v17
	v_cvt_pk_fp8_f32 v10, v16, v17 op_sel:[0,0,1]
	v_pk_mul_f32 v[16:17], v[44:45], s[16:17] op_sel_hi:[1,0]
	v_lshlrev_b32_e32 v182, 16, v9
	v_mov_b32_e32 v22, v16
	v_mov_b32_e32 v23, v18
	v_pk_mul_f32 v[22:23], v[22:23], v[182:183]
	v_and_b32_e32 v182, 0xffff0000, v9
	v_add_f32_e32 v16, v22, v23
	v_mov_b32_e32 v18, v17
	v_mul_f32_e32 v24, 0x41800000, v16
	v_pk_mul_f32 v[16:17], v[18:19], v[182:183]
	v_cvt_pk_f32_fp8_e32 v[18:19], v99
	v_mul_f32_e32 v12, 0x41800000, v13
	v_mul_f32_e32 v13, 0x41800000, v20
	v_pk_mul_f32 v[20:21], v[42:43], s[16:17] op_sel_hi:[1,0]
	v_add_f32_e32 v25, v16, v17
	v_lshlrev_b32_e32 v182, 16, v8
	v_mov_b32_e32 v16, v20
	v_mov_b32_e32 v17, v18
	v_pk_mul_f32 v[16:17], v[16:17], v[182:183]
	v_and_b32_e32 v182, 0xffff0000, v8
	v_add_f32_e32 v9, v16, v17
	v_mov_b32_e32 v18, v21
	v_mul_f32_e32 v16, 0x41800000, v9
	v_pk_mul_f32 v[8:9], v[18:19], v[182:183]
	v_cvt_pk_f32_fp8_sdwa v[18:19], v98 src0_sel:WORD_1
	v_add_f32_e32 v8, v8, v9
	v_mul_f32_e32 v8, 0x41800000, v8
	v_mov_b32_e32 v17, 0
	v_cvt_pk_fp8_f32 v17, v16, v8
	v_pk_mul_f32 v[8:9], v[40:41], s[16:17] op_sel_hi:[1,0]
	v_mov_b32_e32 v23, v18
	v_mov_b32_e32 v22, v8
	v_mov_b32_e32 v18, v9
	v_cvt_pk_f32_fp8_e32 v[8:9], v98
	v_lshlrev_b32_e32 v182, 16, v7
	v_pk_mul_f32 v[20:21], v[38:39], s[16:17] op_sel_hi:[1,0]
	v_pk_mul_f32 v[22:23], v[22:23], v[182:183]
	v_and_b32_e32 v182, 0xffff0000, v7
	v_add_f32_e32 v26, v22, v23
	v_pk_mul_f32 v[18:19], v[18:19], v[182:183]
	v_lshlrev_b32_e32 v182, 16, v6
	v_mov_b32_e32 v22, v20
	v_mov_b32_e32 v23, v8
	v_pk_mul_f32 v[22:23], v[22:23], v[182:183]
	v_and_b32_e32 v182, 0xffff0000, v6
	v_add_f32_e32 v7, v22, v23
	v_mov_b32_e32 v8, v21
	v_mul_f32_e32 v20, 0x41800000, v7
	v_pk_mul_f32 v[6:7], v[8:9], v[182:183]
	v_mov_b32_e32 v16, 0
	v_add_f32_e32 v6, v6, v7
	v_mul_f32_e32 v6, 0x41800000, v6
	v_cvt_pk_fp8_f32 v16, v20, v6
	v_add_f32_e32 v7, v18, v19
	v_cvt_pk_fp8_f32 v11, v12, v13 op_sel:[0,0,1]
	v_or_b32_e32 v12, v100, v195
	v_mul_f32_e32 v6, 0x41800000, v26
	v_mul_f32_e32 v7, 0x41800000, v7
	v_ashrrev_i32_e32 v13, 31, v12
	v_cvt_pk_fp8_f32 v16, v6, v7 op_sel:[0,0,1]
	v_mul_f32_e32 v6, 0x41800000, v25
	v_lshlrev_b64 v[12:13], 11, v[12:13]
	v_cvt_pk_fp8_f32 v17, v24, v6 op_sel:[0,0,1]
	v_lshl_add_u64 v[6:7], s[4:5], 0, v[12:13]
	s_waitcnt vmcnt(2)
	v_cvt_pk_f32_fp8_sdwa v[12:13], v33 src0_sel:WORD_1
	v_lshl_add_u64 v[6:7], v[6:7], 0, v[30:31]
	v_permlane16_swap_b32_e32 v14, v16
	v_permlane16_swap_b32_e32 v15, v17
	v_lshl_add_u64 v[6:7], v[6:7], 0, v[174:175]
	v_pk_mul_f32 v[8:9], v[48:49], s[16:17] op_sel_hi:[1,0]
	global_store_dwordx4 v[6:7], v[14:17], off
	v_lshlrev_b32_e32 v182, 16, v5
	s_nop 0
	v_mov_b32_e32 v16, v8
	v_mov_b32_e32 v17, v12
	v_pk_mul_f32 v[16:17], v[16:17], v[182:183]
	v_and_b32_e32 v182, 0xffff0000, v5
	v_add_f32_e32 v8, v16, v17
	v_mov_b32_e32 v12, v9
	v_mul_f32_e32 v18, 0x41800000, v8
	v_pk_mul_f32 v[8:9], v[12:13], v[182:183]
	v_cvt_pk_f32_fp8_e32 v[12:13], v33
	v_pk_mul_f32 v[14:15], v[46:47], s[16:17] op_sel_hi:[1,0]
	v_add_f32_e32 v19, v8, v9
	v_lshlrev_b32_e32 v182, 16, v4
	v_mov_b32_e32 v8, v14
	v_mov_b32_e32 v9, v12
	v_pk_mul_f32 v[8:9], v[8:9], v[182:183]
	v_and_b32_e32 v182, 0xffff0000, v4
	v_add_f32_e32 v5, v8, v9
	v_mov_b32_e32 v12, v15
	v_mul_f32_e32 v8, 0x41800000, v5
	v_pk_mul_f32 v[4:5], v[12:13], v[182:183]
	v_mov_b32_e32 v13, 0
	v_add_f32_e32 v4, v4, v5
	v_mul_f32_e32 v4, 0x41800000, v4
	v_cvt_pk_fp8_f32 v13, v8, v4
	v_cvt_pk_f32_fp8_sdwa v[8:9], v32 src0_sel:WORD_1
	v_pk_mul_f32 v[4:5], v[36:37], s[16:17] op_sel_hi:[1,0]
	v_lshlrev_b32_e32 v182, 16, v3
	v_mov_b32_e32 v16, v4
	v_mov_b32_e32 v17, v8
	v_mov_b32_e32 v8, v5
	v_cvt_pk_f32_fp8_e32 v[4:5], v32
	v_pk_mul_f32 v[14:15], v[34:35], s[16:17] op_sel_hi:[1,0]
	v_pk_mul_f32 v[16:17], v[16:17], v[182:183]
	v_and_b32_e32 v182, 0xffff0000, v3
	v_add_f32_e32 v20, v16, v17
	v_pk_mul_f32 v[8:9], v[8:9], v[182:183]
	v_lshlrev_b32_e32 v182, 16, v2
	v_mov_b32_e32 v16, v14
	v_mov_b32_e32 v17, v4
	v_pk_mul_f32 v[16:17], v[16:17], v[182:183]
	v_and_b32_e32 v182, 0xffff0000, v2
	v_add_f32_e32 v3, v16, v17
	v_mov_b32_e32 v4, v15
	v_mul_f32_e32 v14, 0x41800000, v3
	v_pk_mul_f32 v[2:3], v[4:5], v[182:183]
	v_mov_b32_e32 v12, 0
	v_add_f32_e32 v2, v2, v3
	v_mul_f32_e32 v2, 0x41800000, v2
	v_cvt_pk_fp8_f32 v12, v14, v2
	v_add_f32_e32 v3, v8, v9
	v_mul_f32_e32 v2, 0x41800000, v20
	v_mul_f32_e32 v3, 0x41800000, v3
	v_cvt_pk_fp8_f32 v12, v2, v3 op_sel:[0,0,1]
	v_mul_f32_e32 v2, 0x41800000, v19
	v_cvt_pk_fp8_f32 v13, v18, v2 op_sel:[0,0,1]
	v_permlane16_swap_b32_e32 v10, v12
	s_nop 0
	v_permlane16_swap_b32_e32 v11, v13
	global_store_dwordx4 v[6:7], v[10:13], off offset:128
	s_cbranch_vccnz .LBB0_546
	s_andn2_b64 vcc, exec, s[0:1]
	s_cbranch_vccnz .LBB0_545
	s_barrier
	s_branch .LBB0_545

.LBB0_632:
	s_ashr_i32 s17, s16, 31
	s_lshl_b64 s[20:21], s[16:17], 19
	s_add_u32 s20, s13, s20
	s_addc_u32 s21, s15, s21
	s_and_b64 s[22:23], s[30:31], exec
	s_cselect_b32 s17, s21, s27
	s_cselect_b32 s49, s20, s26
	s_ashr_i32 s19, s18, 31
	s_lshl_b64 s[22:23], s[18:19], 19
	s_add_u32 s22, s36, s22
	s_addc_u32 s23, s37, s23
	s_and_b64 s[30:31], s[30:31], exec
	s_cselect_b32 s19, s23, s29
	s_cselect_b32 s50, s22, s28
	s_add_u32 s51, s28, 0x100
	v_mov_b32_e32 v34, 0
	s_addc_u32 s52, s29, 0
	s_mov_b32 s53, -2
	v_mov_b32_e32 v35, v34
	v_mov_b64_e32 v[36:37], 0
	v_mov_b64_e32 v[38:39], 0
	v_mov_b64_e32 v[40:41], 0
	v_mov_b64_e32 v[42:43], 0
	v_mov_b64_e32 v[44:45], 0
	v_mov_b64_e32 v[46:47], 0
	v_mov_b64_e32 v[48:49], 0
	v_mov_b64_e32 v[50:51], 0
	v_mov_b64_e32 v[52:53], 0
	v_mov_b64_e32 v[54:55], 0
	v_mov_b64_e32 v[56:57], 0
	v_mov_b64_e32 v[58:59], 0
	v_mov_b64_e32 v[60:61], 0
	v_mov_b64_e32 v[62:63], 0
	v_mov_b64_e32 v[64:65], 0
	v_mov_b64_e32 v[66:67], 0
	v_mov_b64_e32 v[68:69], 0
	v_mov_b64_e32 v[70:71], 0
	v_mov_b64_e32 v[72:73], 0
	v_mov_b64_e32 v[74:75], 0
	v_mov_b64_e32 v[76:77], 0
	v_mov_b64_e32 v[78:79], 0
	v_mov_b64_e32 v[80:81], 0
	v_mov_b64_e32 v[82:83], 0
	v_mov_b64_e32 v[84:85], 0
	v_mov_b64_e32 v[86:87], 0
	v_mov_b64_e32 v[88:89], 0
	v_mov_b64_e32 v[90:91], 0
	v_mov_b64_e32 v[92:93], 0
	v_mov_b64_e32 v[94:95], 0
	v_mov_b64_e32 v[96:97], 0
	v_mov_b64_e32 v[98:99], 0
	v_mov_b64_e32 v[100:101], 0
	v_mov_b64_e32 v[102:103], 0
	v_mov_b64_e32 v[104:105], 0
	v_mov_b64_e32 v[106:107], 0
	v_mov_b64_e32 v[108:109], 0
	v_mov_b64_e32 v[110:111], 0
	v_mov_b64_e32 v[112:113], 0
	v_mov_b64_e32 v[114:115], 0
	v_mov_b64_e32 v[116:117], 0
	v_mov_b64_e32 v[118:119], 0
	v_mov_b64_e32 v[120:121], 0
	v_mov_b64_e32 v[122:123], 0
	v_mov_b64_e32 v[124:125], 0
	v_mov_b64_e32 v[126:127], 0
	v_mov_b64_e32 v[128:129], 0
	v_mov_b64_e32 v[130:131], 0
	v_mov_b64_e32 v[132:133], 0
	v_mov_b64_e32 v[134:135], 0
	v_mov_b64_e32 v[136:137], 0
	v_mov_b64_e32 v[138:139], 0
	v_mov_b64_e32 v[140:141], 0
	v_mov_b64_e32 v[142:143], 0
	v_mov_b64_e32 v[144:145], 0
	v_mov_b64_e32 v[146:147], 0
	v_mov_b64_e32 v[148:149], 0
	v_mov_b64_e32 v[150:151], 0
	v_mov_b64_e32 v[152:153], 0
	v_mov_b64_e32 v[154:155], 0
	v_mov_b64_e32 v[156:157], 0
	v_mov_b64_e32 v[158:159], 0
	v_mov_b64_e32 v[160:161], 0

.LBB0_636:
	v_lshl_add_u32 v6, s24, 8, v188
	v_lshl_or_b32 v2, s48, 8, v190
	v_readlane_b32 s48, v254, 13
	v_ashrrev_i32_e32 v3, 31, v2
	v_readlane_b32 s49, v254, 14
	v_ashrrev_i32_e32 v7, 31, v6
	v_lshlrev_b64 v[4:5], 13, v[6:7]
	v_lshl_add_u64 v[8:9], v[2:3], 2, s[48:49]
	s_nop 11
	v_lshl_add_u64 v[4:5], v[8:9], 0, v[4:5]
	global_load_dwordx4 v[12:15], v[4:5], off nt
	global_load_dwordx4 v[20:23], v[4:5], off offset:64 nt
	global_load_dwordx4 v[24:27], v[4:5], off offset:512 nt
	global_load_dwordx4 v[28:31], v[4:5], off offset:576 nt
	v_or_b32_e32 v4, 16, v6
	v_ashrrev_i32_e32 v5, 31, v4
	v_lshlrev_b64 v[10:11], 13, v[4:5]
	v_lshl_add_u64 v[16:17], v[8:9], 0, v[10:11]
	global_load_dwordx4 v[180:183], v[16:17], off nt
	global_load_dwordx4 v[184:187], v[16:17], off offset:64 nt
	global_load_dwordx4 v[194:197], v[16:17], off offset:512 nt
	global_load_dwordx4 v[198:201], v[16:17], off offset:576 nt
	v_or_b32_e32 v32, 32, v6
	v_or_b32_e32 v10, 48, v6
	v_ashrrev_i32_e32 v33, 31, v32
	v_ashrrev_i32_e32 v11, 31, v10
	v_lshlrev_b64 v[202:203], 12, v[6:7]
	v_lshlrev_b64 v[18:19], 1, v[2:3]
	v_lshlrev_b64 v[2:3], 13, v[32:33]
	v_lshlrev_b64 v[16:17], 13, v[10:11]
	v_lshl_add_u64 v[202:203], s[4:5], 0, v[202:203]
	v_lshlrev_b64 v[230:231], 12, v[4:5]
	v_lshl_add_u64 v[2:3], v[8:9], 0, v[2:3]
	v_lshl_add_u64 v[4:5], v[8:9], 0, v[16:17]
	v_lshl_add_u64 v[16:17], v[202:203], 0, v[18:19]
	global_load_dwordx4 v[202:205], v[2:3], off nt
	global_load_dwordx4 v[206:209], v[2:3], off offset:64 nt
	global_load_dwordx4 v[210:213], v[2:3], off offset:512 nt
	global_load_dwordx4 v[214:217], v[2:3], off offset:576 nt
	global_load_dwordx4 v[218:221], v[4:5], off nt
	global_load_dwordx4 v[222:225], v[4:5], off offset:64 nt
	global_load_dwordx4 v[226:229], v[4:5], off offset:512 nt
	s_nop 0
	global_load_dwordx4 v[2:5], v[4:5], off offset:576 nt
	v_lshl_add_u64 v[16:17], v[16:17], 0, v[170:171]
	v_lshl_add_u64 v[16:17], v[16:17], 0, v[178:179]
	s_and_b64 vcc, exec, s[6:7]
	s_mov_b64 s[6:7], -1
	v_readlane_b32 s50, v254, 15
	v_readlane_b32 s51, v254, 16
	v_readlane_b32 s52, v254, 17
	v_readlane_b32 s53, v254, 18
	v_readlane_b32 s54, v254, 19
	v_readlane_b32 s55, v254, 20
	v_readlane_b32 s56, v254, 21
	v_readlane_b32 s57, v254, 22
	v_readlane_b32 s58, v254, 23
	v_readlane_b32 s59, v254, 24
	v_readlane_b32 s60, v254, 25
	v_readlane_b32 s61, v254, 26
	v_readlane_b32 s62, v254, 27
	v_readlane_b32 s63, v254, 28
	s_waitcnt vmcnt(0)
	v_pk_mul_f32 v[14:15], v[14:15], s[12:13] op_sel_hi:[1,0]
	v_pk_mul_f32 v[12:13], v[12:13], s[12:13] op_sel_hi:[1,0]
	v_pk_mul_f32 v[22:23], v[22:23], s[12:13] op_sel_hi:[1,0]
	v_pk_mul_f32 v[20:21], v[20:21], s[12:13] op_sel_hi:[1,0]
	v_pk_fma_f32 v[14:15], v[160:161], s[14:15], v[14:15] op_sel_hi:[1,0,1]
	v_pk_fma_f32 v[12:13], v[158:159], s[14:15], v[12:13] op_sel_hi:[1,0,1]
	v_pk_fma_f32 v[22:23], v[156:157], s[14:15], v[22:23] op_sel_hi:[1,0,1]
	v_pk_fma_f32 v[20:21], v[154:155], s[14:15], v[20:21] op_sel_hi:[1,0,1]
	v_cvt_pk_bf16_f32 v12, v12, v13
	v_cvt_pk_bf16_f32 v13, v14, v15
	v_pk_mul_f32 v[26:27], v[26:27], s[12:13] op_sel_hi:[1,0]
	v_cvt_pk_bf16_f32 v14, v20, v21
	v_cvt_pk_bf16_f32 v15, v22, v23
	v_pk_mul_f32 v[24:25], v[24:25], s[12:13] op_sel_hi:[1,0]
	v_pk_mul_f32 v[30:31], v[30:31], s[12:13] op_sel_hi:[1,0]
	v_pk_mul_f32 v[28:29], v[28:29], s[12:13] op_sel_hi:[1,0]
	v_permlane16_swap_b32_e32 v12, v14
	v_permlane16_swap_b32_e32 v13, v15
	v_pk_fma_f32 v[26:27], v[152:153], s[14:15], v[26:27] op_sel_hi:[1,0,1]
	v_pk_fma_f32 v[24:25], v[150:151], s[14:15], v[24:25] op_sel_hi:[1,0,1]
	v_pk_fma_f32 v[30:31], v[144:145], s[14:15], v[30:31] op_sel_hi:[1,0,1]
	v_pk_fma_f32 v[28:29], v[142:143], s[14:15], v[28:29] op_sel_hi:[1,0,1]
	global_store_dwordx4 v[16:17], v[12:15], off
	v_pk_mul_f32 v[142:143], v[182:183], s[12:13] op_sel_hi:[1,0]
	v_pk_mul_f32 v[144:145], v[180:181], s[12:13] op_sel_hi:[1,0]
	v_cvt_pk_bf16_f32 v12, v24, v25
	v_cvt_pk_bf16_f32 v13, v26, v27
	v_cvt_pk_bf16_f32 v14, v28, v29
	v_cvt_pk_bf16_f32 v15, v30, v31
	v_pk_mul_f32 v[150:151], v[186:187], s[12:13] op_sel_hi:[1,0]
	v_permlane16_swap_b32_e32 v12, v14
	v_permlane16_swap_b32_e32 v13, v15
	global_store_dwordx4 v[16:17], v[12:15], off offset:256
	v_lshl_add_u64 v[16:17], s[4:5], 0, v[230:231]
	v_pk_mul_f32 v[152:153], v[184:185], s[12:13] op_sel_hi:[1,0]
	v_lshl_add_u64 v[16:17], v[16:17], 0, v[18:19]
	v_pk_fma_f32 v[20:21], v[148:149], s[14:15], v[142:143] op_sel_hi:[1,0,1]
	v_pk_fma_f32 v[22:23], v[146:147], s[14:15], v[144:145] op_sel_hi:[1,0,1]
	v_pk_fma_f32 v[140:141], v[140:141], s[14:15], v[150:151] op_sel_hi:[1,0,1]
	v_pk_fma_f32 v[138:139], v[138:139], s[14:15], v[152:153] op_sel_hi:[1,0,1]
	v_cvt_pk_bf16_f32 v12, v22, v23
	v_cvt_pk_bf16_f32 v13, v20, v21
	v_lshl_add_u64 v[16:17], v[16:17], 0, v[170:171]
	v_cvt_pk_bf16_f32 v14, v138, v139
	v_cvt_pk_bf16_f32 v15, v140, v141
	v_lshl_add_u64 v[16:17], v[16:17], 0, v[178:179]
	v_permlane16_swap_b32_e32 v12, v14
	v_permlane16_swap_b32_e32 v13, v15
	global_store_dwordx4 v[16:17], v[12:15], off
	v_pk_mul_f32 v[4:5], v[4:5], s[12:13] op_sel_hi:[1,0]
	v_pk_mul_f32 v[2:3], v[2:3], s[12:13] op_sel_hi:[1,0]
	v_pk_mul_f32 v[12:13], v[196:197], s[12:13] op_sel_hi:[1,0]
	v_pk_mul_f32 v[14:15], v[194:195], s[12:13] op_sel_hi:[1,0]
	v_pk_fma_f32 v[20:21], v[136:137], s[14:15], v[12:13] op_sel_hi:[1,0,1]
	v_pk_fma_f32 v[12:13], v[134:135], s[14:15], v[14:15] op_sel_hi:[1,0,1]
	v_pk_mul_f32 v[14:15], v[200:201], s[12:13] op_sel_hi:[1,0]
	v_cvt_pk_bf16_f32 v12, v12, v13
	v_cvt_pk_bf16_f32 v13, v20, v21
	v_pk_mul_f32 v[20:21], v[198:199], s[12:13] op_sel_hi:[1,0]
	v_pk_fma_f32 v[22:23], v[128:129], s[14:15], v[14:15] op_sel_hi:[1,0,1]
	v_pk_fma_f32 v[14:15], v[126:127], s[14:15], v[20:21] op_sel_hi:[1,0,1]
	v_add_u32_e32 v134, 0x80, v6
	v_cvt_pk_bf16_f32 v14, v14, v15
	v_cvt_pk_bf16_f32 v15, v22, v23
	v_pk_fma_f32 v[4:5], v[100:101], s[14:15], v[4:5] op_sel_hi:[1,0,1]
	v_permlane16_swap_b32_e32 v12, v14
	v_permlane16_swap_b32_e32 v13, v15
	global_store_dwordx4 v[16:17], v[12:15], off offset:256
	v_lshlrev_b64 v[16:17], 12, v[32:33]
	v_lshl_add_u64 v[16:17], s[4:5], 0, v[16:17]
	v_pk_mul_f32 v[12:13], v[204:205], s[12:13] op_sel_hi:[1,0]
	v_pk_mul_f32 v[14:15], v[202:203], s[12:13] op_sel_hi:[1,0]
	v_pk_fma_f32 v[20:21], v[132:133], s[14:15], v[12:13] op_sel_hi:[1,0,1]
	v_pk_fma_f32 v[12:13], v[130:131], s[14:15], v[14:15] op_sel_hi:[1,0,1]
	v_pk_mul_f32 v[14:15], v[208:209], s[12:13] op_sel_hi:[1,0]
	v_cvt_pk_bf16_f32 v12, v12, v13
	v_cvt_pk_bf16_f32 v13, v20, v21
	v_pk_mul_f32 v[20:21], v[206:207], s[12:13] op_sel_hi:[1,0]
	v_pk_fma_f32 v[22:23], v[124:125], s[14:15], v[14:15] op_sel_hi:[1,0,1]
	v_pk_fma_f32 v[14:15], v[122:123], s[14:15], v[20:21] op_sel_hi:[1,0,1]
	v_lshl_add_u64 v[16:17], v[16:17], 0, v[18:19]
	v_cvt_pk_bf16_f32 v14, v14, v15
	v_cvt_pk_bf16_f32 v15, v22, v23
	v_lshl_add_u64 v[16:17], v[16:17], 0, v[170:171]
	v_permlane16_swap_b32_e32 v12, v14
	v_permlane16_swap_b32_e32 v13, v15
	v_lshl_add_u64 v[16:17], v[16:17], 0, v[178:179]
	global_store_dwordx4 v[16:17], v[12:15], off
	v_pk_fma_f32 v[2:3], v[98:99], s[14:15], v[2:3] op_sel_hi:[1,0,1]
	v_ashrrev_i32_e32 v135, 31, v134
	v_pk_mul_f32 v[12:13], v[212:213], s[12:13] op_sel_hi:[1,0]
	v_pk_mul_f32 v[14:15], v[210:211], s[12:13] op_sel_hi:[1,0]
	v_pk_fma_f32 v[20:21], v[120:121], s[14:15], v[12:13] op_sel_hi:[1,0,1]
	v_pk_fma_f32 v[12:13], v[118:119], s[14:15], v[14:15] op_sel_hi:[1,0,1]
	v_pk_mul_f32 v[14:15], v[216:217], s[12:13] op_sel_hi:[1,0]
	v_cvt_pk_bf16_f32 v12, v12, v13
	v_cvt_pk_bf16_f32 v13, v20, v21
	v_pk_mul_f32 v[20:21], v[214:215], s[12:13] op_sel_hi:[1,0]
	v_pk_fma_f32 v[22:23], v[112:113], s[14:15], v[14:15] op_sel_hi:[1,0,1]
	v_pk_fma_f32 v[14:15], v[110:111], s[14:15], v[20:21] op_sel_hi:[1,0,1]
	v_add_u32_e32 v136, 0x90, v6
	v_cvt_pk_bf16_f32 v14, v14, v15
	v_cvt_pk_bf16_f32 v15, v22, v23
	v_ashrrev_i32_e32 v137, 31, v136
	v_permlane16_swap_b32_e32 v12, v14
	v_permlane16_swap_b32_e32 v13, v15
	global_store_dwordx4 v[16:17], v[12:15], off offset:256
	v_add_u32_e32 v138, 0xa0, v6
	v_ashrrev_i32_e32 v139, 31, v138
	v_lshlrev_b64 v[14:15], 12, v[10:11]
	v_pk_mul_f32 v[10:11], v[220:221], s[12:13] op_sel_hi:[1,0]
	v_pk_mul_f32 v[12:13], v[218:219], s[12:13] op_sel_hi:[1,0]
	v_pk_fma_f32 v[16:17], v[116:117], s[14:15], v[10:11] op_sel_hi:[1,0,1]
	v_pk_fma_f32 v[10:11], v[114:115], s[14:15], v[12:13] op_sel_hi:[1,0,1]
	v_pk_mul_f32 v[12:13], v[224:225], s[12:13] op_sel_hi:[1,0]
	v_cvt_pk_bf16_f32 v10, v10, v11
	v_cvt_pk_bf16_f32 v11, v16, v17
	v_pk_mul_f32 v[16:17], v[222:223], s[12:13] op_sel_hi:[1,0]
	v_lshl_add_u64 v[14:15], s[4:5], 0, v[14:15]
	v_pk_fma_f32 v[20:21], v[108:109], s[14:15], v[12:13] op_sel_hi:[1,0,1]
	v_pk_fma_f32 v[12:13], v[106:107], s[14:15], v[16:17] op_sel_hi:[1,0,1]
	v_lshl_add_u64 v[14:15], v[14:15], 0, v[18:19]
	v_cvt_pk_bf16_f32 v12, v12, v13
	v_cvt_pk_bf16_f32 v13, v20, v21
	v_lshl_add_u64 v[14:15], v[14:15], 0, v[170:171]
	v_permlane16_swap_b32_e32 v10, v12
	v_permlane16_swap_b32_e32 v11, v13
	v_lshl_add_u64 v[14:15], v[14:15], 0, v[178:179]
	global_store_dwordx4 v[14:15], v[10:13], off
	v_add_u32_e32 v20, 0xb0, v6
	v_ashrrev_i32_e32 v21, 31, v20
	v_pk_mul_f32 v[10:11], v[228:229], s[12:13] op_sel_hi:[1,0]
	v_pk_mul_f32 v[12:13], v[226:227], s[12:13] op_sel_hi:[1,0]
	v_pk_fma_f32 v[16:17], v[104:105], s[14:15], v[10:11] op_sel_hi:[1,0,1]
	v_pk_fma_f32 v[10:11], v[102:103], s[14:15], v[12:13] op_sel_hi:[1,0,1]
	s_nop 0
	v_cvt_pk_bf16_f32 v10, v10, v11
	v_cvt_pk_bf16_f32 v11, v16, v17
	v_cvt_pk_bf16_f32 v12, v2, v3
	v_cvt_pk_bf16_f32 v13, v4, v5
	v_lshlrev_b64 v[2:3], 13, v[134:135]
	v_permlane16_swap_b32_e32 v10, v12
	v_permlane16_swap_b32_e32 v11, v13
	global_store_dwordx4 v[14:15], v[10:13], off offset:256
	v_lshl_add_u64 v[2:3], v[8:9], 0, v[2:3]
	global_load_dwordx4 v[22:25], v[2:3], off nt
	global_load_dwordx4 v[26:29], v[2:3], off offset:64 nt
	global_load_dwordx4 v[30:33], v[2:3], off offset:512 nt
	global_load_dwordx4 v[98:101], v[2:3], off offset:576 nt
	v_lshlrev_b64 v[2:3], 13, v[136:137]
	v_lshl_add_u64 v[2:3], v[8:9], 0, v[2:3]
	global_load_dwordx4 v[102:105], v[2:3], off nt
	global_load_dwordx4 v[106:109], v[2:3], off offset:64 nt
	global_load_dwordx4 v[110:113], v[2:3], off offset:512 nt
	global_load_dwordx4 v[114:117], v[2:3], off offset:576 nt
	v_lshlrev_b64 v[2:3], 13, v[138:139]
	v_lshl_add_u64 v[2:3], v[8:9], 0, v[2:3]
	global_load_dwordx4 v[118:121], v[2:3], off nt
	global_load_dwordx4 v[122:125], v[2:3], off offset:64 nt
	global_load_dwordx4 v[126:129], v[2:3], off offset:512 nt
	global_load_dwordx4 v[130:133], v[2:3], off offset:576 nt
	v_lshlrev_b64 v[2:3], 13, v[20:21]
	v_lshl_add_u64 v[2:3], v[8:9], 0, v[2:3]
	global_load_dwordx4 v[14:17], v[2:3], off nt
	global_load_dwordx4 v[10:13], v[2:3], off offset:64 nt
	global_load_dwordx4 v[6:9], v[2:3], off offset:512 nt
	s_nop 0
	global_load_dwordx4 v[2:5], v[2:3], off offset:576 nt
	v_lshlrev_b64 v[134:135], 12, v[134:135]
	v_lshlrev_b64 v[20:21], 12, v[20:21]
	s_waitcnt vmcnt(15)
	v_pk_mul_f32 v[24:25], v[24:25], s[12:13] op_sel_hi:[1,0]
	v_pk_mul_f32 v[22:23], v[22:23], s[12:13] op_sel_hi:[1,0]
	v_pk_fma_f32 v[24:25], v[88:89], s[14:15], v[24:25] op_sel_hi:[1,0,1]
	v_pk_fma_f32 v[22:23], v[86:87], s[14:15], v[22:23] op_sel_hi:[1,0,1]
	s_waitcnt vmcnt(14)
	v_pk_mul_f32 v[26:27], v[26:27], s[12:13] op_sel_hi:[1,0]
	v_cvt_pk_bf16_f32 v22, v22, v23
	v_cvt_pk_bf16_f32 v23, v24, v25
	v_pk_mul_f32 v[24:25], v[28:29], s[12:13] op_sel_hi:[1,0]
	s_waitcnt vmcnt(3)
	v_pk_mul_f32 v[16:17], v[16:17], s[12:13] op_sel_hi:[1,0]
	v_pk_fma_f32 v[28:29], v[84:85], s[14:15], v[24:25] op_sel_hi:[1,0,1]
	v_pk_fma_f32 v[24:25], v[82:83], s[14:15], v[26:27] op_sel_hi:[1,0,1]
	v_lshl_add_u64 v[26:27], s[4:5], 0, v[134:135]
	v_lshl_add_u64 v[26:27], v[26:27], 0, v[18:19]
	v_cvt_pk_bf16_f32 v24, v24, v25
	v_cvt_pk_bf16_f32 v25, v28, v29
	v_lshl_add_u64 v[26:27], v[26:27], 0, v[170:171]
	v_permlane16_swap_b32_e32 v22, v24
	v_permlane16_swap_b32_e32 v23, v25
	v_lshl_add_u64 v[26:27], v[26:27], 0, v[178:179]
	global_store_dwordx4 v[26:27], v[22:25], off
	v_pk_mul_f32 v[14:15], v[14:15], s[12:13] op_sel_hi:[1,0]
	s_waitcnt vmcnt(3)
	v_pk_mul_f32 v[10:11], v[10:11], s[12:13] op_sel_hi:[1,0]
	v_pk_mul_f32 v[22:23], v[32:33], s[12:13] op_sel_hi:[1,0]
	v_pk_mul_f32 v[24:25], v[30:31], s[12:13] op_sel_hi:[1,0]
	v_pk_fma_f32 v[28:29], v[96:97], s[14:15], v[22:23] op_sel_hi:[1,0,1]
	v_pk_fma_f32 v[22:23], v[94:95], s[14:15], v[24:25] op_sel_hi:[1,0,1]
	v_pk_mul_f32 v[24:25], v[100:101], s[12:13] op_sel_hi:[1,0]
	v_cvt_pk_bf16_f32 v22, v22, v23
	v_cvt_pk_bf16_f32 v23, v28, v29
	v_pk_mul_f32 v[28:29], v[98:99], s[12:13] op_sel_hi:[1,0]
	v_pk_fma_f32 v[30:31], v[92:93], s[14:15], v[24:25] op_sel_hi:[1,0,1]
	v_pk_fma_f32 v[24:25], v[90:91], s[14:15], v[28:29] op_sel_hi:[1,0,1]
	v_pk_fma_f32 v[16:17], v[40:41], s[14:15], v[16:17] op_sel_hi:[1,0,1]
	v_cvt_pk_bf16_f32 v24, v24, v25
	v_cvt_pk_bf16_f32 v25, v30, v31
	v_pk_fma_f32 v[14:15], v[38:39], s[14:15], v[14:15] op_sel_hi:[1,0,1]
	v_permlane16_swap_b32_e32 v22, v24
	v_permlane16_swap_b32_e32 v23, v25
	global_store_dwordx4 v[26:27], v[22:25], off offset:256
	v_lshlrev_b64 v[26:27], 12, v[136:137]
	v_lshl_add_u64 v[26:27], s[4:5], 0, v[26:27]
	v_pk_mul_f32 v[22:23], v[104:105], s[12:13] op_sel_hi:[1,0]
	v_pk_mul_f32 v[24:25], v[102:103], s[12:13] op_sel_hi:[1,0]
	v_pk_fma_f32 v[28:29], v[72:73], s[14:15], v[22:23] op_sel_hi:[1,0,1]
	v_pk_fma_f32 v[22:23], v[70:71], s[14:15], v[24:25] op_sel_hi:[1,0,1]
	v_pk_mul_f32 v[24:25], v[108:109], s[12:13] op_sel_hi:[1,0]
	v_cvt_pk_bf16_f32 v22, v22, v23
	v_cvt_pk_bf16_f32 v23, v28, v29
	v_pk_mul_f32 v[28:29], v[106:107], s[12:13] op_sel_hi:[1,0]
	v_pk_fma_f32 v[30:31], v[68:69], s[14:15], v[24:25] op_sel_hi:[1,0,1]
	v_pk_fma_f32 v[24:25], v[66:67], s[14:15], v[28:29] op_sel_hi:[1,0,1]
	v_lshl_add_u64 v[26:27], v[26:27], 0, v[18:19]
	v_cvt_pk_bf16_f32 v24, v24, v25
	v_cvt_pk_bf16_f32 v25, v30, v31
	v_lshl_add_u64 v[26:27], v[26:27], 0, v[170:171]
	v_permlane16_swap_b32_e32 v22, v24
	v_permlane16_swap_b32_e32 v23, v25
	v_lshl_add_u64 v[26:27], v[26:27], 0, v[178:179]
	global_store_dwordx4 v[26:27], v[22:25], off
	v_pk_fma_f32 v[10:11], v[34:35], s[14:15], v[10:11] op_sel_hi:[1,0,1]
	v_pk_mul_f32 v[12:13], v[12:13], s[12:13] op_sel_hi:[1,0]
	v_pk_mul_f32 v[22:23], v[112:113], s[12:13] op_sel_hi:[1,0]
	v_pk_mul_f32 v[24:25], v[110:111], s[12:13] op_sel_hi:[1,0]
	v_pk_fma_f32 v[28:29], v[80:81], s[14:15], v[22:23] op_sel_hi:[1,0,1]
	v_pk_fma_f32 v[22:23], v[78:79], s[14:15], v[24:25] op_sel_hi:[1,0,1]
	v_pk_mul_f32 v[24:25], v[116:117], s[12:13] op_sel_hi:[1,0]
	v_cvt_pk_bf16_f32 v22, v22, v23
	v_cvt_pk_bf16_f32 v23, v28, v29
	v_pk_mul_f32 v[28:29], v[114:115], s[12:13] op_sel_hi:[1,0]
	v_pk_fma_f32 v[30:31], v[76:77], s[14:15], v[24:25] op_sel_hi:[1,0,1]
	v_pk_fma_f32 v[24:25], v[74:75], s[14:15], v[28:29] op_sel_hi:[1,0,1]
	v_pk_fma_f32 v[12:13], v[36:37], s[14:15], v[12:13] op_sel_hi:[1,0,1]
	v_cvt_pk_bf16_f32 v24, v24, v25
	v_cvt_pk_bf16_f32 v25, v30, v31
	s_waitcnt vmcnt(4)
	v_pk_mul_f32 v[8:9], v[8:9], s[12:13] op_sel_hi:[1,0]
	v_permlane16_swap_b32_e32 v22, v24
	v_permlane16_swap_b32_e32 v23, v25
	global_store_dwordx4 v[26:27], v[22:25], off offset:256
	v_lshlrev_b64 v[26:27], 12, v[138:139]
	v_lshl_add_u64 v[26:27], s[4:5], 0, v[26:27]
	v_pk_mul_f32 v[22:23], v[120:121], s[12:13] op_sel_hi:[1,0]
	v_pk_mul_f32 v[24:25], v[118:119], s[12:13] op_sel_hi:[1,0]
	v_pk_fma_f32 v[28:29], v[56:57], s[14:15], v[22:23] op_sel_hi:[1,0,1]
	v_pk_fma_f32 v[22:23], v[54:55], s[14:15], v[24:25] op_sel_hi:[1,0,1]
	v_pk_mul_f32 v[24:25], v[124:125], s[12:13] op_sel_hi:[1,0]
	v_cvt_pk_bf16_f32 v22, v22, v23
	v_cvt_pk_bf16_f32 v23, v28, v29
	v_pk_mul_f32 v[28:29], v[122:123], s[12:13] op_sel_hi:[1,0]
	v_pk_fma_f32 v[30:31], v[52:53], s[14:15], v[24:25] op_sel_hi:[1,0,1]
	v_pk_fma_f32 v[24:25], v[50:51], s[14:15], v[28:29] op_sel_hi:[1,0,1]
	v_lshl_add_u64 v[26:27], v[26:27], 0, v[18:19]
	v_cvt_pk_bf16_f32 v24, v24, v25
	v_cvt_pk_bf16_f32 v25, v30, v31
	v_lshl_add_u64 v[26:27], v[26:27], 0, v[170:171]
	v_permlane16_swap_b32_e32 v22, v24
	v_permlane16_swap_b32_e32 v23, v25
	v_lshl_add_u64 v[26:27], v[26:27], 0, v[178:179]
	global_store_dwordx4 v[26:27], v[22:25], off
	v_pk_mul_f32 v[6:7], v[6:7], s[12:13] op_sel_hi:[1,0]
	v_pk_fma_f32 v[8:9], v[48:49], s[14:15], v[8:9] op_sel_hi:[1,0,1]
	v_pk_mul_f32 v[22:23], v[128:129], s[12:13] op_sel_hi:[1,0]
	v_pk_mul_f32 v[24:25], v[126:127], s[12:13] op_sel_hi:[1,0]
	v_pk_fma_f32 v[28:29], v[64:65], s[14:15], v[22:23] op_sel_hi:[1,0,1]
	v_pk_fma_f32 v[22:23], v[62:63], s[14:15], v[24:25] op_sel_hi:[1,0,1]
	v_pk_mul_f32 v[24:25], v[132:133], s[12:13] op_sel_hi:[1,0]
	v_cvt_pk_bf16_f32 v22, v22, v23
	v_cvt_pk_bf16_f32 v23, v28, v29
	v_pk_mul_f32 v[28:29], v[130:131], s[12:13] op_sel_hi:[1,0]
	v_pk_fma_f32 v[30:31], v[60:61], s[14:15], v[24:25] op_sel_hi:[1,0,1]
	v_pk_fma_f32 v[24:25], v[58:59], s[14:15], v[28:29] op_sel_hi:[1,0,1]
	v_pk_fma_f32 v[6:7], v[46:47], s[14:15], v[6:7] op_sel_hi:[1,0,1]
	v_cvt_pk_bf16_f32 v24, v24, v25
	v_cvt_pk_bf16_f32 v25, v30, v31
	s_waitcnt vmcnt(5)
	v_pk_mul_f32 v[4:5], v[4:5], s[12:13] op_sel_hi:[1,0]
	v_permlane16_swap_b32_e32 v22, v24
	v_permlane16_swap_b32_e32 v23, v25
	global_store_dwordx4 v[26:27], v[22:25], off offset:256
	v_cvt_pk_bf16_f32 v14, v14, v15
	v_cvt_pk_bf16_f32 v15, v16, v17
	v_cvt_pk_bf16_f32 v16, v10, v11
	v_lshl_add_u64 v[10:11], s[4:5], 0, v[20:21]
	v_lshl_add_u64 v[10:11], v[10:11], 0, v[18:19]
	v_cvt_pk_bf16_f32 v17, v12, v13
	v_lshl_add_u64 v[10:11], v[10:11], 0, v[170:171]
	v_permlane16_swap_b32_e32 v14, v16
	v_permlane16_swap_b32_e32 v15, v17
	v_lshl_add_u64 v[10:11], v[10:11], 0, v[178:179]
	v_pk_mul_f32 v[2:3], v[2:3], s[12:13] op_sel_hi:[1,0]
	global_store_dwordx4 v[10:11], v[14:17], off
	v_cvt_pk_bf16_f32 v6, v6, v7
	v_cvt_pk_bf16_f32 v7, v8, v9
	v_pk_fma_f32 v[4:5], v[44:45], s[14:15], v[4:5] op_sel_hi:[1,0,1]
	v_pk_fma_f32 v[2:3], v[42:43], s[14:15], v[2:3] op_sel_hi:[1,0,1]
	s_nop 0
	v_cvt_pk_bf16_f32 v8, v2, v3
	v_cvt_pk_bf16_f32 v9, v4, v5
	s_nop 0
	v_permlane16_swap_b32_e32 v6, v8
	v_permlane16_swap_b32_e32 v7, v9
	global_store_dwordx4 v[10:11], v[6:9], off offset:256
	s_cbranch_vccnz .LBB0_625
	s_andn2_b64 vcc, exec, s[0:1]
	s_cbranch_vccnz .LBB0_624
	s_barrier
	s_branch .LBB0_624

.LBB0_916:
	s_xor_b64 s[38:39], s[10:11], -1
	v_mov_b32_e32 v68, v67
	v_mov_b32_e32 v69, v67
	v_mov_b32_e32 v211, v67
	v_mov_b32_e32 v209, v67
	s_add_u32 s25, s8, 0x100
	v_mov_b32_e32 v66, v67
	v_mov_b32_e32 v142, 0
	v_mov_b64_e32 v[112:113], v[68:69]
	v_mov_b64_e32 v[104:105], v[68:69]
	v_mov_b64_e32 v[120:121], v[68:69]
	v_mov_b64_e32 v[124:125], v[68:69]
	v_mov_b64_e32 v[80:81], v[68:69]
	v_mov_b64_e32 v[72:73], v[68:69]
	v_mov_b64_e32 v[92:93], v[68:69]
	v_mov_b64_e32 v[100:101], v[68:69]
	v_mov_b64_e32 v[116:117], v[68:69]
	v_mov_b64_e32 v[108:109], v[68:69]
	v_mov_b64_e32 v[128:129], v[68:69]
	v_mov_b64_e32 v[132:133], v[68:69]
	v_mov_b64_e32 v[96:97], v[68:69]
	v_mov_b64_e32 v[88:89], v[68:69]
	v_mov_b64_e32 v[76:77], v[68:69]
	v_mov_b64_e32 v[84:85], v[68:69]
	s_addc_u32 s27, s9, 0
	v_lshl_add_u64 v[216:217], s[16:17], 0, v[210:211]
	v_lshl_add_u64 v[218:219], s[16:17], 0, v[208:209]
	s_mov_b32 s61, -2
	s_mov_b64 s[40:41], 0
	v_cndmask_b32_e64 v201, 0, 1, s[38:39]
	v_mov_b64_e32 v[110:111], v[66:67]
	v_mov_b64_e32 v[102:103], v[66:67]
	v_mov_b64_e32 v[118:119], v[66:67]
	v_mov_b64_e32 v[122:123], v[66:67]
	v_mov_b64_e32 v[78:79], v[66:67]
	v_mov_b64_e32 v[70:71], v[66:67]
	v_mov_b64_e32 v[90:91], v[66:67]
	v_mov_b64_e32 v[98:99], v[66:67]
	v_mov_b64_e32 v[114:115], v[66:67]
	v_mov_b64_e32 v[106:107], v[66:67]
	v_mov_b64_e32 v[126:127], v[66:67]
	v_mov_b64_e32 v[130:131], v[66:67]
	v_mov_b64_e32 v[94:95], v[66:67]
	v_mov_b64_e32 v[86:87], v[66:67]
	v_mov_b64_e32 v[74:75], v[66:67]
	v_mov_b64_e32 v[82:83], v[66:67]
	v_mov_b64_e32 v[134:135], 0
	v_mov_b64_e32 v[136:137], 0
	v_mov_b64_e32 v[138:139], 0
	v_mov_b64_e32 v[140:141], 0
	v_mov_b32_e32 v143, v142
	v_mov_b64_e32 v[144:145], 0
	v_mov_b64_e32 v[146:147], 0
	v_mov_b64_e32 v[148:149], 0
	v_mov_b64_e32 v[150:151], 0
	v_mov_b64_e32 v[152:153], 0
	v_mov_b64_e32 v[154:155], 0
	v_mov_b64_e32 v[156:157], 0
	v_mov_b64_e32 v[158:159], 0
	v_mov_b64_e32 v[160:161], 0
	v_mov_b64_e32 v[162:163], 0
	v_mov_b64_e32 v[164:165], 0
	v_mov_b64_e32 v[166:167], 0
	v_mov_b64_e32 v[168:169], 0
	v_mov_b64_e32 v[170:171], 0
	v_mov_b64_e32 v[172:173], 0
	v_mov_b64_e32 v[174:175], 0
	v_mov_b64_e32 v[176:177], 0
	v_mov_b64_e32 v[178:179], 0
	v_mov_b64_e32 v[180:181], 0
	v_mov_b64_e32 v[182:183], 0
	v_mov_b64_e32 v[184:185], 0
	v_mov_b64_e32 v[186:187], 0
	v_mov_b64_e32 v[188:189], 0
	v_mov_b64_e32 v[190:191], 0
	v_mov_b64_e32 v[192:193], 0
	v_mov_b64_e32 v[194:195], 0
	v_mov_b64_e32 v[196:197], 0
	s_branch .LBB0_918

.LBB0_926:
	s_add_i32 s8, s30, 0x25100
	v_mov_b32_e32 v2, s8
	s_lshl_b32 s8, s31, 11
	s_and_b32 s8, s8, 0x800
	s_nop 11
	v_add_u32_e32 v11, s8, v228
	ds_read_b32 v10, v2
	ds_read_b128 v[6:9], v11 offset:16
	ds_read_b128 v[14:17], v11 offset:512
	ds_read_b128 v[2:5], v11
	ds_read_b128 v[18:21], v11 offset:528
	s_and_b64 vcc, exec, s[6:7]
	s_waitcnt lgkmcnt(0)
	v_pk_fma_f32 v[26:27], v[190:191], s[20:21], v[6:7] op_sel_hi:[1,0,1]
	v_pk_add_f32 v[12:13], v[16:17], 1.0 op_sel_hi:[1,0]
	v_pk_fma_f32 v[22:23], v[194:195], s[20:21], v[2:3] op_sel_hi:[1,0,1]
	v_pk_add_f32 v[16:17], v[20:21], 1.0 op_sel_hi:[1,0]
	v_pk_fma_f32 v[20:21], v[196:197], s[20:21], v[4:5] op_sel_hi:[1,0,1]
	v_min_f32_e32 v22, 0x40e00000, v22
	v_min_f32_e32 v20, 0x40e00000, v20
	v_min_f32_e32 v21, 0x40e00000, v21
	v_min_f32_e32 v26, 0x40e00000, v26
	v_min_f32_e32 v23, 0x40e00000, v23
	v_min_f32_e32 v27, 0x40e00000, v27
	v_pk_mul_f32 v[36:37], v[20:21], s[22:23] op_sel_hi:[1,0]
	v_pk_mul_f32 v[38:39], v[22:23], s[22:23] op_sel_hi:[1,0]
	v_pk_mul_f32 v[42:43], v[26:27], s[22:23] op_sel_hi:[1,0]
	v_exp_f32_e32 v36, v36
	v_exp_f32_e32 v37, v37
	v_exp_f32_e32 v38, v38
	v_exp_f32_e32 v42, v42
	v_exp_f32_e32 v39, v39
	v_exp_f32_e32 v43, v43
	v_pk_add_f32 v[36:37], v[36:37], 1.0 op_sel_hi:[1,0]
	v_pk_fma_f32 v[24:25], v[192:193], s[20:21], v[8:9] op_sel_hi:[1,0,1]
	v_pk_add_f32 v[38:39], v[38:39], 1.0 op_sel_hi:[1,0]
	v_pk_add_f32 v[42:43], v[42:43], 1.0 op_sel_hi:[1,0]
	v_rcp_f32_e32 v36, v36
	v_rcp_f32_e32 v37, v37
	v_min_f32_e32 v24, 0x40e00000, v24
	v_min_f32_e32 v25, 0x40e00000, v25
	v_rcp_f32_e32 v38, v38
	v_rcp_f32_e32 v42, v42
	v_rcp_f32_e32 v39, v39
	v_rcp_f32_e32 v43, v43
	v_pk_mul_f32 v[40:41], v[24:25], s[22:23] op_sel_hi:[1,0]
	v_pk_add_f32 v[14:15], v[14:15], 1.0 op_sel_hi:[1,0]
	v_pk_add_f32 v[18:19], v[18:19], 1.0 op_sel_hi:[1,0]
	v_pk_fma_f32 v[28:29], v[188:189], s[20:21], v[12:13] op_sel_hi:[1,0,1]
	v_exp_f32_e32 v40, v40
	v_exp_f32_e32 v41, v41
	v_pk_fma_f32 v[30:31], v[186:187], s[20:21], v[14:15] op_sel_hi:[1,0,1]
	v_pk_fma_f32 v[34:35], v[182:183], s[20:21], v[18:19] op_sel_hi:[1,0,1]
	v_med3_f32 v28, v28, s56, v235
	v_med3_f32 v29, v29, s56, v235
	v_pk_mul_f32 v[20:21], v[20:21], v[36:37]
	v_med3_f32 v30, v30, s56, v235
	v_med3_f32 v34, v34, s56, v235
	v_med3_f32 v31, v31, s56, v235
	v_med3_f32 v35, v35, s56, v235
	v_pk_mul_f32 v[22:23], v[22:23], v[38:39]
	v_pk_mul_f32 v[28:29], v[28:29], v[20:21]
	v_pk_mul_f32 v[20:21], v[26:27], v[42:43]
	v_pk_mul_f32 v[22:23], v[30:31], v[22:23]
	v_pk_mul_f32 v[26:27], v[34:35], v[20:21]
	v_mov_b32_e32 v20, v67
	v_pk_add_f32 v[40:41], v[40:41], 1.0 op_sel_hi:[1,0]
	v_cvt_pk_fp8_f32 v20, v22, v23
	v_rcp_f32_e32 v40, v40
	v_rcp_f32_e32 v41, v41
	v_pk_fma_f32 v[32:33], v[184:185], s[20:21], v[16:17] op_sel_hi:[1,0,1]
	v_cvt_pk_fp8_f32 v20, v28, v29 op_sel:[0,0,1]
	v_pk_fma_f32 v[28:29], v[178:179], s[20:21], v[6:7] op_sel_hi:[1,0,1]
	v_med3_f32 v32, v32, s56, v235
	v_med3_f32 v33, v33, s56, v235
	v_pk_mul_f32 v[22:23], v[24:25], v[40:41]
	v_min_f32_e32 v28, 0x40e00000, v28
	v_min_f32_e32 v29, 0x40e00000, v29
	v_pk_mul_f32 v[22:23], v[32:33], v[22:23]
	v_pk_mul_f32 v[32:33], v[28:29], s[22:23] op_sel_hi:[1,0]
	v_mov_b32_e32 v21, v67
	v_exp_f32_e32 v32, v32
	v_exp_f32_e32 v33, v33
	v_cvt_pk_fp8_f32 v21, v26, v27
	v_pk_fma_f32 v[26:27], v[180:181], s[20:21], v[8:9] op_sel_hi:[1,0,1]
	v_pk_fma_f32 v[24:25], v[174:175], s[20:21], v[18:19] op_sel_hi:[1,0,1]
	v_min_f32_e32 v26, 0x40e00000, v26
	v_min_f32_e32 v27, 0x40e00000, v27
	v_pk_mul_f32 v[30:31], v[26:27], s[22:23] op_sel_hi:[1,0]
	v_pk_add_f32 v[32:33], v[32:33], 1.0 op_sel_hi:[1,0]
	v_exp_f32_e32 v30, v30
	v_exp_f32_e32 v31, v31
	v_rcp_f32_e32 v32, v32
	v_rcp_f32_e32 v33, v33
	v_cvt_pk_fp8_f32 v21, v22, v23 op_sel:[0,0,1]
	v_pk_fma_f32 v[22:23], v[176:177], s[20:21], v[16:17] op_sel_hi:[1,0,1]
	v_pk_add_f32 v[30:31], v[30:31], 1.0 op_sel_hi:[1,0]
	v_med3_f32 v34, v22, s56, v235
	v_rcp_f32_e32 v30, v30
	v_rcp_f32_e32 v31, v31
	v_med3_f32 v35, v23, s56, v235
	v_pk_mul_f32 v[22:23], v[28:29], v[32:33]
	v_pk_fma_f32 v[32:33], v[170:171], s[20:21], v[2:3] op_sel_hi:[1,0,1]
	v_pk_mul_f32 v[26:27], v[26:27], v[30:31]
	v_min_f32_e32 v32, 0x40e00000, v32
	v_min_f32_e32 v33, 0x40e00000, v33
	v_pk_mul_f32 v[36:37], v[32:33], s[22:23] op_sel_hi:[1,0]
	v_pk_fma_f32 v[30:31], v[172:173], s[20:21], v[4:5] op_sel_hi:[1,0,1]
	v_exp_f32_e32 v36, v36
	v_exp_f32_e32 v37, v37
	v_min_f32_e32 v30, 0x40e00000, v30
	v_min_f32_e32 v31, 0x40e00000, v31
	v_pk_mul_f32 v[38:39], v[30:31], s[22:23] op_sel_hi:[1,0]
	v_pk_add_f32 v[36:37], v[36:37], 1.0 op_sel_hi:[1,0]
	v_exp_f32_e32 v38, v38
	v_exp_f32_e32 v39, v39
	v_rcp_f32_e32 v36, v36
	v_rcp_f32_e32 v37, v37
	v_pk_fma_f32 v[28:29], v[166:167], s[20:21], v[14:15] op_sel_hi:[1,0,1]
	v_pk_add_f32 v[38:39], v[38:39], 1.0 op_sel_hi:[1,0]
	v_med3_f32 v24, v24, s56, v235
	v_med3_f32 v25, v25, s56, v235
	v_med3_f32 v28, v28, s56, v235
	v_med3_f32 v29, v29, s56, v235
	v_rcp_f32_e32 v38, v38
	v_rcp_f32_e32 v39, v39
	v_pk_mul_f32 v[32:33], v[32:33], v[36:37]
	v_pk_mul_f32 v[24:25], v[24:25], v[22:23]
	v_pk_mul_f32 v[28:29], v[28:29], v[32:33]
	v_mov_b32_e32 v22, v67
	v_mov_b32_e32 v23, v67
	v_cvt_pk_fp8_f32 v22, v28, v29
	v_cvt_pk_fp8_f32 v23, v24, v25
	v_pk_fma_f32 v[24:25], v[168:169], s[20:21], v[12:13] op_sel_hi:[1,0,1]
	v_pk_mul_f32 v[28:29], v[30:31], v[38:39]
	v_med3_f32 v24, v24, s56, v235
	v_med3_f32 v25, v25, s56, v235
	v_add_u32_e32 v11, s60, v10
	v_pk_mul_f32 v[24:25], v[24:25], v[28:29]
	v_lshl_add_u32 v44, v11, 8, v213
	v_cvt_pk_fp8_f32 v22, v24, v25 op_sel:[0,0,1]
	v_pk_mul_f32 v[24:25], v[34:35], v[26:27]
	v_lshl_or_b32 v10, s34, 7, v231
	v_cvt_pk_fp8_f32 v23, v24, v25 op_sel:[0,0,1]
	v_or_b32_e32 v24, v44, v229
	v_ashrrev_i32_e32 v25, 31, v24
	v_lshlrev_b64 v[24:25], 11, v[24:25]
	v_ashrrev_i32_e32 v11, 31, v10
	v_lshl_add_u64 v[24:25], s[14:15], 0, v[24:25]
	v_lshl_add_u64 v[24:25], v[24:25], 0, v[10:11]
	v_permlane16_swap_b32_e32 v20, v22
	v_permlane16_swap_b32_e32 v21, v23
	v_lshl_add_u64 v[24:25], v[24:25], 0, v[204:205]
	global_store_dwordx4 v[24:25], v[20:23], off
	v_pk_fma_f32 v[26:27], v[158:159], s[20:21], v[6:7] op_sel_hi:[1,0,1]
	v_pk_fma_f32 v[24:25], v[160:161], s[20:21], v[8:9] op_sel_hi:[1,0,1]
	v_pk_fma_f32 v[20:21], v[164:165], s[20:21], v[4:5] op_sel_hi:[1,0,1]
	v_pk_fma_f32 v[22:23], v[162:163], s[20:21], v[2:3] op_sel_hi:[1,0,1]
	v_min_f32_e32 v20, 0x40e00000, v20
	v_min_f32_e32 v21, 0x40e00000, v21
	v_min_f32_e32 v22, 0x40e00000, v22
	v_min_f32_e32 v26, 0x40e00000, v26
	v_min_f32_e32 v23, 0x40e00000, v23
	v_min_f32_e32 v27, 0x40e00000, v27
	v_pk_mul_f32 v[36:37], v[20:21], s[22:23] op_sel_hi:[1,0]
	v_pk_mul_f32 v[38:39], v[22:23], s[22:23] op_sel_hi:[1,0]
	v_pk_mul_f32 v[42:43], v[26:27], s[22:23] op_sel_hi:[1,0]
	v_exp_f32_e32 v36, v36
	v_exp_f32_e32 v37, v37
	v_exp_f32_e32 v38, v38
	v_exp_f32_e32 v42, v42
	v_exp_f32_e32 v39, v39
	v_exp_f32_e32 v43, v43
	v_pk_add_f32 v[36:37], v[36:37], 1.0 op_sel_hi:[1,0]
	v_min_f32_e32 v24, 0x40e00000, v24
	v_pk_add_f32 v[38:39], v[38:39], 1.0 op_sel_hi:[1,0]
	v_pk_add_f32 v[42:43], v[42:43], 1.0 op_sel_hi:[1,0]
	v_rcp_f32_e32 v36, v36
	v_rcp_f32_e32 v37, v37
	v_min_f32_e32 v25, 0x40e00000, v25
	v_rcp_f32_e32 v38, v38
	v_rcp_f32_e32 v42, v42
	v_rcp_f32_e32 v39, v39
	v_rcp_f32_e32 v43, v43
	v_pk_mul_f32 v[40:41], v[24:25], s[22:23] op_sel_hi:[1,0]
	v_pk_fma_f32 v[28:29], v[156:157], s[20:21], v[12:13] op_sel_hi:[1,0,1]
	v_exp_f32_e32 v40, v40
	v_exp_f32_e32 v41, v41
	v_pk_fma_f32 v[30:31], v[154:155], s[20:21], v[14:15] op_sel_hi:[1,0,1]
	v_pk_fma_f32 v[34:35], v[150:151], s[20:21], v[18:19] op_sel_hi:[1,0,1]
	v_med3_f32 v28, v28, s56, v235
	v_med3_f32 v29, v29, s56, v235
	v_pk_mul_f32 v[20:21], v[20:21], v[36:37]
	v_med3_f32 v30, v30, s56, v235
	v_med3_f32 v34, v34, s56, v235
	v_med3_f32 v31, v31, s56, v235
	v_med3_f32 v35, v35, s56, v235
	v_pk_mul_f32 v[22:23], v[22:23], v[38:39]
	v_pk_mul_f32 v[28:29], v[28:29], v[20:21]
	v_pk_mul_f32 v[20:21], v[26:27], v[42:43]
	v_pk_mul_f32 v[22:23], v[30:31], v[22:23]
	v_pk_mul_f32 v[26:27], v[34:35], v[20:21]
	v_mov_b32_e32 v20, v67
	v_pk_add_f32 v[40:41], v[40:41], 1.0 op_sel_hi:[1,0]
	v_cvt_pk_fp8_f32 v20, v22, v23
	v_rcp_f32_e32 v40, v40
	v_rcp_f32_e32 v41, v41
	v_pk_fma_f32 v[32:33], v[152:153], s[20:21], v[16:17] op_sel_hi:[1,0,1]
	v_cvt_pk_fp8_f32 v20, v28, v29 op_sel:[0,0,1]
	v_pk_fma_f32 v[28:29], v[146:147], s[20:21], v[6:7] op_sel_hi:[1,0,1]
	v_med3_f32 v32, v32, s56, v235
	v_med3_f32 v33, v33, s56, v235
	v_pk_mul_f32 v[22:23], v[24:25], v[40:41]
	v_min_f32_e32 v28, 0x40e00000, v28
	v_min_f32_e32 v29, 0x40e00000, v29
	v_pk_mul_f32 v[22:23], v[32:33], v[22:23]
	v_pk_mul_f32 v[32:33], v[28:29], s[22:23] op_sel_hi:[1,0]
	v_mov_b32_e32 v21, v67
	v_exp_f32_e32 v32, v32
	v_exp_f32_e32 v33, v33
	v_cvt_pk_fp8_f32 v21, v26, v27
	v_pk_fma_f32 v[26:27], v[148:149], s[20:21], v[8:9] op_sel_hi:[1,0,1]
	v_pk_fma_f32 v[24:25], v[142:143], s[20:21], v[18:19] op_sel_hi:[1,0,1]
	v_min_f32_e32 v26, 0x40e00000, v26
	v_min_f32_e32 v27, 0x40e00000, v27
	v_pk_mul_f32 v[30:31], v[26:27], s[22:23] op_sel_hi:[1,0]
	v_pk_add_f32 v[32:33], v[32:33], 1.0 op_sel_hi:[1,0]
	v_exp_f32_e32 v30, v30
	v_exp_f32_e32 v31, v31
	v_rcp_f32_e32 v32, v32
	v_rcp_f32_e32 v33, v33
	v_cvt_pk_fp8_f32 v21, v22, v23 op_sel:[0,0,1]
	v_pk_fma_f32 v[22:23], v[144:145], s[20:21], v[16:17] op_sel_hi:[1,0,1]
	v_pk_add_f32 v[30:31], v[30:31], 1.0 op_sel_hi:[1,0]
	v_med3_f32 v34, v22, s56, v235
	v_rcp_f32_e32 v30, v30
	v_rcp_f32_e32 v31, v31
	v_med3_f32 v35, v23, s56, v235
	v_pk_mul_f32 v[22:23], v[28:29], v[32:33]
	v_pk_fma_f32 v[32:33], v[138:139], s[20:21], v[2:3] op_sel_hi:[1,0,1]
	v_pk_mul_f32 v[26:27], v[26:27], v[30:31]
	v_min_f32_e32 v32, 0x40e00000, v32
	v_min_f32_e32 v33, 0x40e00000, v33
	v_pk_mul_f32 v[36:37], v[32:33], s[22:23] op_sel_hi:[1,0]
	v_pk_fma_f32 v[30:31], v[140:141], s[20:21], v[4:5] op_sel_hi:[1,0,1]
	v_exp_f32_e32 v36, v36
	v_exp_f32_e32 v37, v37
	v_min_f32_e32 v30, 0x40e00000, v30
	v_min_f32_e32 v31, 0x40e00000, v31
	v_pk_mul_f32 v[38:39], v[30:31], s[22:23] op_sel_hi:[1,0]
	v_pk_add_f32 v[36:37], v[36:37], 1.0 op_sel_hi:[1,0]
	v_exp_f32_e32 v38, v38
	v_exp_f32_e32 v39, v39
	v_rcp_f32_e32 v36, v36
	v_rcp_f32_e32 v37, v37
	v_pk_fma_f32 v[28:29], v[134:135], s[20:21], v[14:15] op_sel_hi:[1,0,1]
	v_pk_add_f32 v[38:39], v[38:39], 1.0 op_sel_hi:[1,0]
	v_med3_f32 v24, v24, s56, v235
	v_med3_f32 v25, v25, s56, v235
	v_med3_f32 v28, v28, s56, v235
	v_med3_f32 v29, v29, s56, v235
	v_rcp_f32_e32 v38, v38
	v_rcp_f32_e32 v39, v39
	v_pk_mul_f32 v[32:33], v[32:33], v[36:37]
	v_pk_mul_f32 v[24:25], v[24:25], v[22:23]
	v_pk_mul_f32 v[28:29], v[28:29], v[32:33]
	v_mov_b32_e32 v22, v67
	v_mov_b32_e32 v23, v67
	v_cvt_pk_fp8_f32 v22, v28, v29
	v_cvt_pk_fp8_f32 v23, v24, v25
	v_pk_fma_f32 v[24:25], v[136:137], s[20:21], v[12:13] op_sel_hi:[1,0,1]
	v_pk_mul_f32 v[28:29], v[30:31], v[38:39]
	v_med3_f32 v24, v24, s56, v235
	v_med3_f32 v25, v25, s56, v235
	v_pk_mul_f32 v[24:25], v[24:25], v[28:29]
	v_pk_fma_f32 v[28:29], v[124:125], s[20:21], v[12:13] op_sel_hi:[1,0,1]
	v_cvt_pk_fp8_f32 v22, v24, v25 op_sel:[0,0,1]
	v_pk_mul_f32 v[24:25], v[34:35], v[26:27]
	v_pk_fma_f32 v[26:27], v[126:127], s[20:21], v[6:7] op_sel_hi:[1,0,1]
	v_cvt_pk_fp8_f32 v23, v24, v25 op_sel:[0,0,1]
	v_or_b32_e32 v24, v44, v230
	v_ashrrev_i32_e32 v25, 31, v24
	v_lshlrev_b64 v[24:25], 11, v[24:25]
	v_lshl_add_u64 v[24:25], s[14:15], 0, v[24:25]
	v_lshl_add_u64 v[24:25], v[24:25], 0, v[10:11]
	v_permlane16_swap_b32_e32 v20, v22
	v_permlane16_swap_b32_e32 v21, v23
	v_lshl_add_u64 v[24:25], v[24:25], 0, v[204:205]
	global_store_dwordx4 v[24:25], v[20:23], off
	v_min_f32_e32 v26, 0x40e00000, v26
	v_min_f32_e32 v27, 0x40e00000, v27
	v_pk_fma_f32 v[20:21], v[132:133], s[20:21], v[4:5] op_sel_hi:[1,0,1]
	v_pk_fma_f32 v[22:23], v[130:131], s[20:21], v[2:3] op_sel_hi:[1,0,1]
	v_min_f32_e32 v20, 0x40e00000, v20
	v_min_f32_e32 v21, 0x40e00000, v21
	v_min_f32_e32 v22, 0x40e00000, v22
	v_min_f32_e32 v23, 0x40e00000, v23
	v_pk_mul_f32 v[36:37], v[20:21], s[22:23] op_sel_hi:[1,0]
	v_pk_mul_f32 v[38:39], v[22:23], s[22:23] op_sel_hi:[1,0]
	v_pk_mul_f32 v[42:43], v[26:27], s[22:23] op_sel_hi:[1,0]
	v_exp_f32_e32 v36, v36
	v_exp_f32_e32 v37, v37
	v_exp_f32_e32 v38, v38
	v_exp_f32_e32 v42, v42
	v_exp_f32_e32 v39, v39
	v_exp_f32_e32 v43, v43
	v_pk_add_f32 v[36:37], v[36:37], 1.0 op_sel_hi:[1,0]
	v_pk_fma_f32 v[24:25], v[128:129], s[20:21], v[8:9] op_sel_hi:[1,0,1]
	v_pk_add_f32 v[38:39], v[38:39], 1.0 op_sel_hi:[1,0]
	v_pk_add_f32 v[42:43], v[42:43], 1.0 op_sel_hi:[1,0]
	v_rcp_f32_e32 v36, v36
	v_rcp_f32_e32 v37, v37
	v_min_f32_e32 v24, 0x40e00000, v24
	v_min_f32_e32 v25, 0x40e00000, v25
	v_rcp_f32_e32 v38, v38
	v_rcp_f32_e32 v42, v42
	v_rcp_f32_e32 v39, v39
	v_rcp_f32_e32 v43, v43
	v_pk_mul_f32 v[40:41], v[24:25], s[22:23] op_sel_hi:[1,0]
	v_pk_fma_f32 v[30:31], v[122:123], s[20:21], v[14:15] op_sel_hi:[1,0,1]
	v_exp_f32_e32 v40, v40
	v_exp_f32_e32 v41, v41
	v_pk_fma_f32 v[34:35], v[118:119], s[20:21], v[18:19] op_sel_hi:[1,0,1]
	v_med3_f32 v28, v28, s56, v235
	v_med3_f32 v29, v29, s56, v235
	v_pk_mul_f32 v[20:21], v[20:21], v[36:37]
	v_med3_f32 v30, v30, s56, v235
	v_med3_f32 v34, v34, s56, v235
	v_med3_f32 v31, v31, s56, v235
	v_med3_f32 v35, v35, s56, v235
	v_pk_mul_f32 v[22:23], v[22:23], v[38:39]
	v_pk_mul_f32 v[28:29], v[28:29], v[20:21]
	v_pk_mul_f32 v[20:21], v[26:27], v[42:43]
	v_pk_mul_f32 v[22:23], v[30:31], v[22:23]
	v_pk_mul_f32 v[26:27], v[34:35], v[20:21]
	v_mov_b32_e32 v20, v67
	v_pk_add_f32 v[40:41], v[40:41], 1.0 op_sel_hi:[1,0]
	v_cvt_pk_fp8_f32 v20, v22, v23
	v_rcp_f32_e32 v40, v40
	v_rcp_f32_e32 v41, v41
	v_pk_fma_f32 v[32:33], v[120:121], s[20:21], v[16:17] op_sel_hi:[1,0,1]
	v_cvt_pk_fp8_f32 v20, v28, v29 op_sel:[0,0,1]
	v_pk_fma_f32 v[28:29], v[114:115], s[20:21], v[6:7] op_sel_hi:[1,0,1]
	v_med3_f32 v32, v32, s56, v235
	v_med3_f32 v33, v33, s56, v235
	v_pk_mul_f32 v[22:23], v[24:25], v[40:41]
	v_min_f32_e32 v28, 0x40e00000, v28
	v_min_f32_e32 v29, 0x40e00000, v29
	v_pk_mul_f32 v[22:23], v[32:33], v[22:23]
	v_pk_mul_f32 v[32:33], v[28:29], s[22:23] op_sel_hi:[1,0]
	v_mov_b32_e32 v21, v67
	v_exp_f32_e32 v32, v32
	v_exp_f32_e32 v33, v33
	v_cvt_pk_fp8_f32 v21, v26, v27
	v_pk_fma_f32 v[26:27], v[116:117], s[20:21], v[8:9] op_sel_hi:[1,0,1]
	v_pk_fma_f32 v[24:25], v[110:111], s[20:21], v[18:19] op_sel_hi:[1,0,1]
	v_min_f32_e32 v26, 0x40e00000, v26
	v_min_f32_e32 v27, 0x40e00000, v27
	v_pk_mul_f32 v[30:31], v[26:27], s[22:23] op_sel_hi:[1,0]
	v_pk_add_f32 v[32:33], v[32:33], 1.0 op_sel_hi:[1,0]
	v_exp_f32_e32 v30, v30
	v_exp_f32_e32 v31, v31
	v_rcp_f32_e32 v32, v32
	v_rcp_f32_e32 v33, v33
	v_cvt_pk_fp8_f32 v21, v22, v23 op_sel:[0,0,1]
	v_pk_fma_f32 v[22:23], v[112:113], s[20:21], v[16:17] op_sel_hi:[1,0,1]
	v_pk_add_f32 v[30:31], v[30:31], 1.0 op_sel_hi:[1,0]
	v_med3_f32 v34, v22, s56, v235
	v_rcp_f32_e32 v30, v30
	v_rcp_f32_e32 v31, v31
	v_med3_f32 v35, v23, s56, v235
	v_pk_mul_f32 v[22:23], v[28:29], v[32:33]
	v_pk_fma_f32 v[32:33], v[106:107], s[20:21], v[2:3] op_sel_hi:[1,0,1]
	v_pk_mul_f32 v[26:27], v[26:27], v[30:31]
	v_min_f32_e32 v32, 0x40e00000, v32
	v_min_f32_e32 v33, 0x40e00000, v33
	v_pk_mul_f32 v[36:37], v[32:33], s[22:23] op_sel_hi:[1,0]
	v_pk_fma_f32 v[30:31], v[108:109], s[20:21], v[4:5] op_sel_hi:[1,0,1]
	v_exp_f32_e32 v36, v36
	v_exp_f32_e32 v37, v37
	v_min_f32_e32 v30, 0x40e00000, v30
	v_min_f32_e32 v31, 0x40e00000, v31
	v_pk_mul_f32 v[38:39], v[30:31], s[22:23] op_sel_hi:[1,0]
	v_pk_add_f32 v[36:37], v[36:37], 1.0 op_sel_hi:[1,0]
	v_exp_f32_e32 v38, v38
	v_exp_f32_e32 v39, v39
	v_rcp_f32_e32 v36, v36
	v_rcp_f32_e32 v37, v37
	v_pk_fma_f32 v[28:29], v[102:103], s[20:21], v[14:15] op_sel_hi:[1,0,1]
	v_pk_add_f32 v[38:39], v[38:39], 1.0 op_sel_hi:[1,0]
	v_med3_f32 v24, v24, s56, v235
	v_med3_f32 v25, v25, s56, v235
	v_med3_f32 v28, v28, s56, v235
	v_med3_f32 v29, v29, s56, v235
	v_rcp_f32_e32 v38, v38
	v_rcp_f32_e32 v39, v39
	v_pk_mul_f32 v[32:33], v[32:33], v[36:37]
	v_pk_mul_f32 v[24:25], v[24:25], v[22:23]
	v_pk_mul_f32 v[28:29], v[28:29], v[32:33]
	v_mov_b32_e32 v22, v67
	v_mov_b32_e32 v23, v67
	v_cvt_pk_fp8_f32 v22, v28, v29
	v_cvt_pk_fp8_f32 v23, v24, v25
	v_pk_fma_f32 v[24:25], v[104:105], s[20:21], v[12:13] op_sel_hi:[1,0,1]
	v_pk_mul_f32 v[28:29], v[30:31], v[38:39]
	v_med3_f32 v24, v24, s56, v235
	v_med3_f32 v25, v25, s56, v235
	v_pk_mul_f32 v[24:25], v[24:25], v[28:29]
	v_add_u32_e32 v44, 0x80, v44
	v_cvt_pk_fp8_f32 v22, v24, v25 op_sel:[0,0,1]
	v_pk_mul_f32 v[24:25], v[34:35], v[26:27]
	v_pk_fma_f32 v[26:27], v[90:91], s[20:21], v[6:7] op_sel_hi:[1,0,1]
	v_cvt_pk_fp8_f32 v23, v24, v25 op_sel:[0,0,1]
	v_or_b32_e32 v24, v44, v229
	v_ashrrev_i32_e32 v25, 31, v24
	v_lshlrev_b64 v[24:25], 11, v[24:25]
	v_lshl_add_u64 v[24:25], s[14:15], 0, v[24:25]
	v_lshl_add_u64 v[24:25], v[24:25], 0, v[10:11]
	v_permlane16_swap_b32_e32 v20, v22
	v_permlane16_swap_b32_e32 v21, v23
	v_lshl_add_u64 v[24:25], v[24:25], 0, v[204:205]
	global_store_dwordx4 v[24:25], v[20:23], off
	v_min_f32_e32 v26, 0x40e00000, v26
	v_min_f32_e32 v27, 0x40e00000, v27
	v_pk_fma_f32 v[20:21], v[100:101], s[20:21], v[4:5] op_sel_hi:[1,0,1]
	v_pk_fma_f32 v[22:23], v[98:99], s[20:21], v[2:3] op_sel_hi:[1,0,1]
	v_min_f32_e32 v20, 0x40e00000, v20
	v_min_f32_e32 v21, 0x40e00000, v21
	v_pk_mul_f32 v[36:37], v[20:21], s[22:23] op_sel_hi:[1,0]
	v_pk_mul_f32 v[42:43], v[26:27], s[22:23] op_sel_hi:[1,0]
	v_exp_f32_e32 v36, v36
	v_exp_f32_e32 v37, v37
	v_min_f32_e32 v22, 0x40e00000, v22
	v_min_f32_e32 v23, 0x40e00000, v23
	v_exp_f32_e32 v42, v42
	v_exp_f32_e32 v43, v43
	v_pk_fma_f32 v[24:25], v[92:93], s[20:21], v[8:9] op_sel_hi:[1,0,1]
	v_pk_mul_f32 v[38:39], v[22:23], s[22:23] op_sel_hi:[1,0]
	v_min_f32_e32 v24, 0x40e00000, v24
	v_min_f32_e32 v25, 0x40e00000, v25
	v_exp_f32_e32 v38, v38
	v_exp_f32_e32 v39, v39
	v_pk_mul_f32 v[40:41], v[24:25], s[22:23] op_sel_hi:[1,0]
	v_pk_add_f32 v[36:37], v[36:37], 1.0 op_sel_hi:[1,0]
	v_exp_f32_e32 v40, v40
	v_exp_f32_e32 v41, v41
	v_pk_add_f32 v[42:43], v[42:43], 1.0 op_sel_hi:[1,0]
	v_rcp_f32_e32 v36, v36
	v_rcp_f32_e32 v37, v37
	v_rcp_f32_e32 v42, v42
	v_rcp_f32_e32 v43, v43
	v_pk_add_f32 v[38:39], v[38:39], 1.0 op_sel_hi:[1,0]
	v_pk_fma_f32 v[28:29], v[96:97], s[20:21], v[12:13] op_sel_hi:[1,0,1]
	v_rcp_f32_e32 v38, v38
	v_rcp_f32_e32 v39, v39
	v_pk_fma_f32 v[34:35], v[86:87], s[20:21], v[18:19] op_sel_hi:[1,0,1]
	v_med3_f32 v28, v28, s56, v235
	v_med3_f32 v29, v29, s56, v235
	v_pk_add_f32 v[40:41], v[40:41], 1.0 op_sel_hi:[1,0]
	v_pk_mul_f32 v[20:21], v[20:21], v[36:37]
	v_med3_f32 v34, v34, s56, v235
	v_med3_f32 v35, v35, s56, v235
	v_rcp_f32_e32 v40, v40
	v_rcp_f32_e32 v41, v41
	v_pk_mul_f32 v[28:29], v[28:29], v[20:21]
	v_pk_mul_f32 v[20:21], v[26:27], v[42:43]
	v_pk_fma_f32 v[30:31], v[94:95], s[20:21], v[14:15] op_sel_hi:[1,0,1]
	v_pk_mul_f32 v[26:27], v[34:35], v[20:21]
	v_mov_b32_e32 v21, v67
	v_med3_f32 v30, v30, s56, v235
	v_med3_f32 v31, v31, s56, v235
	v_pk_mul_f32 v[22:23], v[22:23], v[38:39]
	v_cvt_pk_fp8_f32 v21, v26, v27
	v_pk_fma_f32 v[32:33], v[88:89], s[20:21], v[16:17] op_sel_hi:[1,0,1]
	v_pk_mul_f32 v[22:23], v[30:31], v[22:23]
	v_mov_b32_e32 v20, v67
	v_pk_fma_f32 v[6:7], v[78:79], s[20:21], v[6:7] op_sel_hi:[1,0,1]
	v_med3_f32 v32, v32, s56, v235
	v_med3_f32 v33, v33, s56, v235
	v_cvt_pk_fp8_f32 v20, v22, v23
	v_pk_mul_f32 v[22:23], v[24:25], v[40:41]
	v_pk_fma_f32 v[8:9], v[80:81], s[20:21], v[8:9] op_sel_hi:[1,0,1]
	v_min_f32_e32 v6, 0x40e00000, v6
	v_min_f32_e32 v7, 0x40e00000, v7
	v_pk_mul_f32 v[22:23], v[32:33], v[22:23]
	v_min_f32_e32 v8, 0x40e00000, v8
	v_min_f32_e32 v9, 0x40e00000, v9
	v_pk_mul_f32 v[24:25], v[6:7], s[22:23] op_sel_hi:[1,0]
	v_cvt_pk_fp8_f32 v21, v22, v23 op_sel:[0,0,1]
	v_pk_mul_f32 v[22:23], v[8:9], s[22:23] op_sel_hi:[1,0]
	v_exp_f32_e32 v24, v24
	v_exp_f32_e32 v25, v25
	v_exp_f32_e32 v22, v22
	v_exp_f32_e32 v23, v23
	v_pk_fma_f32 v[18:19], v[82:83], s[20:21], v[18:19] op_sel_hi:[1,0,1]
	v_pk_add_f32 v[24:25], v[24:25], 1.0 op_sel_hi:[1,0]
	v_med3_f32 v18, v18, s56, v235
	v_pk_add_f32 v[22:23], v[22:23], 1.0 op_sel_hi:[1,0]
	v_rcp_f32_e32 v24, v24
	v_rcp_f32_e32 v25, v25
	v_rcp_f32_e32 v22, v22
	v_rcp_f32_e32 v23, v23
	v_med3_f32 v19, v19, s56, v235
	v_pk_mul_f32 v[6:7], v[6:7], v[24:25]
	v_pk_fma_f32 v[2:3], v[70:71], s[20:21], v[2:3] op_sel_hi:[1,0,1]
	v_pk_mul_f32 v[8:9], v[8:9], v[22:23]
	v_pk_mul_f32 v[6:7], v[18:19], v[6:7]
	v_mov_b32_e32 v23, v67
	v_min_f32_e32 v2, 0x40e00000, v2
	v_min_f32_e32 v3, 0x40e00000, v3
	v_cvt_pk_fp8_f32 v23, v6, v7
	v_pk_fma_f32 v[6:7], v[76:77], s[20:21], v[12:13] op_sel_hi:[1,0,1]
	v_pk_fma_f32 v[12:13], v[74:75], s[20:21], v[14:15] op_sel_hi:[1,0,1]
	v_pk_mul_f32 v[14:15], v[2:3], s[22:23] op_sel_hi:[1,0]
	v_pk_fma_f32 v[4:5], v[72:73], s[20:21], v[4:5] op_sel_hi:[1,0,1]
	v_exp_f32_e32 v14, v14
	v_exp_f32_e32 v15, v15
	v_min_f32_e32 v4, 0x40e00000, v4
	v_min_f32_e32 v5, 0x40e00000, v5
	v_pk_mul_f32 v[18:19], v[4:5], s[22:23] op_sel_hi:[1,0]
	v_pk_add_f32 v[14:15], v[14:15], 1.0 op_sel_hi:[1,0]
	v_exp_f32_e32 v18, v18
	v_exp_f32_e32 v19, v19
	v_rcp_f32_e32 v14, v14
	v_rcp_f32_e32 v15, v15
	v_med3_f32 v12, v12, s56, v235
	v_pk_add_f32 v[18:19], v[18:19], 1.0 op_sel_hi:[1,0]
	v_med3_f32 v13, v13, s56, v235
	v_rcp_f32_e32 v18, v18
	v_rcp_f32_e32 v19, v19
	v_pk_mul_f32 v[2:3], v[2:3], v[14:15]
	v_mov_b32_e32 v22, v67
	v_pk_mul_f32 v[2:3], v[12:13], v[2:3]
	v_pk_fma_f32 v[16:17], v[84:85], s[20:21], v[16:17] op_sel_hi:[1,0,1]
	v_cvt_pk_fp8_f32 v22, v2, v3
	v_med3_f32 v6, v6, s56, v235
	v_med3_f32 v7, v7, s56, v235
	v_pk_mul_f32 v[2:3], v[4:5], v[18:19]
	v_med3_f32 v16, v16, s56, v235
	v_med3_f32 v17, v17, s56, v235
	v_pk_mul_f32 v[2:3], v[6:7], v[2:3]
	v_cvt_pk_fp8_f32 v20, v28, v29 op_sel:[0,0,1]
	v_cvt_pk_fp8_f32 v22, v2, v3 op_sel:[0,0,1]
	v_pk_mul_f32 v[2:3], v[16:17], v[8:9]
	s_mov_b64 s[6:7], -1
	v_cvt_pk_fp8_f32 v23, v2, v3 op_sel:[0,0,1]
	v_or_b32_e32 v2, v44, v230
	v_ashrrev_i32_e32 v3, 31, v2
	v_lshlrev_b64 v[2:3], 11, v[2:3]
	v_lshl_add_u64 v[2:3], s[14:15], 0, v[2:3]
	v_lshl_add_u64 v[2:3], v[2:3], 0, v[10:11]
	v_permlane16_swap_b32_e32 v20, v22
	v_permlane16_swap_b32_e32 v21, v23
	v_lshl_add_u64 v[2:3], v[2:3], 0, v[204:205]
	global_store_dwordx4 v[2:3], v[20:23], off
	s_cbranch_vccnz .LBB0_907
	s_andn2_b64 vcc, exec, s[0:1]
	s_cbranch_vccnz .LBB0_906
	s_barrier
	s_branch .LBB0_906

.LBB0_953:
	s_xor_b64 s[36:37], s[10:11], -1
	v_mov_b32_e32 v68, v67
	v_mov_b32_e32 v69, v67
	v_mov_b32_e32 v211, v67
	v_mov_b32_e32 v209, v67
	s_add_u32 s25, s8, 0x100
	v_mov_b32_e32 v66, v67
	v_mov_b32_e32 v142, 0
	v_mov_b64_e32 v[112:113], v[68:69]
	v_mov_b64_e32 v[104:105], v[68:69]
	v_mov_b64_e32 v[120:121], v[68:69]
	v_mov_b64_e32 v[124:125], v[68:69]
	v_mov_b64_e32 v[80:81], v[68:69]
	v_mov_b64_e32 v[72:73], v[68:69]
	v_mov_b64_e32 v[92:93], v[68:69]
	v_mov_b64_e32 v[100:101], v[68:69]
	v_mov_b64_e32 v[116:117], v[68:69]
	v_mov_b64_e32 v[108:109], v[68:69]
	v_mov_b64_e32 v[128:129], v[68:69]
	v_mov_b64_e32 v[132:133], v[68:69]
	v_mov_b64_e32 v[96:97], v[68:69]
	v_mov_b64_e32 v[88:89], v[68:69]
	v_mov_b64_e32 v[76:77], v[68:69]
	v_mov_b64_e32 v[84:85], v[68:69]
	s_addc_u32 s27, s9, 0
	v_lshl_add_u64 v[216:217], s[16:17], 0, v[210:211]
	v_lshl_add_u64 v[218:219], s[16:17], 0, v[208:209]
	s_mov_b32 s61, -2
	s_mov_b64 s[38:39], 0
	v_cndmask_b32_e64 v201, 0, 1, s[36:37]
	v_mov_b64_e32 v[110:111], v[66:67]
	v_mov_b64_e32 v[102:103], v[66:67]
	v_mov_b64_e32 v[118:119], v[66:67]
	v_mov_b64_e32 v[122:123], v[66:67]
	v_mov_b64_e32 v[78:79], v[66:67]
	v_mov_b64_e32 v[70:71], v[66:67]
	v_mov_b64_e32 v[90:91], v[66:67]
	v_mov_b64_e32 v[98:99], v[66:67]
	v_mov_b64_e32 v[114:115], v[66:67]
	v_mov_b64_e32 v[106:107], v[66:67]
	v_mov_b64_e32 v[126:127], v[66:67]
	v_mov_b64_e32 v[130:131], v[66:67]
	v_mov_b64_e32 v[94:95], v[66:67]
	v_mov_b64_e32 v[86:87], v[66:67]
	v_mov_b64_e32 v[74:75], v[66:67]
	v_mov_b64_e32 v[82:83], v[66:67]
	v_mov_b64_e32 v[134:135], 0
	v_mov_b64_e32 v[136:137], 0
	v_mov_b64_e32 v[138:139], 0
	v_mov_b64_e32 v[140:141], 0
	v_mov_b32_e32 v143, v142
	v_mov_b64_e32 v[144:145], 0
	v_mov_b64_e32 v[146:147], 0
	v_mov_b64_e32 v[148:149], 0
	v_mov_b64_e32 v[150:151], 0
	v_mov_b64_e32 v[152:153], 0
	v_mov_b64_e32 v[154:155], 0
	v_mov_b64_e32 v[156:157], 0
	v_mov_b64_e32 v[158:159], 0
	v_mov_b64_e32 v[160:161], 0
	v_mov_b64_e32 v[162:163], 0
	v_mov_b64_e32 v[164:165], 0
	v_mov_b64_e32 v[166:167], 0
	v_mov_b64_e32 v[168:169], 0
	v_mov_b64_e32 v[170:171], 0
	v_mov_b64_e32 v[172:173], 0
	v_mov_b64_e32 v[174:175], 0
	v_mov_b64_e32 v[176:177], 0
	v_mov_b64_e32 v[178:179], 0
	v_mov_b64_e32 v[180:181], 0
	v_mov_b64_e32 v[182:183], 0
	v_mov_b64_e32 v[184:185], 0
	v_mov_b64_e32 v[186:187], 0
	v_mov_b64_e32 v[188:189], 0
	v_mov_b64_e32 v[190:191], 0
	v_mov_b64_e32 v[192:193], 0
	v_mov_b64_e32 v[194:195], 0
	v_mov_b64_e32 v[196:197], 0
	s_branch .LBB0_955

.LBB0_963:
	s_add_i32 s8, s60, 0x25100
	v_mov_b32_e32 v2, s8
	s_lshl_b32 s8, s59, 11
	s_and_b32 s8, s8, 0x800
	s_nop 11
	v_add_u32_e32 v11, s8, v228
	ds_read_b32 v10, v2
	ds_read_b128 v[6:9], v11 offset:16
	ds_read_b128 v[14:17], v11 offset:512
	ds_read_b128 v[2:5], v11
	ds_read_b128 v[18:21], v11 offset:528
	s_and_b64 vcc, exec, s[6:7]
	s_waitcnt lgkmcnt(0)
	v_pk_fma_f32 v[26:27], v[190:191], s[20:21], v[6:7] op_sel_hi:[1,0,1]
	v_pk_add_f32 v[12:13], v[16:17], 1.0 op_sel_hi:[1,0]
	v_pk_fma_f32 v[22:23], v[194:195], s[20:21], v[2:3] op_sel_hi:[1,0,1]
	v_pk_add_f32 v[16:17], v[20:21], 1.0 op_sel_hi:[1,0]
	v_pk_fma_f32 v[20:21], v[196:197], s[20:21], v[4:5] op_sel_hi:[1,0,1]
	v_min_f32_e32 v22, 0x40e00000, v22
	v_min_f32_e32 v20, 0x40e00000, v20
	v_min_f32_e32 v21, 0x40e00000, v21
	v_min_f32_e32 v26, 0x40e00000, v26
	v_min_f32_e32 v23, 0x40e00000, v23
	v_min_f32_e32 v27, 0x40e00000, v27
	v_pk_mul_f32 v[36:37], v[20:21], s[22:23] op_sel_hi:[1,0]
	v_pk_mul_f32 v[38:39], v[22:23], s[22:23] op_sel_hi:[1,0]
	v_pk_mul_f32 v[42:43], v[26:27], s[22:23] op_sel_hi:[1,0]
	v_exp_f32_e32 v36, v36
	v_exp_f32_e32 v37, v37
	v_exp_f32_e32 v38, v38
	v_exp_f32_e32 v42, v42
	v_exp_f32_e32 v39, v39
	v_exp_f32_e32 v43, v43
	v_pk_add_f32 v[36:37], v[36:37], 1.0 op_sel_hi:[1,0]
	v_pk_fma_f32 v[24:25], v[192:193], s[20:21], v[8:9] op_sel_hi:[1,0,1]
	v_pk_add_f32 v[38:39], v[38:39], 1.0 op_sel_hi:[1,0]
	v_pk_add_f32 v[42:43], v[42:43], 1.0 op_sel_hi:[1,0]
	v_rcp_f32_e32 v36, v36
	v_rcp_f32_e32 v37, v37
	v_min_f32_e32 v24, 0x40e00000, v24
	v_min_f32_e32 v25, 0x40e00000, v25
	v_rcp_f32_e32 v38, v38
	v_rcp_f32_e32 v42, v42
	v_rcp_f32_e32 v39, v39
	v_rcp_f32_e32 v43, v43
	v_pk_mul_f32 v[40:41], v[24:25], s[22:23] op_sel_hi:[1,0]
	v_pk_add_f32 v[14:15], v[14:15], 1.0 op_sel_hi:[1,0]
	v_pk_add_f32 v[18:19], v[18:19], 1.0 op_sel_hi:[1,0]
	v_pk_fma_f32 v[28:29], v[188:189], s[20:21], v[12:13] op_sel_hi:[1,0,1]
	v_exp_f32_e32 v40, v40
	v_exp_f32_e32 v41, v41
	v_pk_fma_f32 v[30:31], v[186:187], s[20:21], v[14:15] op_sel_hi:[1,0,1]
	v_pk_fma_f32 v[34:35], v[182:183], s[20:21], v[18:19] op_sel_hi:[1,0,1]
	v_med3_f32 v28, v28, s54, v235
	v_med3_f32 v29, v29, s54, v235
	v_pk_mul_f32 v[20:21], v[20:21], v[36:37]
	v_med3_f32 v30, v30, s54, v235
	v_med3_f32 v34, v34, s54, v235
	v_med3_f32 v31, v31, s54, v235
	v_med3_f32 v35, v35, s54, v235
	v_pk_mul_f32 v[22:23], v[22:23], v[38:39]
	v_pk_mul_f32 v[28:29], v[28:29], v[20:21]
	v_pk_mul_f32 v[20:21], v[26:27], v[42:43]
	v_pk_mul_f32 v[22:23], v[30:31], v[22:23]
	v_pk_mul_f32 v[26:27], v[34:35], v[20:21]
	v_mov_b32_e32 v20, v67
	v_pk_add_f32 v[40:41], v[40:41], 1.0 op_sel_hi:[1,0]
	v_cvt_pk_fp8_f32 v20, v22, v23
	v_rcp_f32_e32 v40, v40
	v_rcp_f32_e32 v41, v41
	v_pk_fma_f32 v[32:33], v[184:185], s[20:21], v[16:17] op_sel_hi:[1,0,1]
	v_cvt_pk_fp8_f32 v20, v28, v29 op_sel:[0,0,1]
	v_pk_fma_f32 v[28:29], v[178:179], s[20:21], v[6:7] op_sel_hi:[1,0,1]
	v_med3_f32 v32, v32, s54, v235
	v_med3_f32 v33, v33, s54, v235
	v_pk_mul_f32 v[22:23], v[24:25], v[40:41]
	v_min_f32_e32 v28, 0x40e00000, v28
	v_min_f32_e32 v29, 0x40e00000, v29
	v_pk_mul_f32 v[22:23], v[32:33], v[22:23]
	v_pk_mul_f32 v[32:33], v[28:29], s[22:23] op_sel_hi:[1,0]
	v_mov_b32_e32 v21, v67
	v_exp_f32_e32 v32, v32
	v_exp_f32_e32 v33, v33
	v_cvt_pk_fp8_f32 v21, v26, v27
	v_pk_fma_f32 v[26:27], v[180:181], s[20:21], v[8:9] op_sel_hi:[1,0,1]
	v_pk_fma_f32 v[24:25], v[174:175], s[20:21], v[18:19] op_sel_hi:[1,0,1]
	v_min_f32_e32 v26, 0x40e00000, v26
	v_min_f32_e32 v27, 0x40e00000, v27
	v_pk_mul_f32 v[30:31], v[26:27], s[22:23] op_sel_hi:[1,0]
	v_pk_add_f32 v[32:33], v[32:33], 1.0 op_sel_hi:[1,0]
	v_exp_f32_e32 v30, v30
	v_exp_f32_e32 v31, v31
	v_rcp_f32_e32 v32, v32
	v_rcp_f32_e32 v33, v33
	v_cvt_pk_fp8_f32 v21, v22, v23 op_sel:[0,0,1]
	v_pk_fma_f32 v[22:23], v[176:177], s[20:21], v[16:17] op_sel_hi:[1,0,1]
	v_pk_add_f32 v[30:31], v[30:31], 1.0 op_sel_hi:[1,0]
	v_med3_f32 v34, v22, s54, v235
	v_rcp_f32_e32 v30, v30
	v_rcp_f32_e32 v31, v31
	v_med3_f32 v35, v23, s54, v235
	v_pk_mul_f32 v[22:23], v[28:29], v[32:33]
	v_pk_fma_f32 v[32:33], v[170:171], s[20:21], v[2:3] op_sel_hi:[1,0,1]
	v_pk_mul_f32 v[26:27], v[26:27], v[30:31]
	v_min_f32_e32 v32, 0x40e00000, v32
	v_min_f32_e32 v33, 0x40e00000, v33
	v_pk_mul_f32 v[36:37], v[32:33], s[22:23] op_sel_hi:[1,0]
	v_pk_fma_f32 v[30:31], v[172:173], s[20:21], v[4:5] op_sel_hi:[1,0,1]
	v_exp_f32_e32 v36, v36
	v_exp_f32_e32 v37, v37
	v_min_f32_e32 v30, 0x40e00000, v30
	v_min_f32_e32 v31, 0x40e00000, v31
	v_pk_mul_f32 v[38:39], v[30:31], s[22:23] op_sel_hi:[1,0]
	v_pk_add_f32 v[36:37], v[36:37], 1.0 op_sel_hi:[1,0]
	v_exp_f32_e32 v38, v38
	v_exp_f32_e32 v39, v39
	v_rcp_f32_e32 v36, v36
	v_rcp_f32_e32 v37, v37
	v_pk_fma_f32 v[28:29], v[166:167], s[20:21], v[14:15] op_sel_hi:[1,0,1]
	v_pk_add_f32 v[38:39], v[38:39], 1.0 op_sel_hi:[1,0]
	v_med3_f32 v24, v24, s54, v235
	v_med3_f32 v25, v25, s54, v235
	v_med3_f32 v28, v28, s54, v235
	v_med3_f32 v29, v29, s54, v235
	v_rcp_f32_e32 v38, v38
	v_rcp_f32_e32 v39, v39
	v_pk_mul_f32 v[32:33], v[32:33], v[36:37]
	v_pk_mul_f32 v[24:25], v[24:25], v[22:23]
	v_pk_mul_f32 v[28:29], v[28:29], v[32:33]
	v_mov_b32_e32 v22, v67
	v_mov_b32_e32 v23, v67
	v_cvt_pk_fp8_f32 v22, v28, v29
	v_cvt_pk_fp8_f32 v23, v24, v25
	v_pk_fma_f32 v[24:25], v[168:169], s[20:21], v[12:13] op_sel_hi:[1,0,1]
	v_pk_mul_f32 v[28:29], v[30:31], v[38:39]
	v_med3_f32 v24, v24, s54, v235
	v_med3_f32 v25, v25, s54, v235
	v_add_u32_e32 v11, s58, v10
	v_pk_mul_f32 v[24:25], v[24:25], v[28:29]
	v_lshl_add_u32 v44, v11, 8, v213
	v_cvt_pk_fp8_f32 v22, v24, v25 op_sel:[0,0,1]
	v_pk_mul_f32 v[24:25], v[34:35], v[26:27]
	v_lshl_or_b32 v10, s30, 7, v231
	v_cvt_pk_fp8_f32 v23, v24, v25 op_sel:[0,0,1]
	v_or_b32_e32 v24, v44, v229
	v_ashrrev_i32_e32 v25, 31, v24
	v_lshlrev_b64 v[24:25], 11, v[24:25]
	v_ashrrev_i32_e32 v11, 31, v10
	v_lshl_add_u64 v[24:25], s[14:15], 0, v[24:25]
	v_lshl_add_u64 v[24:25], v[24:25], 0, v[10:11]
	v_permlane16_swap_b32_e32 v20, v22
	v_permlane16_swap_b32_e32 v21, v23
	v_lshl_add_u64 v[24:25], v[24:25], 0, v[204:205]
	global_store_dwordx4 v[24:25], v[20:23], off
	v_pk_fma_f32 v[26:27], v[158:159], s[20:21], v[6:7] op_sel_hi:[1,0,1]
	v_pk_fma_f32 v[24:25], v[160:161], s[20:21], v[8:9] op_sel_hi:[1,0,1]
	v_pk_fma_f32 v[20:21], v[164:165], s[20:21], v[4:5] op_sel_hi:[1,0,1]
	v_pk_fma_f32 v[22:23], v[162:163], s[20:21], v[2:3] op_sel_hi:[1,0,1]
	v_min_f32_e32 v20, 0x40e00000, v20
	v_min_f32_e32 v21, 0x40e00000, v21
	v_min_f32_e32 v22, 0x40e00000, v22
	v_min_f32_e32 v26, 0x40e00000, v26
	v_min_f32_e32 v23, 0x40e00000, v23
	v_min_f32_e32 v27, 0x40e00000, v27
	v_pk_mul_f32 v[36:37], v[20:21], s[22:23] op_sel_hi:[1,0]
	v_pk_mul_f32 v[38:39], v[22:23], s[22:23] op_sel_hi:[1,0]
	v_pk_mul_f32 v[42:43], v[26:27], s[22:23] op_sel_hi:[1,0]
	v_exp_f32_e32 v36, v36
	v_exp_f32_e32 v37, v37
	v_exp_f32_e32 v38, v38
	v_exp_f32_e32 v42, v42
	v_exp_f32_e32 v39, v39
	v_exp_f32_e32 v43, v43
	v_pk_add_f32 v[36:37], v[36:37], 1.0 op_sel_hi:[1,0]
	v_min_f32_e32 v24, 0x40e00000, v24
	v_pk_add_f32 v[38:39], v[38:39], 1.0 op_sel_hi:[1,0]
	v_pk_add_f32 v[42:43], v[42:43], 1.0 op_sel_hi:[1,0]
	v_rcp_f32_e32 v36, v36
	v_rcp_f32_e32 v37, v37
	v_min_f32_e32 v25, 0x40e00000, v25
	v_rcp_f32_e32 v38, v38
	v_rcp_f32_e32 v42, v42
	v_rcp_f32_e32 v39, v39
	v_rcp_f32_e32 v43, v43
	v_pk_mul_f32 v[40:41], v[24:25], s[22:23] op_sel_hi:[1,0]
	v_pk_fma_f32 v[28:29], v[156:157], s[20:21], v[12:13] op_sel_hi:[1,0,1]
	v_exp_f32_e32 v40, v40
	v_exp_f32_e32 v41, v41
	v_pk_fma_f32 v[30:31], v[154:155], s[20:21], v[14:15] op_sel_hi:[1,0,1]
	v_pk_fma_f32 v[34:35], v[150:151], s[20:21], v[18:19] op_sel_hi:[1,0,1]
	v_med3_f32 v28, v28, s54, v235
	v_med3_f32 v29, v29, s54, v235
	v_pk_mul_f32 v[20:21], v[20:21], v[36:37]
	v_med3_f32 v30, v30, s54, v235
	v_med3_f32 v34, v34, s54, v235
	v_med3_f32 v31, v31, s54, v235
	v_med3_f32 v35, v35, s54, v235
	v_pk_mul_f32 v[22:23], v[22:23], v[38:39]
	v_pk_mul_f32 v[28:29], v[28:29], v[20:21]
	v_pk_mul_f32 v[20:21], v[26:27], v[42:43]
	v_pk_mul_f32 v[22:23], v[30:31], v[22:23]
	v_pk_mul_f32 v[26:27], v[34:35], v[20:21]
	v_mov_b32_e32 v20, v67
	v_pk_add_f32 v[40:41], v[40:41], 1.0 op_sel_hi:[1,0]
	v_cvt_pk_fp8_f32 v20, v22, v23
	v_rcp_f32_e32 v40, v40
	v_rcp_f32_e32 v41, v41
	v_pk_fma_f32 v[32:33], v[152:153], s[20:21], v[16:17] op_sel_hi:[1,0,1]
	v_cvt_pk_fp8_f32 v20, v28, v29 op_sel:[0,0,1]
	v_pk_fma_f32 v[28:29], v[146:147], s[20:21], v[6:7] op_sel_hi:[1,0,1]
	v_med3_f32 v32, v32, s54, v235
	v_med3_f32 v33, v33, s54, v235
	v_pk_mul_f32 v[22:23], v[24:25], v[40:41]
	v_min_f32_e32 v28, 0x40e00000, v28
	v_min_f32_e32 v29, 0x40e00000, v29
	v_pk_mul_f32 v[22:23], v[32:33], v[22:23]
	v_pk_mul_f32 v[32:33], v[28:29], s[22:23] op_sel_hi:[1,0]
	v_mov_b32_e32 v21, v67
	v_exp_f32_e32 v32, v32
	v_exp_f32_e32 v33, v33
	v_cvt_pk_fp8_f32 v21, v26, v27
	v_pk_fma_f32 v[26:27], v[148:149], s[20:21], v[8:9] op_sel_hi:[1,0,1]
	v_pk_fma_f32 v[24:25], v[142:143], s[20:21], v[18:19] op_sel_hi:[1,0,1]
	v_min_f32_e32 v26, 0x40e00000, v26
	v_min_f32_e32 v27, 0x40e00000, v27
	v_pk_mul_f32 v[30:31], v[26:27], s[22:23] op_sel_hi:[1,0]
	v_pk_add_f32 v[32:33], v[32:33], 1.0 op_sel_hi:[1,0]
	v_exp_f32_e32 v30, v30
	v_exp_f32_e32 v31, v31
	v_rcp_f32_e32 v32, v32
	v_rcp_f32_e32 v33, v33
	v_cvt_pk_fp8_f32 v21, v22, v23 op_sel:[0,0,1]
	v_pk_fma_f32 v[22:23], v[144:145], s[20:21], v[16:17] op_sel_hi:[1,0,1]
	v_pk_add_f32 v[30:31], v[30:31], 1.0 op_sel_hi:[1,0]
	v_med3_f32 v34, v22, s54, v235
	v_rcp_f32_e32 v30, v30
	v_rcp_f32_e32 v31, v31
	v_med3_f32 v35, v23, s54, v235
	v_pk_mul_f32 v[22:23], v[28:29], v[32:33]
	v_pk_fma_f32 v[32:33], v[138:139], s[20:21], v[2:3] op_sel_hi:[1,0,1]
	v_pk_mul_f32 v[26:27], v[26:27], v[30:31]
	v_min_f32_e32 v32, 0x40e00000, v32
	v_min_f32_e32 v33, 0x40e00000, v33
	v_pk_mul_f32 v[36:37], v[32:33], s[22:23] op_sel_hi:[1,0]
	v_pk_fma_f32 v[30:31], v[140:141], s[20:21], v[4:5] op_sel_hi:[1,0,1]
	v_exp_f32_e32 v36, v36
	v_exp_f32_e32 v37, v37
	v_min_f32_e32 v30, 0x40e00000, v30
	v_min_f32_e32 v31, 0x40e00000, v31
	v_pk_mul_f32 v[38:39], v[30:31], s[22:23] op_sel_hi:[1,0]
	v_pk_add_f32 v[36:37], v[36:37], 1.0 op_sel_hi:[1,0]
	v_exp_f32_e32 v38, v38
	v_exp_f32_e32 v39, v39
	v_rcp_f32_e32 v36, v36
	v_rcp_f32_e32 v37, v37
	v_pk_fma_f32 v[28:29], v[134:135], s[20:21], v[14:15] op_sel_hi:[1,0,1]
	v_pk_add_f32 v[38:39], v[38:39], 1.0 op_sel_hi:[1,0]
	v_med3_f32 v24, v24, s54, v235
	v_med3_f32 v25, v25, s54, v235
	v_med3_f32 v28, v28, s54, v235
	v_med3_f32 v29, v29, s54, v235
	v_rcp_f32_e32 v38, v38
	v_rcp_f32_e32 v39, v39
	v_pk_mul_f32 v[32:33], v[32:33], v[36:37]
	v_pk_mul_f32 v[24:25], v[24:25], v[22:23]
	v_pk_mul_f32 v[28:29], v[28:29], v[32:33]
	v_mov_b32_e32 v22, v67
	v_mov_b32_e32 v23, v67
	v_cvt_pk_fp8_f32 v22, v28, v29
	v_cvt_pk_fp8_f32 v23, v24, v25
	v_pk_fma_f32 v[24:25], v[136:137], s[20:21], v[12:13] op_sel_hi:[1,0,1]
	v_pk_mul_f32 v[28:29], v[30:31], v[38:39]
	v_med3_f32 v24, v24, s54, v235
	v_med3_f32 v25, v25, s54, v235
	v_pk_mul_f32 v[24:25], v[24:25], v[28:29]
	v_pk_fma_f32 v[28:29], v[124:125], s[20:21], v[12:13] op_sel_hi:[1,0,1]
	v_cvt_pk_fp8_f32 v22, v24, v25 op_sel:[0,0,1]
	v_pk_mul_f32 v[24:25], v[34:35], v[26:27]
	v_pk_fma_f32 v[26:27], v[126:127], s[20:21], v[6:7] op_sel_hi:[1,0,1]
	v_cvt_pk_fp8_f32 v23, v24, v25 op_sel:[0,0,1]
	v_or_b32_e32 v24, v44, v230
	v_ashrrev_i32_e32 v25, 31, v24
	v_lshlrev_b64 v[24:25], 11, v[24:25]
	v_lshl_add_u64 v[24:25], s[14:15], 0, v[24:25]
	v_lshl_add_u64 v[24:25], v[24:25], 0, v[10:11]
	v_permlane16_swap_b32_e32 v20, v22
	v_permlane16_swap_b32_e32 v21, v23
	v_lshl_add_u64 v[24:25], v[24:25], 0, v[204:205]
	global_store_dwordx4 v[24:25], v[20:23], off
	v_min_f32_e32 v26, 0x40e00000, v26
	v_min_f32_e32 v27, 0x40e00000, v27
	v_pk_fma_f32 v[20:21], v[132:133], s[20:21], v[4:5] op_sel_hi:[1,0,1]
	v_pk_fma_f32 v[22:23], v[130:131], s[20:21], v[2:3] op_sel_hi:[1,0,1]
	v_min_f32_e32 v20, 0x40e00000, v20
	v_min_f32_e32 v21, 0x40e00000, v21
	v_min_f32_e32 v22, 0x40e00000, v22
	v_min_f32_e32 v23, 0x40e00000, v23
	v_pk_mul_f32 v[36:37], v[20:21], s[22:23] op_sel_hi:[1,0]
	v_pk_mul_f32 v[38:39], v[22:23], s[22:23] op_sel_hi:[1,0]
	v_pk_mul_f32 v[42:43], v[26:27], s[22:23] op_sel_hi:[1,0]
	v_exp_f32_e32 v36, v36
	v_exp_f32_e32 v37, v37
	v_exp_f32_e32 v38, v38
	v_exp_f32_e32 v42, v42
	v_exp_f32_e32 v39, v39
	v_exp_f32_e32 v43, v43
	v_pk_add_f32 v[36:37], v[36:37], 1.0 op_sel_hi:[1,0]
	v_pk_fma_f32 v[24:25], v[128:129], s[20:21], v[8:9] op_sel_hi:[1,0,1]
	v_pk_add_f32 v[38:39], v[38:39], 1.0 op_sel_hi:[1,0]
	v_pk_add_f32 v[42:43], v[42:43], 1.0 op_sel_hi:[1,0]
	v_rcp_f32_e32 v36, v36
	v_rcp_f32_e32 v37, v37
	v_min_f32_e32 v24, 0x40e00000, v24
	v_min_f32_e32 v25, 0x40e00000, v25
	v_rcp_f32_e32 v38, v38
	v_rcp_f32_e32 v42, v42
	v_rcp_f32_e32 v39, v39
	v_rcp_f32_e32 v43, v43
	v_pk_mul_f32 v[40:41], v[24:25], s[22:23] op_sel_hi:[1,0]
	v_pk_fma_f32 v[30:31], v[122:123], s[20:21], v[14:15] op_sel_hi:[1,0,1]
	v_exp_f32_e32 v40, v40
	v_exp_f32_e32 v41, v41
	v_pk_fma_f32 v[34:35], v[118:119], s[20:21], v[18:19] op_sel_hi:[1,0,1]
	v_med3_f32 v28, v28, s54, v235
	v_med3_f32 v29, v29, s54, v235
	v_pk_mul_f32 v[20:21], v[20:21], v[36:37]
	v_med3_f32 v30, v30, s54, v235
	v_med3_f32 v34, v34, s54, v235
	v_med3_f32 v31, v31, s54, v235
	v_med3_f32 v35, v35, s54, v235
	v_pk_mul_f32 v[22:23], v[22:23], v[38:39]
	v_pk_mul_f32 v[28:29], v[28:29], v[20:21]
	v_pk_mul_f32 v[20:21], v[26:27], v[42:43]
	v_pk_mul_f32 v[22:23], v[30:31], v[22:23]
	v_pk_mul_f32 v[26:27], v[34:35], v[20:21]
	v_mov_b32_e32 v20, v67
	v_pk_add_f32 v[40:41], v[40:41], 1.0 op_sel_hi:[1,0]
	v_cvt_pk_fp8_f32 v20, v22, v23
	v_rcp_f32_e32 v40, v40
	v_rcp_f32_e32 v41, v41
	v_pk_fma_f32 v[32:33], v[120:121], s[20:21], v[16:17] op_sel_hi:[1,0,1]
	v_cvt_pk_fp8_f32 v20, v28, v29 op_sel:[0,0,1]
	v_pk_fma_f32 v[28:29], v[114:115], s[20:21], v[6:7] op_sel_hi:[1,0,1]
	v_med3_f32 v32, v32, s54, v235
	v_med3_f32 v33, v33, s54, v235
	v_pk_mul_f32 v[22:23], v[24:25], v[40:41]
	v_min_f32_e32 v28, 0x40e00000, v28
	v_min_f32_e32 v29, 0x40e00000, v29
	v_pk_mul_f32 v[22:23], v[32:33], v[22:23]
	v_pk_mul_f32 v[32:33], v[28:29], s[22:23] op_sel_hi:[1,0]
	v_mov_b32_e32 v21, v67
	v_exp_f32_e32 v32, v32
	v_exp_f32_e32 v33, v33
	v_cvt_pk_fp8_f32 v21, v26, v27
	v_pk_fma_f32 v[26:27], v[116:117], s[20:21], v[8:9] op_sel_hi:[1,0,1]
	v_pk_fma_f32 v[24:25], v[110:111], s[20:21], v[18:19] op_sel_hi:[1,0,1]
	v_min_f32_e32 v26, 0x40e00000, v26
	v_min_f32_e32 v27, 0x40e00000, v27
	v_pk_mul_f32 v[30:31], v[26:27], s[22:23] op_sel_hi:[1,0]
	v_pk_add_f32 v[32:33], v[32:33], 1.0 op_sel_hi:[1,0]
	v_exp_f32_e32 v30, v30
	v_exp_f32_e32 v31, v31
	v_rcp_f32_e32 v32, v32
	v_rcp_f32_e32 v33, v33
	v_cvt_pk_fp8_f32 v21, v22, v23 op_sel:[0,0,1]
	v_pk_fma_f32 v[22:23], v[112:113], s[20:21], v[16:17] op_sel_hi:[1,0,1]
	v_pk_add_f32 v[30:31], v[30:31], 1.0 op_sel_hi:[1,0]
	v_med3_f32 v34, v22, s54, v235
	v_rcp_f32_e32 v30, v30
	v_rcp_f32_e32 v31, v31
	v_med3_f32 v35, v23, s54, v235
	v_pk_mul_f32 v[22:23], v[28:29], v[32:33]
	v_pk_fma_f32 v[32:33], v[106:107], s[20:21], v[2:3] op_sel_hi:[1,0,1]
	v_pk_mul_f32 v[26:27], v[26:27], v[30:31]
	v_min_f32_e32 v32, 0x40e00000, v32
	v_min_f32_e32 v33, 0x40e00000, v33
	v_pk_mul_f32 v[36:37], v[32:33], s[22:23] op_sel_hi:[1,0]
	v_pk_fma_f32 v[30:31], v[108:109], s[20:21], v[4:5] op_sel_hi:[1,0,1]
	v_exp_f32_e32 v36, v36
	v_exp_f32_e32 v37, v37
	v_min_f32_e32 v30, 0x40e00000, v30
	v_min_f32_e32 v31, 0x40e00000, v31
	v_pk_mul_f32 v[38:39], v[30:31], s[22:23] op_sel_hi:[1,0]
	v_pk_add_f32 v[36:37], v[36:37], 1.0 op_sel_hi:[1,0]
	v_exp_f32_e32 v38, v38
	v_exp_f32_e32 v39, v39
	v_rcp_f32_e32 v36, v36
	v_rcp_f32_e32 v37, v37
	v_pk_fma_f32 v[28:29], v[102:103], s[20:21], v[14:15] op_sel_hi:[1,0,1]
	v_pk_add_f32 v[38:39], v[38:39], 1.0 op_sel_hi:[1,0]
	v_med3_f32 v24, v24, s54, v235
	v_med3_f32 v25, v25, s54, v235
	v_med3_f32 v28, v28, s54, v235
	v_med3_f32 v29, v29, s54, v235
	v_rcp_f32_e32 v38, v38
	v_rcp_f32_e32 v39, v39
	v_pk_mul_f32 v[32:33], v[32:33], v[36:37]
	v_pk_mul_f32 v[24:25], v[24:25], v[22:23]
	v_pk_mul_f32 v[28:29], v[28:29], v[32:33]
	v_mov_b32_e32 v22, v67
	v_mov_b32_e32 v23, v67
	v_cvt_pk_fp8_f32 v22, v28, v29
	v_cvt_pk_fp8_f32 v23, v24, v25
	v_pk_fma_f32 v[24:25], v[104:105], s[20:21], v[12:13] op_sel_hi:[1,0,1]
	v_pk_mul_f32 v[28:29], v[30:31], v[38:39]
	v_med3_f32 v24, v24, s54, v235
	v_med3_f32 v25, v25, s54, v235
	v_pk_mul_f32 v[24:25], v[24:25], v[28:29]
	v_add_u32_e32 v44, 0x80, v44
	v_cvt_pk_fp8_f32 v22, v24, v25 op_sel:[0,0,1]
	v_pk_mul_f32 v[24:25], v[34:35], v[26:27]
	v_pk_fma_f32 v[26:27], v[90:91], s[20:21], v[6:7] op_sel_hi:[1,0,1]
	v_cvt_pk_fp8_f32 v23, v24, v25 op_sel:[0,0,1]
	v_or_b32_e32 v24, v44, v229
	v_ashrrev_i32_e32 v25, 31, v24
	v_lshlrev_b64 v[24:25], 11, v[24:25]
	v_lshl_add_u64 v[24:25], s[14:15], 0, v[24:25]
	v_lshl_add_u64 v[24:25], v[24:25], 0, v[10:11]
	v_permlane16_swap_b32_e32 v20, v22
	v_permlane16_swap_b32_e32 v21, v23
	v_lshl_add_u64 v[24:25], v[24:25], 0, v[204:205]
	global_store_dwordx4 v[24:25], v[20:23], off
	v_min_f32_e32 v26, 0x40e00000, v26
	v_min_f32_e32 v27, 0x40e00000, v27
	v_pk_fma_f32 v[20:21], v[100:101], s[20:21], v[4:5] op_sel_hi:[1,0,1]
	v_pk_fma_f32 v[22:23], v[98:99], s[20:21], v[2:3] op_sel_hi:[1,0,1]
	v_min_f32_e32 v20, 0x40e00000, v20
	v_min_f32_e32 v21, 0x40e00000, v21
	v_pk_mul_f32 v[36:37], v[20:21], s[22:23] op_sel_hi:[1,0]
	v_pk_mul_f32 v[42:43], v[26:27], s[22:23] op_sel_hi:[1,0]
	v_exp_f32_e32 v36, v36
	v_exp_f32_e32 v37, v37
	v_min_f32_e32 v22, 0x40e00000, v22
	v_min_f32_e32 v23, 0x40e00000, v23
	v_exp_f32_e32 v42, v42
	v_exp_f32_e32 v43, v43
	v_pk_fma_f32 v[24:25], v[92:93], s[20:21], v[8:9] op_sel_hi:[1,0,1]
	v_pk_mul_f32 v[38:39], v[22:23], s[22:23] op_sel_hi:[1,0]
	v_min_f32_e32 v24, 0x40e00000, v24
	v_min_f32_e32 v25, 0x40e00000, v25
	v_exp_f32_e32 v38, v38
	v_exp_f32_e32 v39, v39
	v_pk_mul_f32 v[40:41], v[24:25], s[22:23] op_sel_hi:[1,0]
	v_pk_add_f32 v[36:37], v[36:37], 1.0 op_sel_hi:[1,0]
	v_exp_f32_e32 v40, v40
	v_exp_f32_e32 v41, v41
	v_pk_add_f32 v[42:43], v[42:43], 1.0 op_sel_hi:[1,0]
	v_rcp_f32_e32 v36, v36
	v_rcp_f32_e32 v37, v37
	v_rcp_f32_e32 v42, v42
	v_rcp_f32_e32 v43, v43
	v_pk_add_f32 v[38:39], v[38:39], 1.0 op_sel_hi:[1,0]
	v_pk_fma_f32 v[28:29], v[96:97], s[20:21], v[12:13] op_sel_hi:[1,0,1]
	v_rcp_f32_e32 v38, v38
	v_rcp_f32_e32 v39, v39
	v_pk_fma_f32 v[34:35], v[86:87], s[20:21], v[18:19] op_sel_hi:[1,0,1]
	v_med3_f32 v28, v28, s54, v235
	v_med3_f32 v29, v29, s54, v235
	v_pk_add_f32 v[40:41], v[40:41], 1.0 op_sel_hi:[1,0]
	v_pk_mul_f32 v[20:21], v[20:21], v[36:37]
	v_med3_f32 v34, v34, s54, v235
	v_med3_f32 v35, v35, s54, v235
	v_rcp_f32_e32 v40, v40
	v_rcp_f32_e32 v41, v41
	v_pk_mul_f32 v[28:29], v[28:29], v[20:21]
	v_pk_mul_f32 v[20:21], v[26:27], v[42:43]
	v_pk_fma_f32 v[30:31], v[94:95], s[20:21], v[14:15] op_sel_hi:[1,0,1]
	v_pk_mul_f32 v[26:27], v[34:35], v[20:21]
	v_mov_b32_e32 v21, v67
	v_med3_f32 v30, v30, s54, v235
	v_med3_f32 v31, v31, s54, v235
	v_pk_mul_f32 v[22:23], v[22:23], v[38:39]
	v_cvt_pk_fp8_f32 v21, v26, v27
	v_pk_fma_f32 v[32:33], v[88:89], s[20:21], v[16:17] op_sel_hi:[1,0,1]
	v_pk_mul_f32 v[22:23], v[30:31], v[22:23]
	v_mov_b32_e32 v20, v67
	v_pk_fma_f32 v[6:7], v[78:79], s[20:21], v[6:7] op_sel_hi:[1,0,1]
	v_med3_f32 v32, v32, s54, v235
	v_med3_f32 v33, v33, s54, v235
	v_cvt_pk_fp8_f32 v20, v22, v23
	v_pk_mul_f32 v[22:23], v[24:25], v[40:41]
	v_pk_fma_f32 v[8:9], v[80:81], s[20:21], v[8:9] op_sel_hi:[1,0,1]
	v_min_f32_e32 v6, 0x40e00000, v6
	v_min_f32_e32 v7, 0x40e00000, v7
	v_pk_mul_f32 v[22:23], v[32:33], v[22:23]
	v_min_f32_e32 v8, 0x40e00000, v8
	v_min_f32_e32 v9, 0x40e00000, v9
	v_pk_mul_f32 v[24:25], v[6:7], s[22:23] op_sel_hi:[1,0]
	v_cvt_pk_fp8_f32 v21, v22, v23 op_sel:[0,0,1]
	v_pk_mul_f32 v[22:23], v[8:9], s[22:23] op_sel_hi:[1,0]
	v_exp_f32_e32 v24, v24
	v_exp_f32_e32 v25, v25
	v_exp_f32_e32 v22, v22
	v_exp_f32_e32 v23, v23
	v_pk_fma_f32 v[18:19], v[82:83], s[20:21], v[18:19] op_sel_hi:[1,0,1]
	v_pk_add_f32 v[24:25], v[24:25], 1.0 op_sel_hi:[1,0]
	v_med3_f32 v18, v18, s54, v235
	v_pk_add_f32 v[22:23], v[22:23], 1.0 op_sel_hi:[1,0]
	v_rcp_f32_e32 v24, v24
	v_rcp_f32_e32 v25, v25
	v_rcp_f32_e32 v22, v22
	v_rcp_f32_e32 v23, v23
	v_med3_f32 v19, v19, s54, v235
	v_pk_mul_f32 v[6:7], v[6:7], v[24:25]
	v_pk_fma_f32 v[2:3], v[70:71], s[20:21], v[2:3] op_sel_hi:[1,0,1]
	v_pk_mul_f32 v[8:9], v[8:9], v[22:23]
	v_pk_mul_f32 v[6:7], v[18:19], v[6:7]
	v_mov_b32_e32 v23, v67
	v_min_f32_e32 v2, 0x40e00000, v2
	v_min_f32_e32 v3, 0x40e00000, v3
	v_cvt_pk_fp8_f32 v23, v6, v7
	v_pk_fma_f32 v[6:7], v[76:77], s[20:21], v[12:13] op_sel_hi:[1,0,1]
	v_pk_fma_f32 v[12:13], v[74:75], s[20:21], v[14:15] op_sel_hi:[1,0,1]
	v_pk_mul_f32 v[14:15], v[2:3], s[22:23] op_sel_hi:[1,0]
	v_pk_fma_f32 v[4:5], v[72:73], s[20:21], v[4:5] op_sel_hi:[1,0,1]
	v_exp_f32_e32 v14, v14
	v_exp_f32_e32 v15, v15
	v_min_f32_e32 v4, 0x40e00000, v4
	v_min_f32_e32 v5, 0x40e00000, v5
	v_pk_mul_f32 v[18:19], v[4:5], s[22:23] op_sel_hi:[1,0]
	v_pk_add_f32 v[14:15], v[14:15], 1.0 op_sel_hi:[1,0]
	v_exp_f32_e32 v18, v18
	v_exp_f32_e32 v19, v19
	v_rcp_f32_e32 v14, v14
	v_rcp_f32_e32 v15, v15
	v_med3_f32 v12, v12, s54, v235
	v_pk_add_f32 v[18:19], v[18:19], 1.0 op_sel_hi:[1,0]
	v_med3_f32 v13, v13, s54, v235
	v_rcp_f32_e32 v18, v18
	v_rcp_f32_e32 v19, v19
	v_pk_mul_f32 v[2:3], v[2:3], v[14:15]
	v_mov_b32_e32 v22, v67
	v_pk_mul_f32 v[2:3], v[12:13], v[2:3]
	v_pk_fma_f32 v[16:17], v[84:85], s[20:21], v[16:17] op_sel_hi:[1,0,1]
	v_cvt_pk_fp8_f32 v22, v2, v3
	v_med3_f32 v6, v6, s54, v235
	v_med3_f32 v7, v7, s54, v235
	v_pk_mul_f32 v[2:3], v[4:5], v[18:19]
	v_med3_f32 v16, v16, s54, v235
	v_med3_f32 v17, v17, s54, v235
	v_pk_mul_f32 v[2:3], v[6:7], v[2:3]
	v_cvt_pk_fp8_f32 v20, v28, v29 op_sel:[0,0,1]
	v_cvt_pk_fp8_f32 v22, v2, v3 op_sel:[0,0,1]
	v_pk_mul_f32 v[2:3], v[16:17], v[8:9]
	s_mov_b64 s[6:7], -1
	v_cvt_pk_fp8_f32 v23, v2, v3 op_sel:[0,0,1]
	v_or_b32_e32 v2, v44, v230
	v_ashrrev_i32_e32 v3, 31, v2
	v_lshlrev_b64 v[2:3], 11, v[2:3]
	v_lshl_add_u64 v[2:3], s[14:15], 0, v[2:3]
	v_lshl_add_u64 v[2:3], v[2:3], 0, v[10:11]
	v_permlane16_swap_b32_e32 v20, v22
	v_permlane16_swap_b32_e32 v21, v23
	v_lshl_add_u64 v[2:3], v[2:3], 0, v[204:205]
	global_store_dwordx4 v[2:3], v[20:23], off
	s_cbranch_vccnz .LBB0_944
	s_andn2_b64 vcc, exec, s[0:1]
	s_cbranch_vccnz .LBB0_943
	s_barrier
	s_branch .LBB0_943

.LBB0_1118:
	s_xor_b64 s[34:35], s[34:35], -1
	v_mov_b32_e32 v68, v66
	v_mov_b32_e32 v69, v66
	s_add_u32 s19, s8, 0x100
	v_mov_b32_e32 v67, v66
	v_mov_b32_e32 v134, 0
	v_mov_b64_e32 v[84:85], v[68:69]
	v_mov_b64_e32 v[80:81], v[68:69]
	v_mov_b64_e32 v[92:93], v[68:69]
	v_mov_b64_e32 v[100:101], v[68:69]
	v_mov_b64_e32 v[116:117], v[68:69]
	v_mov_b64_e32 v[112:113], v[68:69]
	v_mov_b64_e32 v[128:129], v[68:69]
	v_mov_b64_e32 v[132:133], v[68:69]
	v_mov_b64_e32 v[124:125], v[68:69]
	v_mov_b64_e32 v[120:121], v[68:69]
	v_mov_b64_e32 v[104:105], v[68:69]
	v_mov_b64_e32 v[108:109], v[68:69]
	v_mov_b64_e32 v[96:97], v[68:69]
	v_mov_b64_e32 v[88:89], v[68:69]
	v_mov_b64_e32 v[72:73], v[68:69]
	v_mov_b64_e32 v[76:77], v[68:69]
	s_addc_u32 s21, s9, 0
	s_mov_b32 s63, -2
	v_cndmask_b32_e64 v242, 0, 1, s[34:35]
	v_mov_b64_e32 v[82:83], v[66:67]
	v_mov_b64_e32 v[78:79], v[66:67]
	v_mov_b64_e32 v[90:91], v[66:67]
	v_mov_b64_e32 v[98:99], v[66:67]
	v_mov_b64_e32 v[114:115], v[66:67]
	v_mov_b64_e32 v[110:111], v[66:67]
	v_mov_b64_e32 v[126:127], v[66:67]
	v_mov_b64_e32 v[130:131], v[66:67]
	v_mov_b64_e32 v[122:123], v[66:67]
	v_mov_b64_e32 v[118:119], v[66:67]
	v_mov_b64_e32 v[102:103], v[66:67]
	v_mov_b64_e32 v[106:107], v[66:67]
	v_mov_b64_e32 v[94:95], v[66:67]
	v_mov_b64_e32 v[86:87], v[66:67]
	v_mov_b64_e32 v[70:71], v[66:67]
	v_mov_b64_e32 v[74:75], v[66:67]
	v_mov_b32_e32 v135, v134
	v_mov_b64_e32 v[136:137], 0
	v_mov_b64_e32 v[138:139], 0
	v_mov_b64_e32 v[140:141], 0
	v_mov_b64_e32 v[142:143], 0
	v_mov_b64_e32 v[144:145], 0
	v_mov_b64_e32 v[146:147], 0
	v_mov_b64_e32 v[148:149], 0
	v_mov_b64_e32 v[150:151], 0
	v_mov_b64_e32 v[152:153], 0
	v_mov_b64_e32 v[154:155], 0
	v_mov_b64_e32 v[156:157], 0
	v_mov_b64_e32 v[158:159], 0
	v_mov_b64_e32 v[160:161], 0
	v_mov_b64_e32 v[162:163], 0
	v_mov_b64_e32 v[164:165], 0
	v_mov_b64_e32 v[166:167], 0
	v_mov_b64_e32 v[168:169], 0
	v_mov_b64_e32 v[170:171], 0
	v_mov_b64_e32 v[172:173], 0
	v_mov_b64_e32 v[174:175], 0
	v_mov_b64_e32 v[176:177], 0
	v_mov_b64_e32 v[178:179], 0
	v_mov_b64_e32 v[180:181], 0
	v_mov_b64_e32 v[182:183], 0
	v_mov_b64_e32 v[184:185], 0
	v_mov_b64_e32 v[186:187], 0
	v_mov_b64_e32 v[188:189], 0
	v_mov_b64_e32 v[190:191], 0
	v_mov_b64_e32 v[192:193], 0
	v_mov_b64_e32 v[194:195], 0
	v_mov_b64_e32 v[196:197], 0
	s_branch .LBB0_1120

.LBB0_1132:
	s_lshl_b32 s8, s59, 11
	s_and_b32 s8, s8, 0x800
	s_add_i32 s8, s8, 0
	s_add_i32 s9, s62, 0x25100
	s_add_i32 s8, s8, 0x25500
	v_mov_b32_e32 v2, s9
	s_lshl_b32 s9, s50, 2
	s_nop 11
	s_add_i32 s9, s8, s9
	v_lshl_add_u32 v4, v226, 2, s8
	v_lshl_add_u32 v3, v227, 2, s9
	ds_read_b32 v23, v2
	ds_read_b128 v[10:13], v3
	v_mov_b32_e32 v2, s61
	v_add_u32_e32 v22, 0x400, v4
	ds_read2_b32 v[18:19], v22 offset1:16
	ds_read_b128 v[6:9], v3 offset:528
	ds_read_b32 v25, v2
	ds_read_b128 v[14:17], v3 offset:16
	ds_read_b128 v[2:5], v3 offset:512
	v_add_u32_e32 v20, s60, v226
	s_waitcnt lgkmcnt(0)
	v_mul_f32_e32 v18, 0x41800000, v18
	v_cmp_lt_i32_e32 vcc, v20, v25
	ds_read2_b32 v[20:21], v22 offset0:32 offset1:48
	v_mul_f32_e32 v19, 0x41800000, v19
	v_cndmask_b32_e32 v32, 0, v18, vcc
	v_add_u32_e32 v18, s60, v229
	v_cmp_lt_i32_e32 vcc, v18, v25
	v_add_u32_e32 v18, s60, v230
	v_pk_fma_f32 v[30:31], v[196:197], s[16:17], v[12:13] op_sel_hi:[1,0,1]
	v_cndmask_b32_e32 v38, 0, v19, vcc
	s_waitcnt lgkmcnt(0)
	v_mul_f32_e32 v19, 0x41800000, v20
	v_cmp_lt_i32_e32 vcc, v18, v25
	v_pk_mul_f32 v[36:37], v[30:31], v[32:33] op_sel_hi:[1,0]
	v_pk_fma_f32 v[30:31], v[190:191], s[16:17], v[14:15] op_sel_hi:[1,0,1]
	v_cndmask_b32_e32 v40, 0, v19, vcc
	ds_read2_b32 v[18:19], v22 offset0:128 offset1:144
	v_pk_mul_f32 v[42:43], v[30:31], v[32:33] op_sel_hi:[1,0]
	v_mov_b32_e32 v31, 0
	v_add_u32_e32 v20, s60, v231
	v_pk_fma_f32 v[34:35], v[194:195], s[16:17], v[10:11] op_sel_hi:[1,0,1]
	v_cvt_pk_fp8_f32 v31, v42, v43
	v_mul_f32_e32 v21, 0x41800000, v21
	v_cmp_lt_i32_e32 vcc, v20, v25
	v_add_u32_e32 v20, s60, v232
	v_pk_mul_f32 v[34:35], v[34:35], v[32:33] op_sel_hi:[1,0]
	v_mov_b32_e32 v30, 0
	v_cndmask_b32_e32 v28, 0, v21, vcc
	v_cmp_lt_i32_e32 vcc, v20, v25
	ds_read2_b32 v[20:21], v22 offset0:160 offset1:176
	v_cvt_pk_fp8_f32 v30, v34, v35
	v_pk_fma_f32 v[34:35], v[192:193], s[16:17], v[16:17] op_sel_hi:[1,0,1]
	s_waitcnt lgkmcnt(0)
	v_mul_f32_e32 v18, 0x41800000, v18
	v_pk_mul_f32 v[34:35], v[34:35], v[32:33] op_sel_hi:[1,0]
	v_cndmask_b32_e32 v26, 0, v18, vcc
	v_cvt_pk_fp8_f32 v31, v34, v35 op_sel:[0,0,1]
	v_pk_fma_f32 v[34:35], v[188:189], s[16:17], v[4:5] op_sel_hi:[1,0,1]
	v_add_u32_e32 v18, s60, v233
	v_pk_mul_f32 v[42:43], v[34:35], v[32:33] op_sel_hi:[1,0]
	v_pk_fma_f32 v[34:35], v[178:179], s[16:17], v[6:7] op_sel_hi:[1,0,1]
	v_mul_f32_e32 v19, 0x41800000, v19
	v_cmp_lt_i32_e32 vcc, v18, v25
	v_add_u32_e32 v18, s60, v234
	v_pk_mul_f32 v[44:45], v[34:35], v[32:33] op_sel_hi:[1,0]
	v_mov_b32_e32 v35, 0
	v_cndmask_b32_e32 v24, 0, v19, vcc
	v_mul_f32_e32 v19, 0x41800000, v20
	v_cmp_lt_i32_e32 vcc, v18, v25
	v_add_u32_e32 v18, s60, v235
	v_cvt_pk_fp8_f32 v30, v36, v37 op_sel:[0,0,1]
	v_pk_fma_f32 v[36:37], v[186:187], s[16:17], v[2:3] op_sel_hi:[1,0,1]
	v_cvt_pk_fp8_f32 v35, v44, v45
	v_cndmask_b32_e32 v22, 0, v19, vcc
	v_mul_f32_e32 v19, 0x41800000, v21
	v_cmp_lt_i32_e32 vcc, v18, v25
	v_pk_mul_f32 v[36:37], v[36:37], v[32:33] op_sel_hi:[1,0]
	v_mov_b32_e32 v34, 0
	v_cndmask_b32_e32 v18, 0, v19, vcc
	v_add_u32_e32 v19, s58, v23
	v_cvt_pk_fp8_f32 v34, v36, v37
	v_pk_fma_f32 v[36:37], v[180:181], s[16:17], v[8:9] op_sel_hi:[1,0,1]
	v_lshl_add_u32 v19, v19, 8, v226
	v_pk_mul_f32 v[32:33], v[36:37], v[32:33] op_sel_hi:[1,0]
	v_pk_fma_f32 v[46:47], v[174:175], s[16:17], v[10:11] op_sel_hi:[1,0,1]
	v_cvt_pk_fp8_f32 v35, v32, v33 op_sel:[0,0,1]
	v_or_b32_e32 v32, v19, v236
	v_ashrrev_i32_e32 v33, 31, v32
	v_lshlrev_b64 v[36:37], 11, v[32:33]
	v_pk_fma_f32 v[32:33], v[182:183], s[16:17], v[14:15] op_sel_hi:[1,0,1]
	v_pk_mul_f32 v[46:47], v[46:47], v[38:39] op_sel_hi:[1,0]
	v_pk_mul_f32 v[44:45], v[32:33], v[38:39] op_sel_hi:[1,0]
	v_mov_b32_e32 v33, 0
	v_mov_b32_e32 v32, 0
	v_cvt_pk_fp8_f32 v32, v46, v47
	v_cvt_pk_fp8_f32 v33, v44, v45
	v_cvt_pk_fp8_f32 v34, v42, v43 op_sel:[0,0,1]
	v_pk_fma_f32 v[42:43], v[184:185], s[16:17], v[16:17] op_sel_hi:[1,0,1]
	v_pk_fma_f32 v[44:45], v[176:177], s[16:17], v[12:13] op_sel_hi:[1,0,1]
	v_pk_mul_f32 v[42:43], v[42:43], v[38:39] op_sel_hi:[1,0]
	v_pk_mul_f32 v[44:45], v[44:45], v[38:39] op_sel_hi:[1,0]
	v_cvt_pk_fp8_f32 v33, v42, v43 op_sel:[0,0,1]
	v_cvt_pk_fp8_f32 v32, v44, v45 op_sel:[0,0,1]
	v_lshl_or_b32 v20, s26, 8, v238
	v_ashrrev_i32_e32 v21, 31, v20
	v_lshl_add_u64 v[36:37], s[4:5], 0, v[36:37]
	v_lshl_add_u64 v[36:37], v[36:37], 0, v[20:21]
	v_permlane16_swap_b32_e32 v30, v32
	v_permlane16_swap_b32_e32 v31, v33
	v_lshl_add_u64 v[42:43], v[36:37], 0, v[214:215]
	global_store_dwordx4 v[42:43], v[30:33], off
	v_pk_fma_f32 v[44:45], v[162:163], s[16:17], v[2:3] op_sel_hi:[1,0,1]
	v_mov_b32_e32 v37, 0
	v_pk_fma_f32 v[32:33], v[170:171], s[16:17], v[6:7] op_sel_hi:[1,0,1]
	v_pk_mul_f32 v[44:45], v[44:45], v[38:39] op_sel_hi:[1,0]
	v_pk_mul_f32 v[32:33], v[32:33], v[38:39] op_sel_hi:[1,0]
	v_mov_b32_e32 v36, 0
	v_cvt_pk_fp8_f32 v36, v44, v45
	v_cvt_pk_fp8_f32 v37, v32, v33
	v_pk_fma_f32 v[30:31], v[172:173], s[16:17], v[8:9] op_sel_hi:[1,0,1]
	v_pk_fma_f32 v[32:33], v[164:165], s[16:17], v[4:5] op_sel_hi:[1,0,1]
	v_pk_mul_f32 v[30:31], v[30:31], v[38:39] op_sel_hi:[1,0]
	v_pk_mul_f32 v[32:33], v[32:33], v[38:39] op_sel_hi:[1,0]
	v_cvt_pk_fp8_f32 v37, v30, v31 op_sel:[0,0,1]
	v_cvt_pk_fp8_f32 v36, v32, v33 op_sel:[0,0,1]
	v_pk_fma_f32 v[30:31], v[168:169], s[16:17], v[12:13] op_sel_hi:[1,0,1]
	v_pk_fma_f32 v[32:33], v[166:167], s[16:17], v[10:11] op_sel_hi:[1,0,1]
	v_permlane16_swap_b32_e32 v35, v37
	v_permlane16_swap_b32_e32 v34, v36
	global_store_dwordx4 v[42:43], v[34:37], off offset:128
	v_pk_mul_f32 v[32:33], v[32:33], v[40:41] op_sel_hi:[1,0]
	v_pk_fma_f32 v[42:43], v[142:143], s[16:17], v[10:11] op_sel_hi:[1,0,1]
	v_pk_mul_f32 v[34:35], v[30:31], v[40:41] op_sel_hi:[1,0]
	v_pk_fma_f32 v[30:31], v[158:159], s[16:17], v[14:15] op_sel_hi:[1,0,1]
	v_pk_mul_f32 v[42:43], v[42:43], v[28:29] op_sel_hi:[1,0]
	v_pk_mul_f32 v[36:37], v[30:31], v[40:41] op_sel_hi:[1,0]
	v_mov_b32_e32 v30, 0
	v_cvt_pk_fp8_f32 v30, v32, v33
	v_mov_b32_e32 v31, 0
	v_cvt_pk_fp8_f32 v31, v36, v37
	v_pk_fma_f32 v[32:33], v[160:161], s[16:17], v[16:17] op_sel_hi:[1,0,1]
	v_cvt_pk_fp8_f32 v30, v34, v35 op_sel:[0,0,1]
	v_pk_fma_f32 v[34:35], v[154:155], s[16:17], v[2:3] op_sel_hi:[1,0,1]
	v_pk_mul_f32 v[32:33], v[32:33], v[40:41] op_sel_hi:[1,0]
	v_pk_mul_f32 v[36:37], v[34:35], v[40:41] op_sel_hi:[1,0]
	v_pk_fma_f32 v[34:35], v[146:147], s[16:17], v[6:7] op_sel_hi:[1,0,1]
	v_cvt_pk_fp8_f32 v31, v32, v33 op_sel:[0,0,1]
	v_pk_mul_f32 v[38:39], v[34:35], v[40:41] op_sel_hi:[1,0]
	v_mov_b32_e32 v34, 0
	v_cvt_pk_fp8_f32 v34, v36, v37
	v_mov_b32_e32 v35, 0
	v_pk_fma_f32 v[32:33], v[156:157], s[16:17], v[4:5] op_sel_hi:[1,0,1]
	v_cvt_pk_fp8_f32 v35, v38, v39
	v_pk_mul_f32 v[32:33], v[32:33], v[40:41] op_sel_hi:[1,0]
	v_pk_fma_f32 v[36:37], v[148:149], s[16:17], v[8:9] op_sel_hi:[1,0,1]
	v_cvt_pk_fp8_f32 v34, v32, v33 op_sel:[0,0,1]
	v_or_b32_e32 v32, v19, v237
	v_pk_mul_f32 v[36:37], v[36:37], v[40:41] op_sel_hi:[1,0]
	v_ashrrev_i32_e32 v33, 31, v32
	v_cvt_pk_fp8_f32 v35, v36, v37 op_sel:[0,0,1]
	v_lshlrev_b64 v[36:37], 11, v[32:33]
	v_pk_fma_f32 v[32:33], v[150:151], s[16:17], v[14:15] op_sel_hi:[1,0,1]
	v_pk_fma_f32 v[38:39], v[152:153], s[16:17], v[16:17] op_sel_hi:[1,0,1]
	v_pk_mul_f32 v[40:41], v[32:33], v[28:29] op_sel_hi:[1,0]
	v_mov_b32_e32 v33, 0
	v_mov_b32_e32 v32, 0
	v_cvt_pk_fp8_f32 v32, v42, v43
	v_cvt_pk_fp8_f32 v33, v40, v41
	v_pk_fma_f32 v[40:41], v[144:145], s[16:17], v[12:13] op_sel_hi:[1,0,1]
	v_pk_mul_f32 v[38:39], v[38:39], v[28:29] op_sel_hi:[1,0]
	v_pk_mul_f32 v[40:41], v[40:41], v[28:29] op_sel_hi:[1,0]
	v_cvt_pk_fp8_f32 v33, v38, v39 op_sel:[0,0,1]
	v_cvt_pk_fp8_f32 v32, v40, v41 op_sel:[0,0,1]
	v_lshl_add_u64 v[36:37], s[4:5], 0, v[36:37]
	v_lshl_add_u64 v[36:37], v[36:37], 0, v[20:21]
	v_permlane16_swap_b32_e32 v31, v33
	v_permlane16_swap_b32_e32 v30, v32
	v_lshl_add_u64 v[38:39], v[36:37], 0, v[214:215]
	global_store_dwordx4 v[38:39], v[30:33], off
	v_pk_fma_f32 v[40:41], v[138:139], s[16:17], v[2:3] op_sel_hi:[1,0,1]
	v_mov_b32_e32 v37, 0
	v_pk_fma_f32 v[32:33], v[134:135], s[16:17], v[6:7] op_sel_hi:[1,0,1]
	v_pk_mul_f32 v[40:41], v[40:41], v[28:29] op_sel_hi:[1,0]
	v_pk_mul_f32 v[32:33], v[32:33], v[28:29] op_sel_hi:[1,0]
	v_mov_b32_e32 v36, 0
	v_cvt_pk_fp8_f32 v36, v40, v41
	v_cvt_pk_fp8_f32 v37, v32, v33
	v_pk_fma_f32 v[30:31], v[136:137], s[16:17], v[8:9] op_sel_hi:[1,0,1]
	v_pk_fma_f32 v[32:33], v[140:141], s[16:17], v[4:5] op_sel_hi:[1,0,1]
	v_add_u32_e32 v19, 0x80, v19
	v_pk_mul_f32 v[32:33], v[32:33], v[28:29] op_sel_hi:[1,0]
	v_pk_mul_f32 v[28:29], v[30:31], v[28:29] op_sel_hi:[1,0]
	v_cvt_pk_fp8_f32 v36, v32, v33 op_sel:[0,0,1]
	v_cvt_pk_fp8_f32 v37, v28, v29 op_sel:[0,0,1]
	v_pk_fma_f32 v[28:29], v[132:133], s[16:17], v[12:13] op_sel_hi:[1,0,1]
	v_pk_fma_f32 v[30:31], v[130:131], s[16:17], v[10:11] op_sel_hi:[1,0,1]
	v_permlane16_swap_b32_e32 v34, v36
	v_permlane16_swap_b32_e32 v35, v37
	v_pk_mul_f32 v[32:33], v[28:29], v[26:27] op_sel_hi:[1,0]
	v_pk_fma_f32 v[28:29], v[126:127], s[16:17], v[14:15] op_sel_hi:[1,0,1]
	global_store_dwordx4 v[38:39], v[34:37], off offset:128
	v_pk_mul_f32 v[30:31], v[30:31], v[26:27] op_sel_hi:[1,0]
	v_pk_fma_f32 v[38:39], v[110:111], s[16:17], v[10:11] op_sel_hi:[1,0,1]
	v_pk_mul_f32 v[34:35], v[28:29], v[26:27] op_sel_hi:[1,0]
	v_mov_b32_e32 v28, 0
	v_cvt_pk_fp8_f32 v28, v30, v31
	v_mov_b32_e32 v29, 0
	v_cvt_pk_fp8_f32 v29, v34, v35
	v_pk_fma_f32 v[30:31], v[128:129], s[16:17], v[16:17] op_sel_hi:[1,0,1]
	v_cvt_pk_fp8_f32 v28, v32, v33 op_sel:[0,0,1]
	v_pk_fma_f32 v[32:33], v[122:123], s[16:17], v[2:3] op_sel_hi:[1,0,1]
	v_pk_mul_f32 v[30:31], v[30:31], v[26:27] op_sel_hi:[1,0]
	v_pk_mul_f32 v[34:35], v[32:33], v[26:27] op_sel_hi:[1,0]
	v_pk_fma_f32 v[32:33], v[118:119], s[16:17], v[6:7] op_sel_hi:[1,0,1]
	v_cvt_pk_fp8_f32 v29, v30, v31 op_sel:[0,0,1]
	v_pk_mul_f32 v[36:37], v[32:33], v[26:27] op_sel_hi:[1,0]
	v_mov_b32_e32 v32, 0
	v_cvt_pk_fp8_f32 v32, v34, v35
	v_pk_fma_f32 v[30:31], v[124:125], s[16:17], v[4:5] op_sel_hi:[1,0,1]
	v_mov_b32_e32 v33, 0
	v_pk_mul_f32 v[30:31], v[30:31], v[26:27] op_sel_hi:[1,0]
	v_cvt_pk_fp8_f32 v33, v36, v37
	v_cvt_pk_fp8_f32 v32, v30, v31 op_sel:[0,0,1]
	v_pk_fma_f32 v[30:31], v[114:115], s[16:17], v[14:15] op_sel_hi:[1,0,1]
	v_pk_mul_f32 v[38:39], v[38:39], v[24:25] op_sel_hi:[1,0]
	v_pk_mul_f32 v[36:37], v[30:31], v[24:25] op_sel_hi:[1,0]
	v_mov_b32_e32 v31, 0
	v_mov_b32_e32 v30, 0
	v_cvt_pk_fp8_f32 v30, v38, v39
	v_cvt_pk_fp8_f32 v31, v36, v37
	v_pk_fma_f32 v[34:35], v[120:121], s[16:17], v[8:9] op_sel_hi:[1,0,1]
	v_pk_fma_f32 v[36:37], v[112:113], s[16:17], v[12:13] op_sel_hi:[1,0,1]
	v_pk_mul_f32 v[26:27], v[34:35], v[26:27] op_sel_hi:[1,0]
	v_pk_fma_f32 v[34:35], v[116:117], s[16:17], v[16:17] op_sel_hi:[1,0,1]
	v_cvt_pk_fp8_f32 v33, v26, v27 op_sel:[0,0,1]
	v_or_b32_e32 v26, v19, v236
	v_pk_mul_f32 v[36:37], v[36:37], v[24:25] op_sel_hi:[1,0]
	v_pk_mul_f32 v[34:35], v[34:35], v[24:25] op_sel_hi:[1,0]
	v_ashrrev_i32_e32 v27, 31, v26
	v_cvt_pk_fp8_f32 v30, v36, v37 op_sel:[0,0,1]
	v_cvt_pk_fp8_f32 v31, v34, v35 op_sel:[0,0,1]
	v_lshlrev_b64 v[26:27], 11, v[26:27]
	v_lshl_add_u64 v[26:27], s[4:5], 0, v[26:27]
	v_lshl_add_u64 v[26:27], v[26:27], 0, v[20:21]
	v_permlane16_swap_b32_e32 v28, v30
	v_permlane16_swap_b32_e32 v29, v31
	v_lshl_add_u64 v[26:27], v[26:27], 0, v[214:215]
	global_store_dwordx4 v[26:27], v[28:31], off
	v_pk_fma_f32 v[36:37], v[102:103], s[16:17], v[2:3] op_sel_hi:[1,0,1]
	v_mov_b32_e32 v35, 0
	v_pk_fma_f32 v[30:31], v[106:107], s[16:17], v[6:7] op_sel_hi:[1,0,1]
	v_pk_mul_f32 v[36:37], v[36:37], v[24:25] op_sel_hi:[1,0]
	v_pk_mul_f32 v[30:31], v[30:31], v[24:25] op_sel_hi:[1,0]
	v_mov_b32_e32 v34, 0
	v_cvt_pk_fp8_f32 v34, v36, v37
	v_cvt_pk_fp8_f32 v35, v30, v31
	v_pk_fma_f32 v[28:29], v[108:109], s[16:17], v[8:9] op_sel_hi:[1,0,1]
	v_pk_fma_f32 v[30:31], v[104:105], s[16:17], v[4:5] op_sel_hi:[1,0,1]
	s_and_b64 vcc, exec, s[6:7]
	v_pk_mul_f32 v[30:31], v[30:31], v[24:25] op_sel_hi:[1,0]
	v_pk_mul_f32 v[24:25], v[28:29], v[24:25] op_sel_hi:[1,0]
	v_cvt_pk_fp8_f32 v34, v30, v31 op_sel:[0,0,1]
	v_cvt_pk_fp8_f32 v35, v24, v25 op_sel:[0,0,1]
	v_pk_fma_f32 v[24:25], v[100:101], s[16:17], v[12:13] op_sel_hi:[1,0,1]
	s_mov_b64 s[6:7], -1
	v_permlane16_swap_b32_e32 v32, v34
	v_permlane16_swap_b32_e32 v33, v35
	global_store_dwordx4 v[26:27], v[32:35], off offset:128
	v_pk_fma_f32 v[26:27], v[98:99], s[16:17], v[10:11] op_sel_hi:[1,0,1]
	v_pk_mul_f32 v[28:29], v[24:25], v[22:23] op_sel_hi:[1,0]
	v_pk_fma_f32 v[24:25], v[90:91], s[16:17], v[14:15] op_sel_hi:[1,0,1]
	v_pk_mul_f32 v[26:27], v[26:27], v[22:23] op_sel_hi:[1,0]
	v_pk_mul_f32 v[30:31], v[24:25], v[22:23] op_sel_hi:[1,0]
	v_mov_b32_e32 v24, 0
	v_cvt_pk_fp8_f32 v24, v26, v27
	v_mov_b32_e32 v25, 0
	v_cvt_pk_fp8_f32 v25, v30, v31
	v_pk_fma_f32 v[26:27], v[92:93], s[16:17], v[16:17] op_sel_hi:[1,0,1]
	v_cvt_pk_fp8_f32 v24, v28, v29 op_sel:[0,0,1]
	v_pk_fma_f32 v[28:29], v[94:95], s[16:17], v[2:3] op_sel_hi:[1,0,1]
	v_pk_mul_f32 v[26:27], v[26:27], v[22:23] op_sel_hi:[1,0]
	v_pk_mul_f32 v[30:31], v[28:29], v[22:23] op_sel_hi:[1,0]
	v_pk_fma_f32 v[28:29], v[86:87], s[16:17], v[6:7] op_sel_hi:[1,0,1]
	v_cvt_pk_fp8_f32 v25, v26, v27 op_sel:[0,0,1]
	v_pk_mul_f32 v[32:33], v[28:29], v[22:23] op_sel_hi:[1,0]
	v_mov_b32_e32 v28, 0
	v_cvt_pk_fp8_f32 v28, v30, v31
	v_pk_fma_f32 v[26:27], v[96:97], s[16:17], v[4:5] op_sel_hi:[1,0,1]
	v_pk_fma_f32 v[30:31], v[88:89], s[16:17], v[8:9] op_sel_hi:[1,0,1]
	v_pk_mul_f32 v[26:27], v[26:27], v[22:23] op_sel_hi:[1,0]
	v_pk_fma_f32 v[10:11], v[78:79], s[16:17], v[10:11] op_sel_hi:[1,0,1]
	v_pk_fma_f32 v[2:3], v[70:71], s[16:17], v[2:3] op_sel_hi:[1,0,1]
	v_mov_b32_e32 v29, 0
	v_pk_mul_f32 v[22:23], v[30:31], v[22:23] op_sel_hi:[1,0]
	v_cvt_pk_fp8_f32 v28, v26, v27 op_sel:[0,0,1]
	v_pk_fma_f32 v[14:15], v[82:83], s[16:17], v[14:15] op_sel_hi:[1,0,1]
	v_pk_mul_f32 v[10:11], v[10:11], v[18:19] op_sel_hi:[1,0]
	v_mov_b32_e32 v26, 0
	v_pk_fma_f32 v[6:7], v[74:75], s[16:17], v[6:7] op_sel_hi:[1,0,1]
	v_pk_mul_f32 v[2:3], v[2:3], v[18:19] op_sel_hi:[1,0]
	v_mov_b32_e32 v30, 0
	v_cvt_pk_fp8_f32 v29, v32, v33
	v_pk_mul_f32 v[14:15], v[14:15], v[18:19] op_sel_hi:[1,0]
	v_mov_b32_e32 v27, 0
	v_cvt_pk_fp8_f32 v26, v10, v11
	v_pk_mul_f32 v[6:7], v[6:7], v[18:19] op_sel_hi:[1,0]
	v_mov_b32_e32 v31, 0
	v_cvt_pk_fp8_f32 v30, v2, v3
	v_cvt_pk_fp8_f32 v27, v14, v15
	v_cvt_pk_fp8_f32 v31, v6, v7
	v_pk_fma_f32 v[10:11], v[80:81], s[16:17], v[12:13] op_sel_hi:[1,0,1]
	v_pk_fma_f32 v[2:3], v[72:73], s[16:17], v[4:5] op_sel_hi:[1,0,1]
	v_pk_fma_f32 v[16:17], v[84:85], s[16:17], v[16:17] op_sel_hi:[1,0,1]
	v_pk_mul_f32 v[10:11], v[10:11], v[18:19] op_sel_hi:[1,0]
	v_pk_fma_f32 v[8:9], v[76:77], s[16:17], v[8:9] op_sel_hi:[1,0,1]
	v_pk_mul_f32 v[2:3], v[2:3], v[18:19] op_sel_hi:[1,0]
	v_cvt_pk_fp8_f32 v29, v22, v23 op_sel:[0,0,1]
	v_or_b32_e32 v22, v19, v237
	v_cvt_pk_fp8_f32 v26, v10, v11 op_sel:[0,0,1]
	v_pk_mul_f32 v[10:11], v[16:17], v[18:19] op_sel_hi:[1,0]
	v_cvt_pk_fp8_f32 v30, v2, v3 op_sel:[0,0,1]
	v_pk_mul_f32 v[2:3], v[8:9], v[18:19] op_sel_hi:[1,0]
	v_ashrrev_i32_e32 v23, 31, v22
	v_cvt_pk_fp8_f32 v27, v10, v11 op_sel:[0,0,1]
	v_cvt_pk_fp8_f32 v31, v2, v3 op_sel:[0,0,1]
	v_lshlrev_b64 v[22:23], 11, v[22:23]
	v_lshl_add_u64 v[10:11], s[4:5], 0, v[22:23]
	v_lshl_add_u64 v[10:11], v[10:11], 0, v[20:21]
	v_permlane16_swap_b32_e32 v24, v26
	v_permlane16_swap_b32_e32 v25, v27
	v_lshl_add_u64 v[10:11], v[10:11], 0, v[214:215]
	v_permlane16_swap_b32_e32 v28, v30
	v_permlane16_swap_b32_e32 v29, v31
	global_store_dwordx4 v[10:11], v[24:27], off
	global_store_dwordx4 v[10:11], v[28:31], off offset:128
	s_cbranch_vccnz .LBB0_1109
	s_andn2_b64 vcc, exec, s[0:1]
	s_cbranch_vccnz .LBB0_1108
	s_barrier
	s_branch .LBB0_1108
